# v3 + accumulator register window rotated by 2 VGPRs (bank placement) in P6 P7 P10 P13 P15
# baseline (speedup 1.0000x reference)
.LBB0_584:
	s_waitcnt lgkmcnt(0)
	v_ashrrev_i32_e32 v1, 31, v8
	v_lshrrev_b32_e32 v1, 26, v1
	v_add_u32_e32 v1, v8, v1
	v_ashrrev_i32_e32 v10, 6, v1
	v_bfe_i32 v1, v8, 27, 1
	v_lshlrev_b32_e32 v0, 4, v8
	v_lshrrev_b32_e32 v1, 22, v1
	v_add_u32_e32 v1, v0, v1
	v_and_b32_e32 v1, 0xfffffc00, v1
	v_sub_u32_e32 v1, v0, v1
	v_lshrrev_b32_e32 v2, 4, v1
	s_add_u32 s43, s54, 0x36200000
	v_bitop3_b32 v2, v2, v1, 32 bitop3:0x6c
	v_ashrrev_i32_e32 v1, 31, v1
	s_addc_u32 s46, s55, 0
	v_lshrrev_b32_e32 v1, 26, v1
	s_add_u32 s47, s54, 0x2200000
	v_add_u32_e32 v1, v2, v1
	s_addc_u32 s48, s55, 0
	s_ashr_i32 s29, s28, 31
	v_ashrrev_i32_e32 v11, 6, v1
	s_lshl_b64 s[10:11], s[28:29], 18
	v_lshlrev_b32_e32 v3, 3, v10
	v_mul_i32_i24_e32 v4, 64, v11
	s_add_u32 s34, s43, s10
	s_sext_i32_i16 s30, s8
	v_and_b32_e32 v3, -16, v3
	v_sub_u32_e32 v2, v2, v4
	v_mov_b32_e32 v4, 1
	s_addc_u32 s35, s46, s11
	s_ashr_i32 s31, s30, 31
	v_add_u32_e32 v1, v11, v3
	v_lshlrev_b32_e32 v3, 5, v10
	v_ashrrev_i16_sdwa v2, v4, sext(v2) dst_sel:DWORD dst_unused:UNUSED_PAD src0_sel:DWORD src1_sel:BYTE_0
	s_lshl_b64 s[8:9], s[30:31], 18
	v_and_b32_e32 v3, 32, v3
	v_bfe_i32 v12, v2, 0, 16
	s_add_u32 s38, s47, s8
	v_and_b32_e32 v6, 3, v11
	s_mov_b32 s8, 0x3fffe0
	v_add_lshl_u32 v3, v3, v12, 1
	v_add_u32_e32 v0, 0x2000, v0
	v_lshlrev_b32_e32 v2, 1, v1
	v_lshrrev_b32_e32 v5, 2, v1
	v_and_or_b32 v6, v1, s8, v6
	v_lshl_add_u32 v32, v1, 10, v3
	v_ashrrev_i32_e32 v1, 31, v0
	v_lshrrev_b32_e32 v1, 22, v1
	v_add_u32_e32 v1, v0, v1
	v_ashrrev_i32_e32 v13, 10, v1
	v_mul_i32_i24_e32 v1, 0x400, v13
	v_sub_u32_e32 v0, v0, v1
	v_and_b32_e32 v2, 24, v2
	v_and_b32_e32 v5, 4, v5
	v_lshrrev_b32_e32 v1, 4, v0
	v_or3_b32 v2, v6, v5, v2
	v_bitop3_b32 v0, v1, v0, 32 bitop3:0x6c
	v_lshl_add_u32 v162, v2, 10, v3
	v_ashrrev_i32_e32 v2, 31, v0
	v_lshrrev_b32_e32 v2, 26, v2
	v_add_u32_e32 v2, v0, v2
	v_lshlrev_b32_e32 v1, 3, v13
	v_ashrrev_i32_e32 v14, 6, v2
	v_and_b32_e32 v2, 0xc0, v2
	v_and_b32_e32 v1, -16, v1
	v_sub_u32_e32 v0, v0, v2
	s_addc_u32 s39, s48, s9
	v_add_u32_e32 v1, v14, v1
	v_ashrrev_i16_sdwa v0, v4, sext(v0) dst_sel:DWORD dst_unused:UNUSED_PAD src0_sel:DWORD src1_sel:BYTE_0
	s_lshl_b32 s29, s3, 10
	v_lshlrev_b32_e32 v3, 5, v13
	v_bfe_i32 v15, v0, 0, 16
	v_lshlrev_b32_e32 v0, 1, v1
	v_lshrrev_b32_e32 v2, 2, v1
	v_and_b32_e32 v4, 3, v14
	s_add_i32 s31, s29, 0
	v_and_b32_e32 v3, 32, v3
	v_and_b32_e32 v0, 24, v0
	v_and_b32_e32 v2, 4, v2
	v_and_or_b32 v4, v1, s8, v4
	s_add_i32 m0, s31, 0x10000
	s_ashr_i32 s14, s2, 8
	v_or3_b32 v0, v4, v2, v0
	v_add_lshl_u32 v2, v3, v15, 1
	global_load_lds_dwordx4 v162, s[38:39]
	s_add_i32 m0, s31, 0x12000
	v_lshl_add_u32 v166, v0, 10, v2
	s_add_u32 s8, s38, 0x20000
	global_load_lds_dwordx4 v166, s[38:39]
	s_addc_u32 s9, s39, 0
	s_add_i32 m0, s31, 0x14000
	s_add_i32 s49, s31, 0x2000
	global_load_lds_dwordx4 v162, s[8:9]
	s_add_i32 m0, s31, 0x16000
	v_lshl_add_u32 v164, v1, 10, v2
	global_load_lds_dwordx4 v166, s[8:9]
	s_mov_b32 m0, s31
	s_add_u32 s8, s34, 0x20000
	global_load_lds_dwordx4 v32, s[34:35]
	s_mov_b32 m0, s49
	s_addc_u32 s9, s35, 0
	s_add_i32 s50, s31, 0x4000
	global_load_lds_dwordx4 v164, s[34:35]
	s_mov_b32 m0, s50
	s_add_i32 s51, s31, 0x6000
	global_load_lds_dwordx4 v32, s[8:9]
	s_mov_b32 m0, s51
	v_mov_b32_e32 v163, 0
	global_load_lds_dwordx4 v164, s[8:9]
	v_mov_b32_e32 v167, v163
	v_mov_b32_e32 v33, v163
	v_mov_b32_e32 v165, v163
	s_cmp_eq_u32 s14, 1
	s_mov_b32 s66, 0
	v_lshl_add_u64 v[6:7], s[38:39], 0, v[162:163]
	v_lshl_add_u64 v[4:5], s[38:39], 0, v[166:167]
	v_lshl_add_u64 v[0:1], s[34:35], 0, v[32:33]
	s_cselect_b64 s[8:9], -1, 0
	s_cmp_lg_u32 s14, 1
	v_lshl_add_u64 v[2:3], s[34:35], 0, v[164:165]
	s_cbranch_scc1 .LBB0_586
	s_barrier

.LBB0_593:
	s_ashr_i32 s17, s16, 31
	s_lshl_b64 s[22:23], s[16:17], 18
	s_add_u32 s22, s43, s22
	s_addc_u32 s23, s46, s23
	s_ashr_i32 s15, s14, 31
	s_lshl_b64 s[26:27], s[14:15], 18
	s_add_u32 s26, s47, s26
	v_mov_b32_e32 v58, 0
	s_addc_u32 s27, s48, s27
	v_lshl_add_u64 v[178:179], s[34:35], 0, v[170:171]
	v_lshl_add_u64 v[180:181], s[34:35], 0, v[172:173]
	s_mov_b32 s15, 0
	v_mov_b32_e32 v59, v58
	v_mov_b32_e32 v60, v58
	v_mov_b32_e32 v61, v58
	v_mov_b32_e32 v70, v58
	v_mov_b32_e32 v71, v58
	v_mov_b32_e32 v72, v58
	v_mov_b32_e32 v73, v58
	v_mov_b32_e32 v82, v58
	v_mov_b32_e32 v83, v58
	v_mov_b32_e32 v84, v58
	v_mov_b32_e32 v85, v58
	v_mov_b32_e32 v90, v58
	v_mov_b32_e32 v91, v58
	v_mov_b32_e32 v92, v58
	v_mov_b32_e32 v93, v58
	v_mov_b32_e32 v34, v58
	v_mov_b32_e32 v35, v58
	v_mov_b32_e32 v36, v58
	v_mov_b32_e32 v37, v58
	v_mov_b32_e32 v38, v58
	v_mov_b32_e32 v39, v58
	v_mov_b32_e32 v40, v58
	v_mov_b32_e32 v41, v58
	v_mov_b32_e32 v46, v58
	v_mov_b32_e32 v47, v58
	v_mov_b32_e32 v48, v58
	v_mov_b32_e32 v49, v58
	v_mov_b32_e32 v54, v58
	v_mov_b32_e32 v55, v58
	v_mov_b32_e32 v56, v58
	v_mov_b32_e32 v57, v58
	v_mov_b32_e32 v66, v58
	v_mov_b32_e32 v67, v58
	v_mov_b32_e32 v68, v58
	v_mov_b32_e32 v69, v58
	v_mov_b32_e32 v78, v58
	v_mov_b32_e32 v79, v58
	v_mov_b32_e32 v80, v58
	v_mov_b32_e32 v81, v58
	v_mov_b32_e32 v86, v58
	v_mov_b32_e32 v87, v58
	v_mov_b32_e32 v88, v58
	v_mov_b32_e32 v89, v58
	v_mov_b32_e32 v94, v58
	v_mov_b32_e32 v95, v58
	v_mov_b32_e32 v96, v58
	v_mov_b32_e32 v97, v58
	v_mov_b32_e32 v98, v58
	v_mov_b32_e32 v99, v58
	v_mov_b32_e32 v100, v58
	v_mov_b32_e32 v101, v58
	v_mov_b32_e32 v106, v58
	v_mov_b32_e32 v107, v58
	v_mov_b32_e32 v108, v58
	v_mov_b32_e32 v109, v58
	v_mov_b32_e32 v114, v58
	v_mov_b32_e32 v115, v58
	v_mov_b32_e32 v116, v58
	v_mov_b32_e32 v117, v58
	v_mov_b32_e32 v122, v58
	v_mov_b32_e32 v123, v58
	v_mov_b32_e32 v124, v58
	v_mov_b32_e32 v125, v58
	v_mov_b32_e32 v130, v58
	v_mov_b32_e32 v131, v58
	v_mov_b32_e32 v132, v58
	v_mov_b32_e32 v133, v58
	v_mov_b32_e32 v138, v58
	v_mov_b32_e32 v139, v58
	v_mov_b32_e32 v140, v58
	v_mov_b32_e32 v141, v58
	v_mov_b32_e32 v146, v58
	v_mov_b32_e32 v147, v58
	v_mov_b32_e32 v148, v58
	v_mov_b32_e32 v149, v58
	v_mov_b32_e32 v154, v58
	v_mov_b32_e32 v155, v58
	v_mov_b32_e32 v156, v58
	v_mov_b32_e32 v157, v58
	v_mov_b32_e32 v102, v58
	v_mov_b32_e32 v103, v58
	v_mov_b32_e32 v104, v58
	v_mov_b32_e32 v105, v58
	v_mov_b32_e32 v110, v58
	v_mov_b32_e32 v111, v58
	v_mov_b32_e32 v112, v58
	v_mov_b32_e32 v113, v58
	v_mov_b32_e32 v118, v58
	v_mov_b32_e32 v119, v58
	v_mov_b32_e32 v120, v58
	v_mov_b32_e32 v121, v58
	v_mov_b32_e32 v126, v58
	v_mov_b32_e32 v127, v58
	v_mov_b32_e32 v128, v58
	v_mov_b32_e32 v129, v58
	v_mov_b32_e32 v134, v58
	v_mov_b32_e32 v135, v58
	v_mov_b32_e32 v136, v58
	v_mov_b32_e32 v137, v58
	v_mov_b32_e32 v142, v58
	v_mov_b32_e32 v143, v58
	v_mov_b32_e32 v144, v58
	v_mov_b32_e32 v145, v58
	v_mov_b32_e32 v150, v58
	v_mov_b32_e32 v151, v58
	v_mov_b32_e32 v152, v58
	v_mov_b32_e32 v153, v58
	v_mov_b32_e32 v158, v58
	v_mov_b32_e32 v159, v58
	v_mov_b32_e32 v160, v58
	v_mov_b32_e32 v161, v58
	v_mov_b32_e32 v74, v58
	v_mov_b32_e32 v75, v58
	v_mov_b32_e32 v76, v58
	v_mov_b32_e32 v77, v58
	v_mov_b32_e32 v62, v58
	v_mov_b32_e32 v63, v58
	v_mov_b32_e32 v64, v58
	v_mov_b32_e32 v65, v58
	v_mov_b32_e32 v50, v58
	v_mov_b32_e32 v51, v58
	v_mov_b32_e32 v52, v58
	v_mov_b32_e32 v53, v58
	v_mov_b32_e32 v42, v58
	v_mov_b32_e32 v43, v58
	v_mov_b32_e32 v44, v58
	v_mov_b32_e32 v45, v58
.LBB0_594:
	ds_read_b128 v[24:27], v186
	ds_read_b128 v[28:31], v186 offset:1024
	ds_read_b128 v[16:19], v186 offset:2048
	ds_read_b128 v[20:23], v186 offset:3072
	ds_read_b128 v[8:11], v187
	ds_read_b128 v[12:15], v187 offset:1024
	ds_read_b128 v[0:3], v187 offset:2048
	ds_read_b128 v[4:7], v187 offset:3072
	s_add_i32 m0, s31, 0xc000
	ds_read_b128 v[192:195], v188
	ds_read_b128 v[196:199], v188 offset:1024
	ds_read_b128 v[200:203], v188 offset:2048
	ds_read_b128 v[204:207], v188 offset:3072
	ds_read_b128 v[208:211], v188 offset:4096
	ds_read_b128 v[212:215], v188 offset:5120
	ds_read_b128 v[224:227], v188 offset:6144
	ds_read_b128 v[228:231], v188 offset:7168
	global_load_lds_dwordx4 v[178:179], off
	s_add_i32 m0, s31, 0xe000
	s_nop 0
	global_load_lds_dwordx4 v[180:181], off
	s_waitcnt vmcnt(8)
	s_waitcnt lgkmcnt(0)
	s_barrier
	s_setprio 1
	s_waitcnt lgkmcnt(0)
	v_mfma_scale_f32_16x16x128_f8f6f4 v[158:161], v[24:31], v[192:199], v[158:161], v189, v189 op_sel_hi:[0,0,0]
	v_mfma_scale_f32_16x16x128_f8f6f4 v[150:153], v[16:23], v[192:199], v[150:153], v189, v189 op_sel_hi:[0,0,0]
	v_mfma_scale_f32_16x16x128_f8f6f4 v[142:145], v[24:31], v[200:207], v[142:145], v189, v189 op_sel_hi:[0,0,0]
	v_mfma_scale_f32_16x16x128_f8f6f4 v[134:137], v[16:23], v[200:207], v[134:137], v189, v189 op_sel_hi:[0,0,0]
	v_mfma_scale_f32_16x16x128_f8f6f4 v[126:129], v[24:31], v[208:215], v[126:129], v189, v189 op_sel_hi:[0,0,0]
	v_mfma_scale_f32_16x16x128_f8f6f4 v[118:121], v[16:23], v[208:215], v[118:121], v189, v189 op_sel_hi:[0,0,0]
	v_mfma_scale_f32_16x16x128_f8f6f4 v[110:113], v[24:31], v[224:231], v[110:113], v189, v189 op_sel_hi:[0,0,0]
	v_mfma_scale_f32_16x16x128_f8f6f4 v[102:105], v[16:23], v[224:231], v[102:105], v189, v189 op_sel_hi:[0,0,0]
	s_setprio 0
	s_setprio 1
	v_mfma_scale_f32_16x16x128_f8f6f4 v[154:157], v[8:15], v[192:199], v[154:157], v189, v189 op_sel_hi:[0,0,0]
	v_mfma_scale_f32_16x16x128_f8f6f4 v[146:149], v[0:7], v[192:199], v[146:149], v189, v189 op_sel_hi:[0,0,0]
	v_mfma_scale_f32_16x16x128_f8f6f4 v[138:141], v[8:15], v[200:207], v[138:141], v189, v189 op_sel_hi:[0,0,0]
	v_mfma_scale_f32_16x16x128_f8f6f4 v[130:133], v[0:7], v[200:207], v[130:133], v189, v189 op_sel_hi:[0,0,0]
	v_mfma_scale_f32_16x16x128_f8f6f4 v[122:125], v[8:15], v[208:215], v[122:125], v189, v189 op_sel_hi:[0,0,0]
	v_mfma_scale_f32_16x16x128_f8f6f4 v[114:117], v[0:7], v[208:215], v[114:117], v189, v189 op_sel_hi:[0,0,0]
	v_mfma_scale_f32_16x16x128_f8f6f4 v[106:109], v[8:15], v[224:231], v[106:109], v189, v189 op_sel_hi:[0,0,0]
	v_mfma_scale_f32_16x16x128_f8f6f4 v[98:101], v[0:7], v[224:231], v[98:101], v189, v189 op_sel_hi:[0,0,0]
	s_setprio 0
	s_barrier
	s_cmp_gt_u32 s15, 5
	s_cselect_b64 s[36:37], -1, 0
	s_and_b64 s[40:41], s[36:37], exec
	v_sub_co_u32_e64 v216, s[40:41], s15, 6
	s_nop 0
	v_readfirstlane_b32 s73, v216
	s_cselect_b32 s17, s27, s39
	s_cselect_b32 s67, s26, s38
	s_add_i32 s76, s73, 8
	s_and_b64 s[74:75], s[36:37], exec
	s_cselect_b32 s74, s73, s76
	s_ashr_i32 s75, s74, 31
	s_lshl_b64 s[74:75], s[74:75], 7
	s_add_u32 s76, s67, s74
	s_addc_u32 s77, s17, s75
	s_add_i32 s17, s61, s29
	v_lshl_add_u64 v[216:217], s[76:77], 0, v[162:163]
	s_mov_b32 m0, s17
	ds_read_b128 v[192:195], v188 offset:16384
	ds_read_b128 v[196:199], v188 offset:17408
	ds_read_b128 v[200:203], v188 offset:18432
	ds_read_b128 v[204:207], v188 offset:19456
	ds_read_b128 v[208:211], v188 offset:20480
	ds_read_b128 v[212:215], v188 offset:21504
	ds_read_b128 v[224:227], v188 offset:22528
	ds_read_b128 v[228:231], v188 offset:23552
	global_load_lds_dwordx4 v[216:217], off
	s_add_i32 m0, s17, 0x2000
	v_lshl_add_u64 v[216:217], s[76:77], 0, v[166:167]
	s_add_u32 s76, s76, 0x20000
	s_addc_u32 s77, s77, 0
	s_add_i32 s17, s62, s29
	global_load_lds_dwordx4 v[216:217], off
	v_lshl_add_u64 v[216:217], s[76:77], 0, v[162:163]
	s_mov_b32 m0, s17
	s_nop 0
	global_load_lds_dwordx4 v[216:217], off
	s_add_i32 m0, s17, 0x2000
	s_and_b64 s[36:37], s[36:37], exec
	s_cselect_b32 s36, s22, s34
	s_cselect_b32 s17, s23, s35
	s_add_u32 s36, s36, s74
	v_lshl_add_u64 v[216:217], s[76:77], 0, v[166:167]
	s_addc_u32 s37, s17, s75
	global_load_lds_dwordx4 v[216:217], off
	v_lshl_add_u64 v[216:217], s[36:37], 0, v[32:33]
	s_mov_b32 m0, s31
	s_nop 0
	global_load_lds_dwordx4 v[216:217], off
	v_lshl_add_u64 v[216:217], s[36:37], 0, v[164:165]
	s_mov_b32 m0, s49
	s_nop 0
	global_load_lds_dwordx4 v[216:217], off
	s_waitcnt vmcnt(8)
	s_waitcnt lgkmcnt(0)
	s_barrier
	s_setprio 1
	s_waitcnt lgkmcnt(0)
	v_mfma_scale_f32_16x16x128_f8f6f4 v[94:97], v[24:31], v[192:199], v[94:97], v189, v189 op_sel_hi:[0,0,0]
	v_mfma_scale_f32_16x16x128_f8f6f4 v[86:89], v[16:23], v[192:199], v[86:89], v189, v189 op_sel_hi:[0,0,0]
	v_mfma_scale_f32_16x16x128_f8f6f4 v[78:81], v[24:31], v[200:207], v[78:81], v189, v189 op_sel_hi:[0,0,0]
	v_mfma_scale_f32_16x16x128_f8f6f4 v[66:69], v[16:23], v[200:207], v[66:69], v189, v189 op_sel_hi:[0,0,0]
	v_mfma_scale_f32_16x16x128_f8f6f4 v[54:57], v[24:31], v[208:215], v[54:57], v189, v189 op_sel_hi:[0,0,0]
	v_mfma_scale_f32_16x16x128_f8f6f4 v[46:49], v[16:23], v[208:215], v[46:49], v189, v189 op_sel_hi:[0,0,0]
	v_mfma_scale_f32_16x16x128_f8f6f4 v[38:41], v[24:31], v[224:231], v[38:41], v189, v189 op_sel_hi:[0,0,0]
	v_mfma_scale_f32_16x16x128_f8f6f4 v[34:37], v[16:23], v[224:231], v[34:37], v189, v189 op_sel_hi:[0,0,0]
	s_setprio 0
	s_setprio 1
	v_mfma_scale_f32_16x16x128_f8f6f4 v[90:93], v[8:15], v[192:199], v[90:93], v189, v189 op_sel_hi:[0,0,0]
	v_mfma_scale_f32_16x16x128_f8f6f4 v[82:85], v[0:7], v[192:199], v[82:85], v189, v189 op_sel_hi:[0,0,0]
	v_mfma_scale_f32_16x16x128_f8f6f4 v[70:73], v[8:15], v[200:207], v[70:73], v189, v189 op_sel_hi:[0,0,0]
	v_mfma_scale_f32_16x16x128_f8f6f4 v[58:61], v[0:7], v[200:207], v[58:61], v189, v189 op_sel_hi:[0,0,0]
	v_mfma_scale_f32_16x16x128_f8f6f4 v[74:77], v[8:15], v[208:215], v[74:77], v189, v189 op_sel_hi:[0,0,0]
	v_mfma_scale_f32_16x16x128_f8f6f4 v[62:65], v[0:7], v[208:215], v[62:65], v189, v189 op_sel_hi:[0,0,0]
	v_mfma_scale_f32_16x16x128_f8f6f4 v[50:53], v[8:15], v[224:231], v[50:53], v189, v189 op_sel_hi:[0,0,0]
	v_mfma_scale_f32_16x16x128_f8f6f4 v[42:45], v[0:7], v[224:231], v[42:45], v189, v189 op_sel_hi:[0,0,0]
	s_setprio 0
	s_barrier
	s_add_i32 s17, 0, 0x18000
	s_add_i32 s67, 0, 0x1c000
	v_add_u32_e32 v0, s17, v183
	v_add_u32_e32 v4, s67, v183
	ds_read_b128 v[24:27], v0
	ds_read_b128 v[28:31], v0 offset:1024
	ds_read_b128 v[16:19], v0 offset:2048
	ds_read_b128 v[20:23], v0 offset:3072
	ds_read_b128 v[8:11], v4
	ds_read_b128 v[12:15], v4 offset:1024
	ds_read_b128 v[0:3], v4 offset:2048
	ds_read_b128 v[4:7], v4 offset:3072
	s_add_u32 s36, s36, 0x20000
	s_addc_u32 s37, s37, 0
	s_mov_b32 m0, s50
	v_lshl_add_u64 v[216:217], s[36:37], 0, v[32:33]
	ds_read_b128 v[192:195], v188 offset:32768
	ds_read_b128 v[196:199], v188 offset:33792
	ds_read_b128 v[200:203], v188 offset:34816
	ds_read_b128 v[204:207], v188 offset:35840
	ds_read_b128 v[208:211], v188 offset:36864
	ds_read_b128 v[212:215], v188 offset:37888
	ds_read_b128 v[224:227], v188 offset:38912
	ds_read_b128 v[228:231], v188 offset:39936
	global_load_lds_dwordx4 v[216:217], off
	v_lshl_add_u64 v[216:217], s[36:37], 0, v[164:165]
	s_mov_b32 m0, s51
	s_nop 0
	global_load_lds_dwordx4 v[216:217], off
	s_waitcnt vmcnt(8)
	s_waitcnt lgkmcnt(0)
	s_barrier
	s_setprio 1
	s_waitcnt lgkmcnt(0)
	v_mfma_scale_f32_16x16x128_f8f6f4 v[158:161], v[24:31], v[192:199], v[158:161], v189, v189 op_sel_hi:[0,0,0]
	v_mfma_scale_f32_16x16x128_f8f6f4 v[150:153], v[16:23], v[192:199], v[150:153], v189, v189 op_sel_hi:[0,0,0]
	v_mfma_scale_f32_16x16x128_f8f6f4 v[142:145], v[24:31], v[200:207], v[142:145], v189, v189 op_sel_hi:[0,0,0]
	v_mfma_scale_f32_16x16x128_f8f6f4 v[134:137], v[16:23], v[200:207], v[134:137], v189, v189 op_sel_hi:[0,0,0]
	v_mfma_scale_f32_16x16x128_f8f6f4 v[126:129], v[24:31], v[208:215], v[126:129], v189, v189 op_sel_hi:[0,0,0]
	v_mfma_scale_f32_16x16x128_f8f6f4 v[118:121], v[16:23], v[208:215], v[118:121], v189, v189 op_sel_hi:[0,0,0]
	v_mfma_scale_f32_16x16x128_f8f6f4 v[110:113], v[24:31], v[224:231], v[110:113], v189, v189 op_sel_hi:[0,0,0]
	v_mfma_scale_f32_16x16x128_f8f6f4 v[102:105], v[16:23], v[224:231], v[102:105], v189, v189 op_sel_hi:[0,0,0]
	s_setprio 0
	s_setprio 1
	v_mfma_scale_f32_16x16x128_f8f6f4 v[154:157], v[8:15], v[192:199], v[154:157], v189, v189 op_sel_hi:[0,0,0]
	v_mfma_scale_f32_16x16x128_f8f6f4 v[146:149], v[0:7], v[192:199], v[146:149], v189, v189 op_sel_hi:[0,0,0]
	v_mfma_scale_f32_16x16x128_f8f6f4 v[138:141], v[8:15], v[200:207], v[138:141], v189, v189 op_sel_hi:[0,0,0]
	v_mfma_scale_f32_16x16x128_f8f6f4 v[130:133], v[0:7], v[200:207], v[130:133], v189, v189 op_sel_hi:[0,0,0]
	v_mfma_scale_f32_16x16x128_f8f6f4 v[122:125], v[8:15], v[208:215], v[122:125], v189, v189 op_sel_hi:[0,0,0]
	v_mfma_scale_f32_16x16x128_f8f6f4 v[114:117], v[0:7], v[208:215], v[114:117], v189, v189 op_sel_hi:[0,0,0]
	v_mfma_scale_f32_16x16x128_f8f6f4 v[106:109], v[8:15], v[224:231], v[106:109], v189, v189 op_sel_hi:[0,0,0]
	v_mfma_scale_f32_16x16x128_f8f6f4 v[98:101], v[0:7], v[224:231], v[98:101], v189, v189 op_sel_hi:[0,0,0]
	s_setprio 0
	s_barrier
	s_cmp_gt_u32 s15, 4
	s_cselect_b64 s[36:37], -1, 0
	s_and_b64 s[74:75], s[36:37], exec
	s_cselect_b32 s74, -5, 3
	s_cselect_b32 s73, s27, s39
	s_cselect_b32 s76, s26, s38
	s_add_i32 s74, s74, s15
	s_ashr_i32 s75, s74, 31
	s_lshl_b64 s[74:75], s[74:75], 7
	s_add_u32 s76, s76, s74
	s_addc_u32 s77, s73, s75
	s_add_i32 s17, s17, s29
	v_lshl_add_u64 v[216:217], s[76:77], 0, v[162:163]
	s_mov_b32 m0, s17
	ds_read_b128 v[192:195], v188 offset:49152
	ds_read_b128 v[196:199], v188 offset:50176
	ds_read_b128 v[200:203], v188 offset:51200
	ds_read_b128 v[204:207], v188 offset:52224
	ds_read_b128 v[208:211], v188 offset:53248
	ds_read_b128 v[212:215], v188 offset:54272
	ds_read_b128 v[224:227], v188 offset:55296
	ds_read_b128 v[228:231], v188 offset:56320
	global_load_lds_dwordx4 v[216:217], off
	s_add_i32 m0, s17, 0x2000
	v_lshl_add_u64 v[216:217], s[76:77], 0, v[166:167]
	s_add_u32 s76, s76, 0x20000
	s_addc_u32 s77, s77, 0
	s_add_i32 s17, s67, s29
	global_load_lds_dwordx4 v[216:217], off
	v_lshl_add_u64 v[216:217], s[76:77], 0, v[162:163]
	s_mov_b32 m0, s17
	s_nop 0
	global_load_lds_dwordx4 v[216:217], off
	s_add_i32 m0, s17, 0x2000
	s_and_b64 s[36:37], s[36:37], exec
	s_cselect_b32 s36, s22, s34
	s_cselect_b32 s17, s23, s35
	s_add_u32 s36, s36, s74
	v_lshl_add_u64 v[216:217], s[76:77], 0, v[166:167]
	s_addc_u32 s37, s17, s75
	global_load_lds_dwordx4 v[216:217], off
	v_lshl_add_u64 v[216:217], s[36:37], 0, v[32:33]
	s_mov_b32 m0, s56
	s_nop 0
	global_load_lds_dwordx4 v[216:217], off
	v_lshl_add_u64 v[216:217], s[36:37], 0, v[164:165]
	s_mov_b32 m0, s57
	s_nop 0
	global_load_lds_dwordx4 v[216:217], off
	s_waitcnt vmcnt(8)
	s_waitcnt lgkmcnt(0)
	s_barrier
	s_setprio 1
	s_waitcnt lgkmcnt(0)
	v_mfma_scale_f32_16x16x128_f8f6f4 v[94:97], v[24:31], v[192:199], v[94:97], v189, v189 op_sel_hi:[0,0,0]
	v_mfma_scale_f32_16x16x128_f8f6f4 v[86:89], v[16:23], v[192:199], v[86:89], v189, v189 op_sel_hi:[0,0,0]
	v_mfma_scale_f32_16x16x128_f8f6f4 v[78:81], v[24:31], v[200:207], v[78:81], v189, v189 op_sel_hi:[0,0,0]
	v_mfma_scale_f32_16x16x128_f8f6f4 v[66:69], v[16:23], v[200:207], v[66:69], v189, v189 op_sel_hi:[0,0,0]
	v_mfma_scale_f32_16x16x128_f8f6f4 v[54:57], v[24:31], v[208:215], v[54:57], v189, v189 op_sel_hi:[0,0,0]
	v_mfma_scale_f32_16x16x128_f8f6f4 v[46:49], v[16:23], v[208:215], v[46:49], v189, v189 op_sel_hi:[0,0,0]
	v_mfma_scale_f32_16x16x128_f8f6f4 v[38:41], v[24:31], v[224:231], v[38:41], v189, v189 op_sel_hi:[0,0,0]
	v_mfma_scale_f32_16x16x128_f8f6f4 v[34:37], v[16:23], v[224:231], v[34:37], v189, v189 op_sel_hi:[0,0,0]
	s_setprio 0
	s_setprio 1
	v_mfma_scale_f32_16x16x128_f8f6f4 v[90:93], v[8:15], v[192:199], v[90:93], v189, v189 op_sel_hi:[0,0,0]
	v_mfma_scale_f32_16x16x128_f8f6f4 v[82:85], v[0:7], v[192:199], v[82:85], v189, v189 op_sel_hi:[0,0,0]
	v_mfma_scale_f32_16x16x128_f8f6f4 v[70:73], v[8:15], v[200:207], v[70:73], v189, v189 op_sel_hi:[0,0,0]
	v_mfma_scale_f32_16x16x128_f8f6f4 v[58:61], v[0:7], v[200:207], v[58:61], v189, v189 op_sel_hi:[0,0,0]
	v_mfma_scale_f32_16x16x128_f8f6f4 v[74:77], v[8:15], v[208:215], v[74:77], v189, v189 op_sel_hi:[0,0,0]
	v_mfma_scale_f32_16x16x128_f8f6f4 v[62:65], v[0:7], v[208:215], v[62:65], v189, v189 op_sel_hi:[0,0,0]
	v_mfma_scale_f32_16x16x128_f8f6f4 v[50:53], v[8:15], v[224:231], v[50:53], v189, v189 op_sel_hi:[0,0,0]
	v_mfma_scale_f32_16x16x128_f8f6f4 v[42:45], v[0:7], v[224:231], v[42:45], v189, v189 op_sel_hi:[0,0,0]
	s_setprio 0
	s_barrier
	v_lshl_add_u64 v[178:179], v[178:179], 0, s[6:7]
	v_lshl_add_u64 v[180:181], v[180:181], 0, s[6:7]
	s_add_i32 s15, s15, 2
	s_and_b64 vcc, exec, s[40:41]
	s_cbranch_vccnz .LBB0_594
	s_andn2_b64 vcc, exec, s[12:13]
	s_cbranch_vccnz .LBB0_597
	s_barrier
.LBB0_597:
	s_mul_hi_u32 s15, s66, 0xaaaaaaab
	s_lshr_b32 s15, s15, 1
	s_mul_i32 s15, s15, 3
	s_sub_i32 s15, s66, s15
	s_nop 15
	s_nop 7
	v_lshl_add_u32 v4, s15, 11, v185
	ds_read2_b64 v[0:3], v4 offset1:16
	v_pk_mul_f32 v[14:15], v[160:161], v[156:157]
	v_pk_mul_f32 v[16:17], v[158:159], v[154:155]
	v_pk_mul_f32 v[18:19], v[150:151], v[146:147]
	s_andn2_b64 vcc, exec, s[2:3]
	s_waitcnt lgkmcnt(0)
	v_ffbh_u32_e32 v5, v1
	v_min_u32_e32 v5, 32, v5
	v_lshlrev_b64 v[0:1], v5, v[0:1]
	v_min_u32_e32 v0, 1, v0
	v_or_b32_e32 v0, v1, v0
	v_ffbh_u32_e32 v6, v3
	v_cvt_f32_u32_e32 v7, v0
	v_min_u32_e32 v6, 32, v6
	v_lshlrev_b64 v[0:1], v6, v[2:3]
	v_sub_u32_e32 v5, 32, v5
	v_min_u32_e32 v0, 1, v0
	v_or_b32_e32 v0, v1, v0
	v_ldexp_f32 v1, v7, v5
	v_fmamk_f32 v1, v1, 0x30800000, v190
	v_cvt_f32_u32_e32 v5, v0
	v_rsq_f32_e32 v7, v1
	ds_read2_b64 v[0:3], v4 offset0:32 offset1:48
	v_sub_u32_e32 v6, 32, v6
	v_ldexp_f32 v5, v5, v6
	v_fmamk_f32 v5, v5, 0x30800000, v190
	v_rsq_f32_e32 v5, v5
	s_waitcnt lgkmcnt(0)
	v_ffbh_u32_e32 v6, v1
	v_min_u32_e32 v6, 32, v6
	v_lshlrev_b64 v[0:1], v6, v[0:1]
	v_min_u32_e32 v0, 1, v0
	v_or_b32_e32 v0, v1, v0
	v_cvt_f32_u32_e32 v0, v0
	v_sub_u32_e32 v1, 32, v6
	v_mul_f32_e32 v20, 0x3b000000, v5
	v_mul_f32_e32 v8, 0x3b000000, v7
	v_ldexp_f32 v0, v0, v1
	v_fmamk_f32 v5, v0, 0x30800000, v190
	v_ffbh_u32_e32 v0, v3
	v_min_u32_e32 v6, 32, v0
	v_lshlrev_b64 v[0:1], v6, v[2:3]
	v_min_u32_e32 v0, 1, v0
	v_or_b32_e32 v0, v1, v0
	v_cvt_f32_u32_e32 v7, v0
	ds_read2_b64 v[0:3], v4 offset0:128 offset1:144
	v_sub_u32_e32 v6, 32, v6
	v_rsq_f32_e32 v5, v5
	v_ldexp_f32 v6, v7, v6
	v_fmamk_f32 v6, v6, 0x30800000, v190
	s_waitcnt lgkmcnt(0)
	v_ffbh_u32_e32 v7, v1
	v_min_u32_e32 v7, 32, v7
	v_lshlrev_b64 v[0:1], v7, v[0:1]
	v_min_u32_e32 v0, 1, v0
	v_or_b32_e32 v0, v1, v0
	v_cvt_f32_u32_e32 v0, v0
	v_rsq_f32_e32 v6, v6
	v_sub_u32_e32 v1, 32, v7
	v_mul_f32_e32 v22, 0x3b000000, v5
	v_ldexp_f32 v5, v0, v1
	v_ffbh_u32_e32 v0, v3
	v_mul_f32_e32 v23, 0x3b000000, v6
	v_min_u32_e32 v6, 32, v0
	v_lshlrev_b64 v[0:1], v6, v[2:3]
	v_min_u32_e32 v0, 1, v0
	v_or_b32_e32 v0, v1, v0
	v_cvt_f32_u32_e32 v7, v0
	ds_read2_b64 v[0:3], v4 offset0:160 offset1:176
	v_fmamk_f32 v4, v5, 0x30800000, v190
	v_sub_u32_e32 v5, 32, v6
	v_ldexp_f32 v5, v7, v5
	v_rsq_f32_e32 v4, v4
	s_waitcnt lgkmcnt(0)
	v_ffbh_u32_e32 v6, v1
	v_min_u32_e32 v6, 32, v6
	v_lshlrev_b64 v[0:1], v6, v[0:1]
	v_min_u32_e32 v0, 1, v0
	v_or_b32_e32 v0, v1, v0
	v_cvt_f32_u32_e32 v0, v0
	v_fmamk_f32 v1, v5, 0x30800000, v190
	v_rsq_f32_e32 v5, v1
	v_sub_u32_e32 v1, 32, v6
	v_ldexp_f32 v6, v0, v1
	v_ffbh_u32_e32 v0, v3
	v_min_u32_e32 v7, 32, v0
	v_lshlrev_b64 v[0:1], v7, v[2:3]
	v_min_u32_e32 v0, 1, v0
	v_or_b32_e32 v0, v1, v0
	v_cvt_f32_u32_e32 v0, v0
	v_sub_u32_e32 v2, 32, v7
	v_fmamk_f32 v1, v6, 0x30800000, v190
	v_rsq_f32_e32 v1, v1
	v_ldexp_f32 v0, v0, v2
	v_mul_f32_e32 v2, v8, v8
	v_mul_f32_e32 v8, 0xbfb8aa3b, v8
	v_pk_mul_f32 v[10:11], v[160:161], v[8:9] op_sel_hi:[1,0]
	v_mul_f32_e32 v2, 0x41000000, v2
	v_exp_f32_e32 v10, v10
	v_exp_f32_e32 v11, v11
	v_pk_mul_f32 v[12:13], v[158:159], v[8:9] op_sel_hi:[1,0]
	v_pk_mul_f32 v[14:15], v[14:15], v[2:3] op_sel_hi:[1,0]
	v_exp_f32_e32 v12, v12
	v_pk_add_f32 v[10:11], v[10:11], 1.0 op_sel_hi:[1,0]
	v_exp_f32_e32 v13, v13
	v_rcp_f32_e32 v10, v10
	v_rcp_f32_e32 v11, v11
	v_pk_mul_f32 v[16:17], v[16:17], v[2:3] op_sel_hi:[1,0]
	v_pk_add_f32 v[12:13], v[12:13], 1.0 op_sel_hi:[1,0]
	v_pk_mul_f32 v[18:19], v[18:19], v[2:3] op_sel_hi:[1,0]
	v_pk_mul_f32 v[10:11], v[14:15], v[10:11]
	v_pk_mul_f32 v[14:15], v[152:153], v[8:9] op_sel_hi:[1,0]
	v_pk_mul_f32 v[8:9], v[150:151], v[8:9] op_sel_hi:[1,0]
	v_exp_f32_e32 v14, v14
	v_exp_f32_e32 v8, v8
	v_exp_f32_e32 v9, v9
	v_exp_f32_e32 v15, v15
	v_rcp_f32_e32 v12, v12
	v_rcp_f32_e32 v13, v13
	v_pk_add_f32 v[8:9], v[8:9], 1.0 op_sel_hi:[1,0]
	v_pk_add_f32 v[14:15], v[14:15], 1.0 op_sel_hi:[1,0]
	v_rcp_f32_e32 v8, v8
	v_rcp_f32_e32 v9, v9
	v_rcp_f32_e32 v14, v14
	v_rcp_f32_e32 v15, v15
	v_pk_mul_f32 v[12:13], v[16:17], v[12:13]
	v_pk_mul_f32 v[16:17], v[152:153], v[148:149]
	v_pk_mul_f32 v[8:9], v[18:19], v[8:9]
	v_pk_mul_f32 v[2:3], v[16:17], v[2:3] op_sel_hi:[1,0]
	v_med3_f32 v12, v12, s63, v191
	v_pk_mul_f32 v[2:3], v[2:3], v[14:15]
	v_med3_f32 v13, v13, s63, v191
	v_med3_f32 v14, v10, s63, v191
	v_med3_f32 v15, v11, s63, v191
	v_mov_b32_e32 v10, 0
	v_med3_f32 v8, v8, s63, v191
	v_med3_f32 v9, v9, s63, v191
	v_mov_b32_e32 v11, 0
	v_fmamk_f32 v0, v0, 0x30800000, v190
	v_cvt_pk_fp8_f32 v10, v12, v13
	v_cvt_pk_fp8_f32 v11, v8, v9
	v_rsq_f32_e32 v0, v0
	v_med3_f32 v2, v2, s63, v191
	v_med3_f32 v3, v3, s63, v191
	v_cvt_pk_fp8_f32 v10, v14, v15 op_sel:[0,0,1]
	v_cvt_pk_fp8_f32 v11, v2, v3 op_sel:[0,0,1]
	v_mul_f32_e32 v24, 0x3b000000, v4
	v_mul_f32_e32 v7, 0x3b000000, v5
	v_mul_f32_e32 v5, 0x3b000000, v0
	v_lshl_or_b32 v0, s30, 7, v184
	v_lshl_add_u32 v4, s28, 8, v182
	v_mov_b64_e32 v[2:3], s[10:11]
	v_mul_f32_e32 v6, 0x3b000000, v1
	v_ashrrev_i32_e32 v1, 31, v0
	v_mad_i64_i32 v[8:9], s[34:35], v4, s64, v[2:3]
	v_lshl_add_u64 v[8:9], v[8:9], 0, v[0:1]
	global_store_dwordx2 v[8:9], v[10:11], off
	v_mul_f32_e32 v10, 0xbfb8aa3b, v20
	v_pk_mul_f32 v[12:13], v[144:145], v[10:11] op_sel_hi:[1,0]
	v_mul_f32_e32 v8, v20, v20
	v_exp_f32_e32 v12, v12
	v_exp_f32_e32 v13, v13
	v_mul_f32_e32 v8, 0x41000000, v8
	v_pk_mul_f32 v[16:17], v[144:145], v[140:141]
	v_pk_mul_f32 v[14:15], v[142:143], v[10:11] op_sel_hi:[1,0]
	v_pk_add_f32 v[12:13], v[12:13], 1.0 op_sel_hi:[1,0]
	v_pk_mul_f32 v[16:17], v[16:17], v[8:9] op_sel_hi:[1,0]
	v_rcp_f32_e32 v12, v12
	v_rcp_f32_e32 v13, v13
	v_exp_f32_e32 v14, v14
	v_exp_f32_e32 v15, v15
	v_pk_mul_f32 v[18:19], v[142:143], v[138:139]
	v_pk_mul_f32 v[12:13], v[16:17], v[12:13]
	v_pk_mul_f32 v[16:17], v[136:137], v[10:11] op_sel_hi:[1,0]
	v_pk_mul_f32 v[10:11], v[134:135], v[10:11] op_sel_hi:[1,0]
	v_exp_f32_e32 v16, v16
	v_exp_f32_e32 v10, v10
	v_exp_f32_e32 v11, v11
	v_exp_f32_e32 v17, v17
	v_pk_add_f32 v[14:15], v[14:15], 1.0 op_sel_hi:[1,0]
	v_pk_mul_f32 v[18:19], v[18:19], v[8:9] op_sel_hi:[1,0]
	v_rcp_f32_e32 v14, v14
	v_rcp_f32_e32 v15, v15
	v_pk_add_f32 v[10:11], v[10:11], 1.0 op_sel_hi:[1,0]
	v_pk_add_f32 v[16:17], v[16:17], 1.0 op_sel_hi:[1,0]
	v_rcp_f32_e32 v10, v10
	v_rcp_f32_e32 v11, v11
	v_rcp_f32_e32 v16, v16
	v_rcp_f32_e32 v17, v17
	v_pk_mul_f32 v[20:21], v[134:135], v[130:131]
	v_pk_mul_f32 v[14:15], v[18:19], v[14:15]
	v_pk_mul_f32 v[18:19], v[136:137], v[132:133]
	v_pk_mul_f32 v[20:21], v[20:21], v[8:9] op_sel_hi:[1,0]
	v_pk_mul_f32 v[8:9], v[18:19], v[8:9] op_sel_hi:[1,0]
	v_pk_mul_f32 v[10:11], v[20:21], v[10:11]
	v_pk_mul_f32 v[8:9], v[8:9], v[16:17]
	v_med3_f32 v14, v14, s63, v191
	v_med3_f32 v15, v15, s63, v191
	v_med3_f32 v17, v12, s63, v191
	v_med3_f32 v18, v13, s63, v191
	v_mov_b32_e32 v12, 0
	v_med3_f32 v10, v10, s63, v191
	v_med3_f32 v11, v11, s63, v191
	v_mov_b32_e32 v13, 0
	v_cvt_pk_fp8_f32 v12, v14, v15
	v_cvt_pk_fp8_f32 v13, v10, v11
	v_med3_f32 v8, v8, s63, v191
	v_med3_f32 v9, v9, s63, v191
	v_cvt_pk_fp8_f32 v12, v17, v18 op_sel:[0,0,1]
	v_cvt_pk_fp8_f32 v13, v8, v9 op_sel:[0,0,1]
	v_or_b32_e32 v16, 16, v4
	v_mad_i64_i32 v[8:9], s[34:35], v16, s64, v[2:3]
	v_lshl_add_u64 v[8:9], v[8:9], 0, v[0:1]
	v_mul_f32_e32 v10, 0xbfb8aa3b, v22
	global_store_dwordx2 v[8:9], v[12:13], off
	v_pk_mul_f32 v[12:13], v[128:129], v[10:11] op_sel_hi:[1,0]
	v_mul_f32_e32 v8, v22, v22
	v_exp_f32_e32 v12, v12
	v_exp_f32_e32 v13, v13
	v_mul_f32_e32 v8, 0x41000000, v8
	v_pk_mul_f32 v[16:17], v[128:129], v[124:125]
	v_pk_mul_f32 v[14:15], v[126:127], v[10:11] op_sel_hi:[1,0]
	v_pk_add_f32 v[12:13], v[12:13], 1.0 op_sel_hi:[1,0]
	v_pk_mul_f32 v[16:17], v[16:17], v[8:9] op_sel_hi:[1,0]
	v_rcp_f32_e32 v12, v12
	v_rcp_f32_e32 v13, v13
	v_exp_f32_e32 v14, v14
	v_exp_f32_e32 v15, v15
	v_pk_mul_f32 v[18:19], v[126:127], v[122:123]
	v_pk_mul_f32 v[12:13], v[16:17], v[12:13]
	v_pk_mul_f32 v[16:17], v[120:121], v[10:11] op_sel_hi:[1,0]
	v_pk_mul_f32 v[10:11], v[118:119], v[10:11] op_sel_hi:[1,0]
	v_exp_f32_e32 v16, v16
	v_exp_f32_e32 v10, v10
	v_exp_f32_e32 v11, v11
	v_exp_f32_e32 v17, v17
	v_pk_add_f32 v[14:15], v[14:15], 1.0 op_sel_hi:[1,0]
	v_pk_mul_f32 v[18:19], v[18:19], v[8:9] op_sel_hi:[1,0]
	v_rcp_f32_e32 v14, v14
	v_rcp_f32_e32 v15, v15
	v_pk_add_f32 v[10:11], v[10:11], 1.0 op_sel_hi:[1,0]
	v_pk_add_f32 v[16:17], v[16:17], 1.0 op_sel_hi:[1,0]
	v_rcp_f32_e32 v10, v10
	v_rcp_f32_e32 v11, v11
	v_rcp_f32_e32 v16, v16
	v_rcp_f32_e32 v17, v17
	v_pk_mul_f32 v[20:21], v[118:119], v[114:115]
	v_pk_mul_f32 v[14:15], v[18:19], v[14:15]
	v_pk_mul_f32 v[18:19], v[120:121], v[116:117]
	v_pk_mul_f32 v[20:21], v[20:21], v[8:9] op_sel_hi:[1,0]
	v_pk_mul_f32 v[8:9], v[18:19], v[8:9] op_sel_hi:[1,0]
	v_pk_mul_f32 v[10:11], v[20:21], v[10:11]
	v_pk_mul_f32 v[8:9], v[8:9], v[16:17]
	v_med3_f32 v14, v14, s63, v191
	v_med3_f32 v15, v15, s63, v191
	v_med3_f32 v17, v12, s63, v191
	v_med3_f32 v18, v13, s63, v191
	v_mov_b32_e32 v12, 0
	v_med3_f32 v10, v10, s63, v191
	v_med3_f32 v11, v11, s63, v191
	v_mov_b32_e32 v13, 0
	v_cvt_pk_fp8_f32 v12, v14, v15
	v_cvt_pk_fp8_f32 v13, v10, v11
	v_med3_f32 v8, v8, s63, v191
	v_med3_f32 v9, v9, s63, v191
	v_cvt_pk_fp8_f32 v12, v17, v18 op_sel:[0,0,1]
	v_cvt_pk_fp8_f32 v13, v8, v9 op_sel:[0,0,1]
	v_or_b32_e32 v16, 32, v4
	v_mad_i64_i32 v[8:9], s[34:35], v16, s64, v[2:3]
	v_lshl_add_u64 v[8:9], v[8:9], 0, v[0:1]
	v_mul_f32_e32 v10, 0xbfb8aa3b, v23
	global_store_dwordx2 v[8:9], v[12:13], off
	v_pk_mul_f32 v[12:13], v[112:113], v[10:11] op_sel_hi:[1,0]
	v_mul_f32_e32 v8, v23, v23
	v_exp_f32_e32 v12, v12
	v_exp_f32_e32 v13, v13
	v_mul_f32_e32 v8, 0x41000000, v8
	v_pk_mul_f32 v[16:17], v[112:113], v[108:109]
	v_pk_mul_f32 v[14:15], v[110:111], v[10:11] op_sel_hi:[1,0]
	v_pk_add_f32 v[12:13], v[12:13], 1.0 op_sel_hi:[1,0]
	v_pk_mul_f32 v[16:17], v[16:17], v[8:9] op_sel_hi:[1,0]
	v_rcp_f32_e32 v12, v12
	v_rcp_f32_e32 v13, v13
	v_exp_f32_e32 v14, v14
	v_exp_f32_e32 v15, v15
	v_pk_mul_f32 v[18:19], v[110:111], v[106:107]
	v_pk_mul_f32 v[12:13], v[16:17], v[12:13]
	v_pk_mul_f32 v[16:17], v[104:105], v[10:11] op_sel_hi:[1,0]
	v_pk_mul_f32 v[10:11], v[102:103], v[10:11] op_sel_hi:[1,0]
	v_exp_f32_e32 v16, v16
	v_exp_f32_e32 v10, v10
	v_exp_f32_e32 v11, v11
	v_exp_f32_e32 v17, v17
	v_pk_add_f32 v[14:15], v[14:15], 1.0 op_sel_hi:[1,0]
	v_pk_mul_f32 v[18:19], v[18:19], v[8:9] op_sel_hi:[1,0]
	v_rcp_f32_e32 v14, v14
	v_rcp_f32_e32 v15, v15
	v_pk_add_f32 v[10:11], v[10:11], 1.0 op_sel_hi:[1,0]
	v_pk_add_f32 v[16:17], v[16:17], 1.0 op_sel_hi:[1,0]
	v_rcp_f32_e32 v10, v10
	v_rcp_f32_e32 v11, v11
	v_rcp_f32_e32 v16, v16
	v_rcp_f32_e32 v17, v17
	v_pk_mul_f32 v[20:21], v[102:103], v[98:99]
	v_pk_mul_f32 v[14:15], v[18:19], v[14:15]
	v_pk_mul_f32 v[18:19], v[104:105], v[100:101]
	v_pk_mul_f32 v[20:21], v[20:21], v[8:9] op_sel_hi:[1,0]
	v_pk_mul_f32 v[8:9], v[18:19], v[8:9] op_sel_hi:[1,0]
	v_pk_mul_f32 v[10:11], v[20:21], v[10:11]
	v_pk_mul_f32 v[8:9], v[8:9], v[16:17]
	v_med3_f32 v14, v14, s63, v191
	v_med3_f32 v15, v15, s63, v191
	v_med3_f32 v17, v12, s63, v191
	v_med3_f32 v18, v13, s63, v191
	v_mov_b32_e32 v12, 0
	v_med3_f32 v10, v10, s63, v191
	v_med3_f32 v11, v11, s63, v191
	v_mov_b32_e32 v13, 0
	v_cvt_pk_fp8_f32 v12, v14, v15
	v_cvt_pk_fp8_f32 v13, v10, v11
	v_med3_f32 v8, v8, s63, v191
	v_med3_f32 v9, v9, s63, v191
	v_cvt_pk_fp8_f32 v12, v17, v18 op_sel:[0,0,1]
	v_cvt_pk_fp8_f32 v13, v8, v9 op_sel:[0,0,1]
	v_or_b32_e32 v16, 48, v4
	v_mad_i64_i32 v[8:9], s[34:35], v16, s64, v[2:3]
	v_lshl_add_u64 v[8:9], v[8:9], 0, v[0:1]
	v_mul_f32_e32 v10, 0xbfb8aa3b, v24
	global_store_dwordx2 v[8:9], v[12:13], off
	v_pk_mul_f32 v[12:13], v[96:97], v[10:11] op_sel_hi:[1,0]
	v_mul_f32_e32 v8, v24, v24
	v_exp_f32_e32 v12, v12
	v_exp_f32_e32 v13, v13
	v_mul_f32_e32 v8, 0x41000000, v8
	v_pk_mul_f32 v[16:17], v[96:97], v[92:93]
	v_pk_mul_f32 v[14:15], v[94:95], v[10:11] op_sel_hi:[1,0]
	v_pk_add_f32 v[12:13], v[12:13], 1.0 op_sel_hi:[1,0]
	v_pk_mul_f32 v[16:17], v[16:17], v[8:9] op_sel_hi:[1,0]
	v_rcp_f32_e32 v12, v12
	v_rcp_f32_e32 v13, v13
	v_exp_f32_e32 v14, v14
	v_exp_f32_e32 v15, v15
	v_pk_mul_f32 v[18:19], v[94:95], v[90:91]
	v_pk_mul_f32 v[12:13], v[16:17], v[12:13]
	v_pk_mul_f32 v[16:17], v[88:89], v[10:11] op_sel_hi:[1,0]
	v_pk_mul_f32 v[10:11], v[86:87], v[10:11] op_sel_hi:[1,0]
	v_exp_f32_e32 v16, v16
	v_exp_f32_e32 v10, v10
	v_exp_f32_e32 v11, v11
	v_exp_f32_e32 v17, v17
	v_pk_add_f32 v[14:15], v[14:15], 1.0 op_sel_hi:[1,0]
	v_pk_mul_f32 v[18:19], v[18:19], v[8:9] op_sel_hi:[1,0]
	v_rcp_f32_e32 v14, v14
	v_rcp_f32_e32 v15, v15
	v_pk_add_f32 v[10:11], v[10:11], 1.0 op_sel_hi:[1,0]
	v_pk_add_f32 v[16:17], v[16:17], 1.0 op_sel_hi:[1,0]
	v_rcp_f32_e32 v10, v10
	v_rcp_f32_e32 v11, v11
	v_rcp_f32_e32 v16, v16
	v_rcp_f32_e32 v17, v17
	v_pk_mul_f32 v[20:21], v[86:87], v[82:83]
	v_pk_mul_f32 v[14:15], v[18:19], v[14:15]
	v_pk_mul_f32 v[18:19], v[88:89], v[84:85]
	v_pk_mul_f32 v[20:21], v[20:21], v[8:9] op_sel_hi:[1,0]
	v_pk_mul_f32 v[8:9], v[18:19], v[8:9] op_sel_hi:[1,0]
	v_pk_mul_f32 v[10:11], v[20:21], v[10:11]
	v_pk_mul_f32 v[8:9], v[8:9], v[16:17]
	v_med3_f32 v14, v14, s63, v191
	v_med3_f32 v15, v15, s63, v191
	v_med3_f32 v16, v12, s63, v191
	v_med3_f32 v17, v13, s63, v191
	v_mov_b32_e32 v12, 0
	v_med3_f32 v10, v10, s63, v191
	v_med3_f32 v11, v11, s63, v191
	v_mov_b32_e32 v13, 0
	v_cvt_pk_fp8_f32 v12, v14, v15
	v_cvt_pk_fp8_f32 v13, v10, v11
	v_med3_f32 v8, v8, s63, v191
	v_med3_f32 v9, v9, s63, v191
	v_cvt_pk_fp8_f32 v12, v16, v17 op_sel:[0,0,1]
	v_cvt_pk_fp8_f32 v13, v8, v9 op_sel:[0,0,1]
	v_add_u32_e32 v22, 0x80, v4
	v_mad_i64_i32 v[8:9], s[34:35], v22, s64, v[2:3]
	v_lshl_add_u64 v[8:9], v[8:9], 0, v[0:1]
	v_mul_f32_e32 v10, 0xbfb8aa3b, v7
	global_store_dwordx2 v[8:9], v[12:13], off
	v_pk_mul_f32 v[12:13], v[80:81], v[10:11] op_sel_hi:[1,0]
	v_mul_f32_e32 v8, v7, v7
	v_exp_f32_e32 v12, v12
	v_exp_f32_e32 v13, v13
	v_mul_f32_e32 v8, 0x41000000, v8
	v_pk_mul_f32 v[16:17], v[80:81], v[72:73]
	v_pk_mul_f32 v[14:15], v[78:79], v[10:11] op_sel_hi:[1,0]
	v_pk_add_f32 v[12:13], v[12:13], 1.0 op_sel_hi:[1,0]
	v_pk_mul_f32 v[16:17], v[16:17], v[8:9] op_sel_hi:[1,0]
	v_rcp_f32_e32 v12, v12
	v_rcp_f32_e32 v13, v13
	v_exp_f32_e32 v14, v14
	v_exp_f32_e32 v15, v15
	v_pk_mul_f32 v[18:19], v[78:79], v[70:71]
	v_pk_mul_f32 v[12:13], v[16:17], v[12:13]
	v_pk_mul_f32 v[16:17], v[68:69], v[10:11] op_sel_hi:[1,0]
	v_pk_mul_f32 v[10:11], v[66:67], v[10:11] op_sel_hi:[1,0]
	v_exp_f32_e32 v16, v16
	v_exp_f32_e32 v10, v10
	v_exp_f32_e32 v11, v11
	v_exp_f32_e32 v17, v17
	v_pk_add_f32 v[14:15], v[14:15], 1.0 op_sel_hi:[1,0]
	v_pk_mul_f32 v[18:19], v[18:19], v[8:9] op_sel_hi:[1,0]
	v_rcp_f32_e32 v14, v14
	v_rcp_f32_e32 v15, v15
	v_pk_add_f32 v[10:11], v[10:11], 1.0 op_sel_hi:[1,0]
	v_pk_add_f32 v[16:17], v[16:17], 1.0 op_sel_hi:[1,0]
	v_rcp_f32_e32 v10, v10
	v_rcp_f32_e32 v11, v11
	v_rcp_f32_e32 v16, v16
	v_rcp_f32_e32 v17, v17
	v_pk_mul_f32 v[20:21], v[66:67], v[58:59]
	v_pk_mul_f32 v[14:15], v[18:19], v[14:15]
	v_pk_mul_f32 v[18:19], v[68:69], v[60:61]
	v_pk_mul_f32 v[20:21], v[20:21], v[8:9] op_sel_hi:[1,0]
	v_pk_mul_f32 v[8:9], v[18:19], v[8:9] op_sel_hi:[1,0]
	v_pk_mul_f32 v[10:11], v[20:21], v[10:11]
	v_pk_mul_f32 v[8:9], v[8:9], v[16:17]
	v_med3_f32 v17, v13, s63, v191
	v_med3_f32 v10, v10, s63, v191
	v_med3_f32 v11, v11, s63, v191
	v_mov_b32_e32 v13, 0
	v_cvt_pk_fp8_f32 v13, v10, v11
	v_add_u32_e32 v7, 0x90, v4
	v_med3_f32 v8, v8, s63, v191
	v_med3_f32 v9, v9, s63, v191
	v_med3_f32 v14, v14, s63, v191
	v_med3_f32 v15, v15, s63, v191
	v_med3_f32 v16, v12, s63, v191
	v_mov_b32_e32 v12, 0
	v_cvt_pk_fp8_f32 v13, v8, v9 op_sel:[0,0,1]
	v_mad_i64_i32 v[8:9], s[34:35], v7, s64, v[2:3]
	v_mul_f32_e32 v7, v6, v6
	v_mul_f32_e32 v6, 0xbfb8aa3b, v6
	v_cvt_pk_fp8_f32 v12, v14, v15
	v_pk_mul_f32 v[10:11], v[56:57], v[6:7] op_sel_hi:[1,0]
	v_lshl_add_u64 v[8:9], v[8:9], 0, v[0:1]
	v_exp_f32_e32 v10, v10
	v_exp_f32_e32 v11, v11
	v_cvt_pk_fp8_f32 v12, v16, v17 op_sel:[0,0,1]
	v_pk_mul_f32 v[14:15], v[56:57], v[76:77]
	v_pk_mul_f32 v[16:17], v[54:55], v[74:75]
	v_pk_add_f32 v[10:11], v[10:11], 1.0 op_sel_hi:[1,0]
	global_store_dwordx2 v[8:9], v[12:13], off
	v_rcp_f32_e32 v10, v10
	v_rcp_f32_e32 v11, v11
	v_mul_f32_e32 v8, 0x41000000, v7
	v_pk_mul_f32 v[12:13], v[54:55], v[6:7] op_sel_hi:[1,0]
	v_pk_mul_f32 v[14:15], v[14:15], v[8:9] op_sel_hi:[1,0]
	v_exp_f32_e32 v12, v12
	v_exp_f32_e32 v13, v13
	v_pk_mul_f32 v[10:11], v[14:15], v[10:11]
	v_pk_mul_f32 v[14:15], v[48:49], v[6:7] op_sel_hi:[1,0]
	v_pk_mul_f32 v[6:7], v[46:47], v[6:7] op_sel_hi:[1,0]
	v_exp_f32_e32 v14, v14
	v_exp_f32_e32 v6, v6
	v_exp_f32_e32 v7, v7
	v_exp_f32_e32 v15, v15
	v_pk_add_f32 v[12:13], v[12:13], 1.0 op_sel_hi:[1,0]
	v_pk_mul_f32 v[16:17], v[16:17], v[8:9] op_sel_hi:[1,0]
	v_rcp_f32_e32 v12, v12
	v_rcp_f32_e32 v13, v13
	v_pk_add_f32 v[6:7], v[6:7], 1.0 op_sel_hi:[1,0]
	v_pk_add_f32 v[14:15], v[14:15], 1.0 op_sel_hi:[1,0]
	v_rcp_f32_e32 v6, v6
	v_rcp_f32_e32 v7, v7
	v_rcp_f32_e32 v14, v14
	v_rcp_f32_e32 v15, v15
	v_pk_mul_f32 v[18:19], v[46:47], v[62:63]
	v_pk_mul_f32 v[12:13], v[16:17], v[12:13]
	v_pk_mul_f32 v[16:17], v[48:49], v[64:65]
	v_pk_mul_f32 v[18:19], v[18:19], v[8:9] op_sel_hi:[1,0]
	v_pk_mul_f32 v[8:9], v[16:17], v[8:9] op_sel_hi:[1,0]
	v_pk_mul_f32 v[6:7], v[18:19], v[6:7]
	v_pk_mul_f32 v[8:9], v[8:9], v[14:15]
	v_med3_f32 v12, v12, s63, v191
	v_med3_f32 v13, v13, s63, v191
	v_med3_f32 v15, v10, s63, v191
	v_med3_f32 v16, v11, s63, v191
	v_mov_b32_e32 v10, 0
	v_med3_f32 v6, v6, s63, v191
	v_med3_f32 v7, v7, s63, v191
	v_mov_b32_e32 v11, 0
	v_cvt_pk_fp8_f32 v10, v12, v13
	v_cvt_pk_fp8_f32 v11, v6, v7
	v_med3_f32 v6, v8, s63, v191
	v_med3_f32 v7, v9, s63, v191
	v_cvt_pk_fp8_f32 v10, v15, v16 op_sel:[0,0,1]
	v_cvt_pk_fp8_f32 v11, v6, v7 op_sel:[0,0,1]
	v_add_u32_e32 v14, 0xa0, v4
	v_mad_i64_i32 v[6:7], s[34:35], v14, s64, v[2:3]
	v_lshl_add_u64 v[6:7], v[6:7], 0, v[0:1]
	v_mul_f32_e32 v8, 0xbfb8aa3b, v5
	global_store_dwordx2 v[6:7], v[10:11], off
	v_pk_mul_f32 v[10:11], v[40:41], v[8:9] op_sel_hi:[1,0]
	v_mul_f32_e32 v6, v5, v5
	v_exp_f32_e32 v10, v10
	v_exp_f32_e32 v11, v11
	v_mul_f32_e32 v6, 0x41000000, v6
	v_pk_mul_f32 v[12:13], v[38:39], v[8:9] op_sel_hi:[1,0]
	v_pk_mul_f32 v[14:15], v[40:41], v[52:53]
	v_pk_add_f32 v[10:11], v[10:11], 1.0 op_sel_hi:[1,0]
	v_exp_f32_e32 v12, v12
	v_rcp_f32_e32 v10, v10
	v_rcp_f32_e32 v11, v11
	v_exp_f32_e32 v13, v13
	v_pk_mul_f32 v[14:15], v[14:15], v[6:7] op_sel_hi:[1,0]
	v_pk_mul_f32 v[16:17], v[38:39], v[50:51]
	v_pk_mul_f32 v[10:11], v[14:15], v[10:11]
	v_pk_mul_f32 v[14:15], v[36:37], v[8:9] op_sel_hi:[1,0]
	v_pk_mul_f32 v[8:9], v[34:35], v[8:9] op_sel_hi:[1,0]
	v_exp_f32_e32 v14, v14
	v_exp_f32_e32 v8, v8
	v_exp_f32_e32 v15, v15
	v_exp_f32_e32 v9, v9
	v_pk_add_f32 v[12:13], v[12:13], 1.0 op_sel_hi:[1,0]
	v_pk_mul_f32 v[16:17], v[16:17], v[6:7] op_sel_hi:[1,0]
	v_rcp_f32_e32 v12, v12
	v_rcp_f32_e32 v13, v13
	v_pk_add_f32 v[14:15], v[14:15], 1.0 op_sel_hi:[1,0]
	v_pk_add_f32 v[8:9], v[8:9], 1.0 op_sel_hi:[1,0]
	v_rcp_f32_e32 v14, v14
	v_rcp_f32_e32 v8, v8
	v_rcp_f32_e32 v15, v15
	v_rcp_f32_e32 v9, v9
	v_pk_mul_f32 v[12:13], v[16:17], v[12:13]
	v_pk_mul_f32 v[16:17], v[36:37], v[44:45]
	v_pk_mul_f32 v[18:19], v[34:35], v[42:43]
	v_med3_f32 v5, v12, s63, v191
	v_pk_mul_f32 v[18:19], v[18:19], v[6:7] op_sel_hi:[1,0]
	v_pk_mul_f32 v[6:7], v[16:17], v[6:7] op_sel_hi:[1,0]
	v_pk_mul_f32 v[8:9], v[18:19], v[8:9]
	v_pk_mul_f32 v[6:7], v[6:7], v[14:15]
	v_add_u32_e32 v14, 0xb0, v4
	v_med3_f32 v12, v13, s63, v191
	v_mov_b32_e32 v4, 0
	v_cvt_pk_fp8_f32 v4, v5, v12
	v_med3_f32 v8, v8, s63, v191
	v_med3_f32 v9, v9, s63, v191
	v_mov_b32_e32 v5, 0
	v_cvt_pk_fp8_f32 v5, v8, v9
	v_med3_f32 v10, v10, s63, v191
	v_med3_f32 v11, v11, s63, v191
	v_med3_f32 v6, v6, s63, v191
	v_med3_f32 v7, v7, s63, v191
	v_cvt_pk_fp8_f32 v4, v10, v11 op_sel:[0,0,1]
	v_cvt_pk_fp8_f32 v5, v6, v7 op_sel:[0,0,1]
	v_mad_i64_i32 v[2:3], s[34:35], v14, s64, v[2:3]
	v_lshl_add_u64 v[0:1], v[2:3], 0, v[0:1]
	s_mov_b64 s[2:3], -1
	global_store_dwordx2 v[0:1], v[4:5], off
	s_cbranch_vccnz .LBB0_588
	s_andn2_b64 vcc, exec, s[8:9]
	s_cbranch_vccnz .LBB0_587
	s_barrier
	s_branch .LBB0_587

.LBB0_661:
	v_ashrrev_i32_e32 v0, 31, v9
	v_lshrrev_b32_e32 v0, 26, v0
	v_add_u32_e32 v0, v9, v0
	v_ashrrev_i32_e32 v10, 6, v0
	v_bfe_i32 v0, v9, 27, 1
	s_waitcnt lgkmcnt(0)
	v_lshlrev_b32_e32 v1, 4, v9
	v_lshrrev_b32_e32 v0, 22, v0
	v_add_u32_e32 v0, v1, v0
	v_and_b32_e32 v0, 0xfffffc00, v0
	v_sub_u32_e32 v0, v1, v0
	v_lshrrev_b32_e32 v2, 4, v0
	v_bitop3_b32 v2, v2, v0, 32 bitop3:0x6c
	v_ashrrev_i32_e32 v0, 31, v0
	v_lshrrev_b32_e32 v0, 26, v0
	v_add_u32_e32 v0, v2, v0
	v_ashrrev_i32_e32 v11, 6, v0
	v_lshlrev_b32_e32 v3, 3, v10
	v_mul_i32_i24_e32 v4, 64, v11
	v_and_b32_e32 v3, -16, v3
	v_sub_u32_e32 v2, v2, v4
	v_mov_b32_e32 v4, 1
	v_add_u32_e32 v3, v11, v3
	v_ashrrev_i16_sdwa v2, v4, sext(v2) dst_sel:DWORD dst_unused:UNUSED_PAD src0_sel:DWORD src1_sel:BYTE_0
	v_lshlrev_b32_e32 v0, 5, v10
	v_bfe_i32 v12, v2, 0, 16
	v_lshlrev_b32_e32 v2, 1, v3
	v_lshrrev_b32_e32 v5, 2, v3
	v_and_b32_e32 v6, 3, v11
	s_mov_b32 s5, 0xffffe0
	v_and_b32_e32 v0, 32, v0
	v_and_b32_e32 v2, 24, v2
	v_and_b32_e32 v5, 4, v5
	v_and_or_b32 v6, v3, s5, v6
	v_or3_b32 v2, v6, v5, v2
	v_add_lshl_u32 v0, v0, v12, 1
	s_movk_i32 s0, 0xb00
	v_mad_u64_u32 v[32:33], s[10:11], v3, s0, v[0:1]
	v_mad_u32_u24 v162, v2, s0, v0
	v_add_u32_e32 v0, 0x2000, v1
	v_ashrrev_i32_e32 v1, 31, v0
	v_lshrrev_b32_e32 v1, 22, v1
	v_add_u32_e32 v1, v0, v1
	v_ashrrev_i32_e32 v13, 10, v1
	v_mul_i32_i24_e32 v1, 0x400, v13
	v_sub_u32_e32 v0, v0, v1
	v_lshrrev_b32_e32 v1, 4, v0
	v_bitop3_b32 v0, v1, v0, 32 bitop3:0x6c
	v_ashrrev_i32_e32 v2, 31, v0
	v_lshrrev_b32_e32 v2, 26, v2
	s_ashr_i32 s1, s3, 3
	v_add_u32_e32 v2, v0, v2
	s_add_u32 s42, s54, 0x1e200000
	v_lshlrev_b32_e32 v1, 3, v13
	v_ashrrev_i32_e32 v14, 6, v2
	v_and_b32_e32 v2, 0xc0, v2
	s_addc_u32 s43, s55, 0
	v_and_b32_e32 v1, -16, v1
	v_sub_u32_e32 v0, v0, v2
	s_add_u32 s46, s54, 0x2d00000
	v_add_u32_e32 v1, v14, v1
	v_ashrrev_i16_sdwa v0, v4, sext(v0) dst_sel:DWORD dst_unused:UNUSED_PAD src0_sel:DWORD src1_sel:BYTE_0
	s_addc_u32 s47, s55, 0
	v_lshlrev_b32_e32 v3, 5, v13
	v_bfe_i32 v15, v0, 0, 16
	v_lshlrev_b32_e32 v0, 1, v1
	v_lshrrev_b32_e32 v2, 2, v1
	v_and_b32_e32 v4, 3, v14
	s_add_i32 s1, s4, s1
	v_and_b32_e32 v3, 32, v3
	v_and_b32_e32 v0, 24, v0
	v_and_b32_e32 v2, 4, v2
	v_and_or_b32 v4, v1, s5, v4
	s_ashr_i32 s4, s1, 31
	v_or3_b32 v2, v4, v2, v0
	v_add_lshl_u32 v0, v3, v15, 1
	s_lshr_b32 s4, s4, 27
	v_mad_u64_u32 v[164:165], s[10:11], v1, s0, v[0:1]
	s_add_i32 s4, s1, s4
	s_ashr_i32 s10, s4, 5
	s_andn2_b32 s4, s4, 31
	s_sub_i32 s1, s1, s4
	s_bfe_i32 s4, s1, 0x80000
	s_bfe_u32 s4, s4, 0x3000c
	s_add_i32 s11, s1, s4
	s_bfe_i32 s4, s11, 0x80000
	s_and_b32 s11, s11, 0xf8
	s_sub_i32 s1, s1, s11
	s_lshl_b32 s10, s10, 3
	s_sext_i32_i16 s12, s4
	s_sext_i32_i8 s1, s1
	s_ashr_i32 s5, s2, 6
	s_add_i32 s65, s10, s1
	s_ashr_i32 s10, s12, 3
	s_ashr_i32 s3, s2, 8
	s_lshl_b32 s48, s5, 10
	s_lshr_b32 s4, s12, 3
	s_mul_hi_i32 s11, s10, 0xb0000
	s_mul_i32 s10, s10, 0xb0000
	s_add_u32 s28, s46, s10
	s_addc_u32 s29, s47, s11
	s_add_i32 s49, s48, 0
	s_add_i32 m0, s49, 0x10000
	v_mad_u32_u24 v166, v2, s0, v0
	global_load_lds_dwordx4 v162, s[28:29]
	s_add_i32 m0, s49, 0x12000
	s_add_u32 s10, s28, 0x58000
	global_load_lds_dwordx4 v166, s[28:29]
	s_addc_u32 s11, s29, 0
	s_add_i32 m0, s49, 0x14000
	s_mul_i32 s13, s65, 0xb0000
	global_load_lds_dwordx4 v162, s[10:11]
	s_add_i32 m0, s49, 0x16000
	s_mul_hi_i32 s1, s65, 0xb0000
	s_add_u32 s40, s42, s13
	s_addc_u32 s41, s43, s1
	s_add_i32 s50, s49, 0x2000
	global_load_lds_dwordx4 v166, s[10:11]
	s_mov_b32 m0, s49
	s_add_u32 s10, s40, 0x58000
	global_load_lds_dwordx4 v32, s[40:41]
	s_mov_b32 m0, s50
	s_addc_u32 s11, s41, 0
	s_add_i32 s51, s49, 0x4000
	global_load_lds_dwordx4 v164, s[40:41]
	s_mov_b32 m0, s51
	s_add_i32 s56, s49, 0x6000
	global_load_lds_dwordx4 v32, s[10:11]
	s_mov_b32 m0, s56
	v_mov_b32_e32 v163, 0
	global_load_lds_dwordx4 v164, s[10:11]
	v_mov_b32_e32 v167, v163
	v_mov_b32_e32 v33, v163
	v_mov_b32_e32 v165, v163
	s_cmp_eq_u32 s3, 1
	s_mov_b32 s1, 0
	v_lshl_add_u64 v[6:7], s[28:29], 0, v[162:163]
	v_lshl_add_u64 v[4:5], s[28:29], 0, v[166:167]
	v_lshl_add_u64 v[0:1], s[40:41], 0, v[32:33]
	s_cselect_b64 s[10:11], -1, 0
	s_cmp_lg_u32 s3, 1
	v_lshl_add_u64 v[2:3], s[40:41], 0, v[164:165]
	s_cbranch_scc1 .LBB0_663
	s_barrier

.LBB0_672:
	s_mul_i32 s34, s64, 0xb0000
	s_mul_hi_i32 s0, s64, 0xb0000
	s_add_u32 s34, s42, s34
	s_addc_u32 s35, s43, s0
	s_mul_i32 s36, s63, 0xb0000
	s_mul_hi_i32 s0, s63, 0xb0000
	s_add_u32 s38, s46, s36
	v_mov_b32_e32 v66, 0
	s_addc_u32 s39, s47, s0
	v_lshl_add_u64 v[178:179], s[40:41], 0, v[170:171]
	v_lshl_add_u64 v[180:181], s[40:41], 0, v[172:173]
	s_mov_b32 s67, 0
	v_mov_b32_e32 v67, v66
	v_mov_b32_e32 v68, v66
	v_mov_b32_e32 v69, v66
	v_mov_b32_e32 v70, v66
	v_mov_b32_e32 v71, v66
	v_mov_b32_e32 v72, v66
	v_mov_b32_e32 v73, v66
	v_mov_b32_e32 v82, v66
	v_mov_b32_e32 v83, v66
	v_mov_b32_e32 v84, v66
	v_mov_b32_e32 v85, v66
	v_mov_b32_e32 v86, v66
	v_mov_b32_e32 v87, v66
	v_mov_b32_e32 v88, v66
	v_mov_b32_e32 v89, v66
	v_mov_b32_e32 v34, v66
	v_mov_b32_e32 v35, v66
	v_mov_b32_e32 v36, v66
	v_mov_b32_e32 v37, v66
	v_mov_b32_e32 v38, v66
	v_mov_b32_e32 v39, v66
	v_mov_b32_e32 v40, v66
	v_mov_b32_e32 v41, v66
	v_mov_b32_e32 v50, v66
	v_mov_b32_e32 v51, v66
	v_mov_b32_e32 v52, v66
	v_mov_b32_e32 v53, v66
	v_mov_b32_e32 v58, v66
	v_mov_b32_e32 v59, v66
	v_mov_b32_e32 v60, v66
	v_mov_b32_e32 v61, v66
	v_mov_b32_e32 v74, v66
	v_mov_b32_e32 v75, v66
	v_mov_b32_e32 v76, v66
	v_mov_b32_e32 v77, v66
	v_mov_b32_e32 v78, v66
	v_mov_b32_e32 v79, v66
	v_mov_b32_e32 v80, v66
	v_mov_b32_e32 v81, v66
	v_mov_b32_e32 v90, v66
	v_mov_b32_e32 v91, v66
	v_mov_b32_e32 v92, v66
	v_mov_b32_e32 v93, v66
	v_mov_b32_e32 v94, v66
	v_mov_b32_e32 v95, v66
	v_mov_b32_e32 v96, v66
	v_mov_b32_e32 v97, v66
	v_mov_b32_e32 v98, v66
	v_mov_b32_e32 v99, v66
	v_mov_b32_e32 v100, v66
	v_mov_b32_e32 v101, v66
	v_mov_b32_e32 v102, v66
	v_mov_b32_e32 v103, v66
	v_mov_b32_e32 v104, v66
	v_mov_b32_e32 v105, v66
	v_mov_b32_e32 v114, v66
	v_mov_b32_e32 v115, v66
	v_mov_b32_e32 v116, v66
	v_mov_b32_e32 v117, v66
	v_mov_b32_e32 v118, v66
	v_mov_b32_e32 v119, v66
	v_mov_b32_e32 v120, v66
	v_mov_b32_e32 v121, v66
	v_mov_b32_e32 v130, v66
	v_mov_b32_e32 v131, v66
	v_mov_b32_e32 v132, v66
	v_mov_b32_e32 v133, v66
	v_mov_b32_e32 v134, v66
	v_mov_b32_e32 v135, v66
	v_mov_b32_e32 v136, v66
	v_mov_b32_e32 v137, v66
	v_mov_b32_e32 v146, v66
	v_mov_b32_e32 v147, v66
	v_mov_b32_e32 v148, v66
	v_mov_b32_e32 v149, v66
	v_mov_b32_e32 v150, v66
	v_mov_b32_e32 v151, v66
	v_mov_b32_e32 v152, v66
	v_mov_b32_e32 v153, v66
	v_mov_b32_e32 v106, v66
	v_mov_b32_e32 v107, v66
	v_mov_b32_e32 v108, v66
	v_mov_b32_e32 v109, v66
	v_mov_b32_e32 v110, v66
	v_mov_b32_e32 v111, v66
	v_mov_b32_e32 v112, v66
	v_mov_b32_e32 v113, v66
	v_mov_b32_e32 v122, v66
	v_mov_b32_e32 v123, v66
	v_mov_b32_e32 v124, v66
	v_mov_b32_e32 v125, v66
	v_mov_b32_e32 v126, v66
	v_mov_b32_e32 v127, v66
	v_mov_b32_e32 v128, v66
	v_mov_b32_e32 v129, v66
	v_mov_b32_e32 v138, v66
	v_mov_b32_e32 v139, v66
	v_mov_b32_e32 v140, v66
	v_mov_b32_e32 v141, v66
	v_mov_b32_e32 v142, v66
	v_mov_b32_e32 v143, v66
	v_mov_b32_e32 v144, v66
	v_mov_b32_e32 v145, v66
	v_mov_b32_e32 v154, v66
	v_mov_b32_e32 v155, v66
	v_mov_b32_e32 v156, v66
	v_mov_b32_e32 v157, v66
	v_mov_b32_e32 v158, v66
	v_mov_b32_e32 v159, v66
	v_mov_b32_e32 v160, v66
	v_mov_b32_e32 v161, v66
	v_mov_b32_e32 v62, v66
	v_mov_b32_e32 v63, v66
	v_mov_b32_e32 v64, v66
	v_mov_b32_e32 v65, v66
	v_mov_b32_e32 v54, v66
	v_mov_b32_e32 v55, v66
	v_mov_b32_e32 v56, v66
	v_mov_b32_e32 v57, v66
	v_mov_b32_e32 v46, v66
	v_mov_b32_e32 v47, v66
	v_mov_b32_e32 v48, v66
	v_mov_b32_e32 v49, v66
	v_mov_b32_e32 v42, v66
	v_mov_b32_e32 v43, v66
	v_mov_b32_e32 v44, v66
	v_mov_b32_e32 v45, v66
.LBB0_673:
	ds_read_b128 v[24:27], v187
	ds_read_b128 v[28:31], v187 offset:1024
	ds_read_b128 v[16:19], v187 offset:2048
	ds_read_b128 v[20:23], v187 offset:3072
	s_waitcnt lgkmcnt(0)
	ds_read_b128 v[8:11], v188
	ds_read_b128 v[12:15], v188 offset:1024
	ds_read_b128 v[0:3], v188 offset:2048
	ds_read_b128 v[4:7], v188 offset:3072
	s_add_i32 m0, s49, 0xc000
	ds_read_b128 v[192:195], v189
	ds_read_b128 v[196:199], v189 offset:1024
	ds_read_b128 v[200:203], v189 offset:2048
	ds_read_b128 v[204:207], v189 offset:3072
	ds_read_b128 v[208:211], v189 offset:4096
	ds_read_b128 v[212:215], v189 offset:5120
	ds_read_b128 v[224:227], v189 offset:6144
	ds_read_b128 v[228:231], v189 offset:7168
	global_load_lds_dwordx4 v[178:179], off
	s_add_i32 m0, s49, 0xe000
	s_nop 0
	global_load_lds_dwordx4 v[180:181], off
	s_waitcnt vmcnt(8)
	s_waitcnt lgkmcnt(0)
	s_barrier
	s_setprio 1
	s_waitcnt lgkmcnt(0)
	v_mfma_scale_f32_16x16x128_f8f6f4 v[158:161], v[24:31], v[192:199], v[158:161], v190, v190 op_sel_hi:[0,0,0]
	v_mfma_scale_f32_16x16x128_f8f6f4 v[154:157], v[16:23], v[192:199], v[154:157], v190, v190 op_sel_hi:[0,0,0]
	v_mfma_scale_f32_16x16x128_f8f6f4 v[142:145], v[24:31], v[200:207], v[142:145], v190, v190 op_sel_hi:[0,0,0]
	v_mfma_scale_f32_16x16x128_f8f6f4 v[138:141], v[16:23], v[200:207], v[138:141], v190, v190 op_sel_hi:[0,0,0]
	v_mfma_scale_f32_16x16x128_f8f6f4 v[126:129], v[24:31], v[208:215], v[126:129], v190, v190 op_sel_hi:[0,0,0]
	v_mfma_scale_f32_16x16x128_f8f6f4 v[122:125], v[16:23], v[208:215], v[122:125], v190, v190 op_sel_hi:[0,0,0]
	v_mfma_scale_f32_16x16x128_f8f6f4 v[110:113], v[24:31], v[224:231], v[110:113], v190, v190 op_sel_hi:[0,0,0]
	v_mfma_scale_f32_16x16x128_f8f6f4 v[106:109], v[16:23], v[224:231], v[106:109], v190, v190 op_sel_hi:[0,0,0]
	s_setprio 0
	s_setprio 1
	v_mfma_scale_f32_16x16x128_f8f6f4 v[150:153], v[8:15], v[192:199], v[150:153], v190, v190 op_sel_hi:[0,0,0]
	v_mfma_scale_f32_16x16x128_f8f6f4 v[146:149], v[0:7], v[192:199], v[146:149], v190, v190 op_sel_hi:[0,0,0]
	v_mfma_scale_f32_16x16x128_f8f6f4 v[134:137], v[8:15], v[200:207], v[134:137], v190, v190 op_sel_hi:[0,0,0]
	v_mfma_scale_f32_16x16x128_f8f6f4 v[130:133], v[0:7], v[200:207], v[130:133], v190, v190 op_sel_hi:[0,0,0]
	v_mfma_scale_f32_16x16x128_f8f6f4 v[118:121], v[8:15], v[208:215], v[118:121], v190, v190 op_sel_hi:[0,0,0]
	v_mfma_scale_f32_16x16x128_f8f6f4 v[114:117], v[0:7], v[208:215], v[114:117], v190, v190 op_sel_hi:[0,0,0]
	v_mfma_scale_f32_16x16x128_f8f6f4 v[102:105], v[8:15], v[224:231], v[102:105], v190, v190 op_sel_hi:[0,0,0]
	v_mfma_scale_f32_16x16x128_f8f6f4 v[98:101], v[0:7], v[224:231], v[98:101], v190, v190 op_sel_hi:[0,0,0]
	s_setprio 0
	s_barrier
	s_add_i32 s73, s67, 2
	s_cmp_lt_u32 s67, 20
	s_cselect_b64 s[36:37], -1, 0
	s_and_b64 s[74:75], s[36:37], exec
	s_cselect_b32 s0, 0, 0xffffffea
	s_cselect_b32 s77, s29, s39
	s_cselect_b32 s76, s28, s38
	s_add_i32 s0, s73, s0
	s_lshl_b64 s[74:75], s[0:1], 7
	s_add_u32 s76, s76, s74
	s_addc_u32 s77, s77, s75
	s_add_i32 s0, s60, s48
	v_lshl_add_u64 v[216:217], s[76:77], 0, v[162:163]
	s_mov_b32 m0, s0
	ds_read_b128 v[192:195], v189 offset:16384
	ds_read_b128 v[196:199], v189 offset:17408
	ds_read_b128 v[200:203], v189 offset:18432
	ds_read_b128 v[204:207], v189 offset:19456
	ds_read_b128 v[208:211], v189 offset:20480
	ds_read_b128 v[212:215], v189 offset:21504
	ds_read_b128 v[224:227], v189 offset:22528
	ds_read_b128 v[228:231], v189 offset:23552
	global_load_lds_dwordx4 v[216:217], off
	s_add_i32 m0, s0, 0x2000
	v_lshl_add_u64 v[216:217], s[76:77], 0, v[166:167]
	s_add_u32 s76, s76, 0x58000
	s_addc_u32 s77, s77, 0
	s_add_i32 s0, s61, s48
	global_load_lds_dwordx4 v[216:217], off
	v_lshl_add_u64 v[216:217], s[76:77], 0, v[162:163]
	s_mov_b32 m0, s0
	s_nop 0
	global_load_lds_dwordx4 v[216:217], off
	s_add_i32 m0, s0, 0x2000
	s_and_b64 vcc, s[36:37], exec
	s_cselect_b32 s36, s40, s34
	s_cselect_b32 s0, s41, s35
	s_add_u32 s36, s36, s74
	v_lshl_add_u64 v[216:217], s[76:77], 0, v[166:167]
	s_addc_u32 s37, s0, s75
	global_load_lds_dwordx4 v[216:217], off
	v_lshl_add_u64 v[216:217], s[36:37], 0, v[32:33]
	s_mov_b32 m0, s49
	s_nop 0
	global_load_lds_dwordx4 v[216:217], off
	v_lshl_add_u64 v[216:217], s[36:37], 0, v[164:165]
	s_mov_b32 m0, s50
	s_nop 0
	global_load_lds_dwordx4 v[216:217], off
	s_waitcnt vmcnt(8)
	s_waitcnt lgkmcnt(0)
	s_barrier
	s_setprio 1
	s_waitcnt lgkmcnt(0)
	v_mfma_scale_f32_16x16x128_f8f6f4 v[94:97], v[24:31], v[192:199], v[94:97], v190, v190 op_sel_hi:[0,0,0]
	v_mfma_scale_f32_16x16x128_f8f6f4 v[90:93], v[16:23], v[192:199], v[90:93], v190, v190 op_sel_hi:[0,0,0]
	v_mfma_scale_f32_16x16x128_f8f6f4 v[78:81], v[24:31], v[200:207], v[78:81], v190, v190 op_sel_hi:[0,0,0]
	v_mfma_scale_f32_16x16x128_f8f6f4 v[74:77], v[16:23], v[200:207], v[74:77], v190, v190 op_sel_hi:[0,0,0]
	v_mfma_scale_f32_16x16x128_f8f6f4 v[58:61], v[24:31], v[208:215], v[58:61], v190, v190 op_sel_hi:[0,0,0]
	v_mfma_scale_f32_16x16x128_f8f6f4 v[50:53], v[16:23], v[208:215], v[50:53], v190, v190 op_sel_hi:[0,0,0]
	v_mfma_scale_f32_16x16x128_f8f6f4 v[38:41], v[24:31], v[224:231], v[38:41], v190, v190 op_sel_hi:[0,0,0]
	v_mfma_scale_f32_16x16x128_f8f6f4 v[34:37], v[16:23], v[224:231], v[34:37], v190, v190 op_sel_hi:[0,0,0]
	s_setprio 0
	s_setprio 1
	v_mfma_scale_f32_16x16x128_f8f6f4 v[86:89], v[8:15], v[192:199], v[86:89], v190, v190 op_sel_hi:[0,0,0]
	v_mfma_scale_f32_16x16x128_f8f6f4 v[82:85], v[0:7], v[192:199], v[82:85], v190, v190 op_sel_hi:[0,0,0]
	v_mfma_scale_f32_16x16x128_f8f6f4 v[70:73], v[8:15], v[200:207], v[70:73], v190, v190 op_sel_hi:[0,0,0]
	v_mfma_scale_f32_16x16x128_f8f6f4 v[66:69], v[0:7], v[200:207], v[66:69], v190, v190 op_sel_hi:[0,0,0]
	v_mfma_scale_f32_16x16x128_f8f6f4 v[62:65], v[8:15], v[208:215], v[62:65], v190, v190 op_sel_hi:[0,0,0]
	v_mfma_scale_f32_16x16x128_f8f6f4 v[54:57], v[0:7], v[208:215], v[54:57], v190, v190 op_sel_hi:[0,0,0]
	v_mfma_scale_f32_16x16x128_f8f6f4 v[46:49], v[8:15], v[224:231], v[46:49], v190, v190 op_sel_hi:[0,0,0]
	v_mfma_scale_f32_16x16x128_f8f6f4 v[42:45], v[0:7], v[224:231], v[42:45], v190, v190 op_sel_hi:[0,0,0]
	s_setprio 0
	s_barrier
	s_add_i32 s78, 0, 0x18000
	s_add_i32 s79, 0, 0x1c000
	v_add_u32_e32 v0, s78, v183
	v_add_u32_e32 v4, s79, v183
	ds_read_b128 v[24:27], v0
	ds_read_b128 v[28:31], v0 offset:1024
	ds_read_b128 v[16:19], v0 offset:2048
	ds_read_b128 v[20:23], v0 offset:3072
	ds_read_b128 v[8:11], v4
	ds_read_b128 v[12:15], v4 offset:1024
	ds_read_b128 v[0:3], v4 offset:2048
	ds_read_b128 v[4:7], v4 offset:3072
	s_add_u32 s36, s36, 0x58000
	s_addc_u32 s37, s37, 0
	s_mov_b32 m0, s51
	v_lshl_add_u64 v[216:217], s[36:37], 0, v[32:33]
	ds_read_b128 v[192:195], v189 offset:32768
	ds_read_b128 v[196:199], v189 offset:33792
	ds_read_b128 v[200:203], v189 offset:34816
	ds_read_b128 v[204:207], v189 offset:35840
	ds_read_b128 v[208:211], v189 offset:36864
	ds_read_b128 v[212:215], v189 offset:37888
	ds_read_b128 v[224:227], v189 offset:38912
	ds_read_b128 v[228:231], v189 offset:39936
	global_load_lds_dwordx4 v[216:217], off
	v_lshl_add_u64 v[216:217], s[36:37], 0, v[164:165]
	s_mov_b32 m0, s56
	s_nop 0
	global_load_lds_dwordx4 v[216:217], off
	s_waitcnt vmcnt(8)
	s_waitcnt lgkmcnt(0)
	s_barrier
	s_setprio 1
	s_waitcnt lgkmcnt(0)
	v_mfma_scale_f32_16x16x128_f8f6f4 v[158:161], v[24:31], v[192:199], v[158:161], v190, v190 op_sel_hi:[0,0,0]
	v_mfma_scale_f32_16x16x128_f8f6f4 v[154:157], v[16:23], v[192:199], v[154:157], v190, v190 op_sel_hi:[0,0,0]
	v_mfma_scale_f32_16x16x128_f8f6f4 v[142:145], v[24:31], v[200:207], v[142:145], v190, v190 op_sel_hi:[0,0,0]
	v_mfma_scale_f32_16x16x128_f8f6f4 v[138:141], v[16:23], v[200:207], v[138:141], v190, v190 op_sel_hi:[0,0,0]
	v_mfma_scale_f32_16x16x128_f8f6f4 v[126:129], v[24:31], v[208:215], v[126:129], v190, v190 op_sel_hi:[0,0,0]
	v_mfma_scale_f32_16x16x128_f8f6f4 v[122:125], v[16:23], v[208:215], v[122:125], v190, v190 op_sel_hi:[0,0,0]
	v_mfma_scale_f32_16x16x128_f8f6f4 v[110:113], v[24:31], v[224:231], v[110:113], v190, v190 op_sel_hi:[0,0,0]
	v_mfma_scale_f32_16x16x128_f8f6f4 v[106:109], v[16:23], v[224:231], v[106:109], v190, v190 op_sel_hi:[0,0,0]
	s_setprio 0
	s_setprio 1
	v_mfma_scale_f32_16x16x128_f8f6f4 v[150:153], v[8:15], v[192:199], v[150:153], v190, v190 op_sel_hi:[0,0,0]
	v_mfma_scale_f32_16x16x128_f8f6f4 v[146:149], v[0:7], v[192:199], v[146:149], v190, v190 op_sel_hi:[0,0,0]
	v_mfma_scale_f32_16x16x128_f8f6f4 v[134:137], v[8:15], v[200:207], v[134:137], v190, v190 op_sel_hi:[0,0,0]
	v_mfma_scale_f32_16x16x128_f8f6f4 v[130:133], v[0:7], v[200:207], v[130:133], v190, v190 op_sel_hi:[0,0,0]
	v_mfma_scale_f32_16x16x128_f8f6f4 v[118:121], v[8:15], v[208:215], v[118:121], v190, v190 op_sel_hi:[0,0,0]
	v_mfma_scale_f32_16x16x128_f8f6f4 v[114:117], v[0:7], v[208:215], v[114:117], v190, v190 op_sel_hi:[0,0,0]
	v_mfma_scale_f32_16x16x128_f8f6f4 v[102:105], v[8:15], v[224:231], v[102:105], v190, v190 op_sel_hi:[0,0,0]
	v_mfma_scale_f32_16x16x128_f8f6f4 v[98:101], v[0:7], v[224:231], v[98:101], v190, v190 op_sel_hi:[0,0,0]
	s_setprio 0
	s_barrier
	s_cmp_lt_u32 s67, 19
	s_cselect_b64 s[36:37], -1, 0
	s_and_b64 s[74:75], s[36:37], exec
	s_cselect_b32 s0, 0, 0xffffffea
	s_cselect_b32 s77, s29, s39
	s_cselect_b32 s76, s28, s38
	s_add_i32 s0, s0, s67
	s_add_i32 s0, s0, 3
	s_lshl_b64 s[74:75], s[0:1], 7
	s_add_u32 s76, s76, s74
	s_addc_u32 s77, s77, s75
	s_add_i32 s0, s78, s48
	v_lshl_add_u64 v[216:217], s[76:77], 0, v[162:163]
	s_mov_b32 m0, s0
	ds_read_b128 v[192:195], v189 offset:49152
	ds_read_b128 v[196:199], v189 offset:50176
	ds_read_b128 v[200:203], v189 offset:51200
	ds_read_b128 v[204:207], v189 offset:52224
	ds_read_b128 v[208:211], v189 offset:53248
	ds_read_b128 v[212:215], v189 offset:54272
	ds_read_b128 v[224:227], v189 offset:55296
	ds_read_b128 v[228:231], v189 offset:56320
	global_load_lds_dwordx4 v[216:217], off
	s_add_i32 m0, s0, 0x2000
	v_lshl_add_u64 v[216:217], s[76:77], 0, v[166:167]
	s_add_u32 s76, s76, 0x58000
	s_addc_u32 s77, s77, 0
	s_add_i32 s0, s79, s48
	global_load_lds_dwordx4 v[216:217], off
	v_lshl_add_u64 v[216:217], s[76:77], 0, v[162:163]
	s_mov_b32 m0, s0
	s_nop 0
	global_load_lds_dwordx4 v[216:217], off
	s_add_i32 m0, s0, 0x2000
	s_and_b64 s[36:37], s[36:37], exec
	s_cselect_b32 s36, s40, s34
	s_cselect_b32 s0, s41, s35
	s_add_u32 s36, s36, s74
	v_lshl_add_u64 v[216:217], s[76:77], 0, v[166:167]
	s_addc_u32 s37, s0, s75
	global_load_lds_dwordx4 v[216:217], off
	v_lshl_add_u64 v[216:217], s[36:37], 0, v[32:33]
	s_mov_b32 m0, s57
	s_nop 0
	global_load_lds_dwordx4 v[216:217], off
	v_lshl_add_u64 v[216:217], s[36:37], 0, v[164:165]
	s_mov_b32 m0, s58
	s_nop 0
	global_load_lds_dwordx4 v[216:217], off
	s_waitcnt vmcnt(8)
	s_waitcnt lgkmcnt(0)
	s_barrier
	s_setprio 1
	s_waitcnt lgkmcnt(0)
	v_mfma_scale_f32_16x16x128_f8f6f4 v[94:97], v[24:31], v[192:199], v[94:97], v190, v190 op_sel_hi:[0,0,0]
	v_mfma_scale_f32_16x16x128_f8f6f4 v[90:93], v[16:23], v[192:199], v[90:93], v190, v190 op_sel_hi:[0,0,0]
	v_mfma_scale_f32_16x16x128_f8f6f4 v[78:81], v[24:31], v[200:207], v[78:81], v190, v190 op_sel_hi:[0,0,0]
	v_mfma_scale_f32_16x16x128_f8f6f4 v[74:77], v[16:23], v[200:207], v[74:77], v190, v190 op_sel_hi:[0,0,0]
	v_mfma_scale_f32_16x16x128_f8f6f4 v[58:61], v[24:31], v[208:215], v[58:61], v190, v190 op_sel_hi:[0,0,0]
	v_mfma_scale_f32_16x16x128_f8f6f4 v[50:53], v[16:23], v[208:215], v[50:53], v190, v190 op_sel_hi:[0,0,0]
	v_mfma_scale_f32_16x16x128_f8f6f4 v[38:41], v[24:31], v[224:231], v[38:41], v190, v190 op_sel_hi:[0,0,0]
	v_mfma_scale_f32_16x16x128_f8f6f4 v[34:37], v[16:23], v[224:231], v[34:37], v190, v190 op_sel_hi:[0,0,0]
	s_setprio 0
	s_setprio 1
	v_mfma_scale_f32_16x16x128_f8f6f4 v[86:89], v[8:15], v[192:199], v[86:89], v190, v190 op_sel_hi:[0,0,0]
	v_mfma_scale_f32_16x16x128_f8f6f4 v[82:85], v[0:7], v[192:199], v[82:85], v190, v190 op_sel_hi:[0,0,0]
	v_mfma_scale_f32_16x16x128_f8f6f4 v[70:73], v[8:15], v[200:207], v[70:73], v190, v190 op_sel_hi:[0,0,0]
	v_mfma_scale_f32_16x16x128_f8f6f4 v[66:69], v[0:7], v[200:207], v[66:69], v190, v190 op_sel_hi:[0,0,0]
	v_mfma_scale_f32_16x16x128_f8f6f4 v[62:65], v[8:15], v[208:215], v[62:65], v190, v190 op_sel_hi:[0,0,0]
	v_mfma_scale_f32_16x16x128_f8f6f4 v[54:57], v[0:7], v[208:215], v[54:57], v190, v190 op_sel_hi:[0,0,0]
	v_mfma_scale_f32_16x16x128_f8f6f4 v[46:49], v[8:15], v[224:231], v[46:49], v190, v190 op_sel_hi:[0,0,0]
	v_mfma_scale_f32_16x16x128_f8f6f4 v[42:45], v[0:7], v[224:231], v[42:45], v190, v190 op_sel_hi:[0,0,0]
	s_setprio 0
	s_barrier
	v_lshl_add_u64 v[178:179], v[178:179], 0, s[26:27]
	v_lshl_add_u64 v[180:181], v[180:181], 0, s[26:27]
	s_mov_b32 s67, s73
	s_cbranch_vccnz .LBB0_673
	s_andn2_b64 vcc, exec, s[22:23]
	s_cbranch_vccnz .LBB0_676
	s_barrier
.LBB0_676:
	s_lshl_b32 s28, s65, 8
	v_lshl_or_b32 v20, s66, 8, v186
	v_add_u32_e32 v24, s28, v182
	v_ashrrev_i32_e32 v21, 31, v20
	v_ashrrev_i32_e32 v25, 31, v24
	v_lshl_add_u64 v[22:23], v[20:21], 1, s[12:13]
	v_lshlrev_b64 v[0:1], 11, v[24:25]
	s_nop 15
	s_nop 7
	v_lshl_add_u64 v[0:1], v[22:23], 0, v[0:1]
	global_load_dwordx4 v[26:29], v[0:1], off
	global_load_dwordx4 v[178:181], v[0:1], off offset:256
	v_or_b32_e32 v200, 16, v24
	v_or_b32_e32 v18, 32, v24
	v_or_b32_e32 v16, 48, v24
	v_ashrrev_i32_e32 v201, 31, v200
	v_ashrrev_i32_e32 v19, 31, v18
	v_ashrrev_i32_e32 v17, 31, v16
	v_lshlrev_b64 v[0:1], 10, v[24:25]
	v_lshlrev_b64 v[2:3], 11, v[200:201]
	v_lshlrev_b64 v[4:5], 11, v[18:19]
	v_lshlrev_b64 v[6:7], 11, v[16:17]
	v_lshl_add_u64 v[0:1], v[0:1], 0, v[20:21]
	v_lshl_add_u64 v[2:3], v[22:23], 0, v[2:3]
	v_lshl_add_u64 v[4:5], v[22:23], 0, v[4:5]
	v_lshl_add_u64 v[202:203], v[22:23], 0, v[6:7]
	v_lshl_add_u64 v[204:205], v[0:1], 1, s[14:15]
	v_lshl_add_u64 v[206:207], s[16:17], 0, v[0:1]
	global_load_dwordx4 v[192:195], v[2:3], off
	global_load_dwordx4 v[196:199], v[2:3], off offset:256
	global_load_dwordx4 v[12:15], v[4:5], off
	global_load_dwordx4 v[8:11], v[4:5], off offset:256
	s_nop 0
	global_load_dwordx4 v[4:7], v[202:203], off
	global_load_dwordx4 v[0:3], v[202:203], off offset:256
	v_mov_b32_e32 v30, 0
	v_mov_b32_e32 v31, 0
	v_lshlrev_b64 v[18:19], 10, v[18:19]
	v_lshlrev_b64 v[16:17], 10, v[16:17]
	v_lshl_add_u64 v[16:17], v[16:17], 0, v[20:21]
	s_waitcnt vmcnt(0)
	v_lshlrev_b32_e32 v202, 16, v26
	v_and_b32_e32 v203, 0xffff0000, v26
	v_lshlrev_b32_e32 v208, 16, v28
	v_and_b32_e32 v209, 0xffff0000, v28
	v_lshlrev_b32_e32 v26, 16, v27
	v_and_b32_e32 v27, 0xffff0000, v27
	v_lshlrev_b32_e32 v28, 16, v29
	v_and_b32_e32 v29, 0xffff0000, v29
	v_lshlrev_b32_e32 v210, 16, v178
	v_and_b32_e32 v211, 0xffff0000, v178
	v_lshlrev_b32_e32 v178, 16, v179
	v_and_b32_e32 v179, 0xffff0000, v179
	v_lshlrev_b32_e32 v212, 16, v180
	v_and_b32_e32 v213, 0xffff0000, v180
	v_lshlrev_b32_e32 v180, 16, v181
	v_and_b32_e32 v181, 0xffff0000, v181
	v_pk_fma_f32 v[158:159], v[158:159], s[30:31], v[202:203] op_sel_hi:[1,0,1]
	v_pk_fma_f32 v[154:155], v[154:155], s[30:31], v[208:209] op_sel_hi:[1,0,1]
	v_pk_fma_f32 v[160:161], v[160:161], s[30:31], v[26:27] op_sel_hi:[1,0,1]
	v_pk_fma_f32 v[156:157], v[156:157], s[30:31], v[28:29] op_sel_hi:[1,0,1]
	v_pk_fma_f32 v[152:153], v[152:153], s[30:31], v[178:179] op_sel_hi:[1,0,1]
	v_pk_fma_f32 v[148:149], v[148:149], s[30:31], v[180:181] op_sel_hi:[1,0,1]
	v_mul_f32_e32 v25, v159, v159
	v_mul_f32_e32 v179, v155, v155
	v_cvt_pk_bf16_f32 v26, v158, v159
	v_cvt_pk_bf16_f32 v27, v160, v161
	v_cvt_pk_bf16_f32 v28, v154, v155
	v_mul_f32_e32 v181, 0x41000000, v158
	v_mul_f32_e32 v159, 0x41000000, v159
	v_mul_f32_e32 v202, 0x41000000, v154
	v_mul_f32_e32 v155, 0x41000000, v155
	v_cvt_pk_fp8_f32 v30, v181, v159
	v_cvt_pk_fp8_f32 v31, v202, v155
	v_mul_f32_e32 v178, v161, v161
	v_mul_f32_e32 v180, v157, v157
	v_cvt_pk_bf16_f32 v29, v156, v157
	v_mul_f32_e32 v191, 0x41000000, v160
	v_mul_f32_e32 v161, 0x41000000, v161
	v_mul_f32_e32 v203, 0x41000000, v156
	v_mul_f32_e32 v157, 0x41000000, v157
	v_cvt_pk_fp8_f32 v30, v191, v161 op_sel:[0,0,1]
	v_cvt_pk_fp8_f32 v31, v203, v157 op_sel:[0,0,1]
	v_pk_fma_f32 v[150:151], v[150:151], s[30:31], v[210:211] op_sel_hi:[1,0,1]
	v_pk_fma_f32 v[146:147], v[146:147], s[30:31], v[212:213] op_sel_hi:[1,0,1]
	global_store_dwordx4 v[204:205], v[26:29], off
	global_store_dwordx2 v[206:207], v[30:31], off
	v_mov_b32_e32 v30, 0
	v_mul_f32_e32 v28, 0x41000000, v150
	v_mul_f32_e32 v29, 0x41000000, v151
	v_mul_f32_e32 v208, v151, v151
	v_mul_f32_e32 v209, v153, v153
	v_mul_f32_e32 v210, v147, v147
	v_mul_f32_e32 v211, v149, v149
	v_fmac_f32_e32 v25, v158, v158
	v_fmac_f32_e32 v178, v160, v160
	v_fmac_f32_e32 v179, v154, v154
	v_fmac_f32_e32 v180, v156, v156
	v_cvt_pk_fp8_f32 v30, v28, v29
	v_mul_f32_e32 v28, 0x41000000, v146
	v_mul_f32_e32 v29, 0x41000000, v147
	v_mov_b32_e32 v31, 0
	v_fmac_f32_e32 v208, v150, v150
	v_fmac_f32_e32 v209, v152, v152
	v_fmac_f32_e32 v210, v146, v146
	v_fmac_f32_e32 v211, v148, v148
	v_add_f32_e32 v25, v25, v178
	v_add_f32_e32 v26, v179, v180
	v_cvt_pk_fp8_f32 v31, v28, v29
	v_add_f32_e32 v27, v208, v209
	v_add_f32_e32 v25, v25, v26
	v_add_f32_e32 v26, v210, v211
	v_add_f32_e32 v26, v27, v26
	v_add_f32_e32 v25, v25, v26
	v_cvt_pk_bf16_f32 v26, v150, v151
	v_mul_f32_e32 v150, 0x41000000, v152
	v_mul_f32_e32 v151, 0x41000000, v153
	v_mul_f32_e32 v28, 0x41000000, v148
	v_mul_f32_e32 v29, 0x41000000, v149
	v_cvt_pk_fp8_f32 v30, v150, v151 op_sel:[0,0,1]
	v_cvt_pk_fp8_f32 v31, v28, v29 op_sel:[0,0,1]
	ds_bpermute_b32 v150, v184, v25
	v_cvt_pk_bf16_f32 v27, v152, v153
	v_cvt_pk_bf16_f32 v28, v146, v147
	v_cvt_pk_bf16_f32 v29, v148, v149
	global_store_dwordx4 v[204:205], v[26:29], off offset:256
	global_store_dwordx2 v[206:207], v[30:31], off offset:128
	s_waitcnt lgkmcnt(0)
	v_add_f32_e32 v146, v25, v150
	v_lshlrev_b64 v[26:27], 10, v[200:201]
	v_lshl_add_u64 v[30:31], v[26:27], 0, v[20:21]
	v_lshlrev_b32_e32 v26, 16, v192
	v_and_b32_e32 v27, 0xffff0000, v192
	v_lshlrev_b32_e32 v28, 16, v193
	v_and_b32_e32 v29, 0xffff0000, v193
	v_pk_fma_f32 v[144:145], v[144:145], s[30:31], v[28:29] op_sel_hi:[1,0,1]
	v_pk_fma_f32 v[142:143], v[142:143], s[30:31], v[26:27] op_sel_hi:[1,0,1]
	v_lshlrev_b32_e32 v148, 16, v194
	v_and_b32_e32 v149, 0xffff0000, v194
	v_lshlrev_b32_e32 v150, 16, v195
	v_and_b32_e32 v151, 0xffff0000, v195
	v_mul_f32_e32 v25, v143, v143
	v_mul_f32_e32 v26, v145, v145
	v_pk_fma_f32 v[140:141], v[140:141], s[30:31], v[150:151] op_sel_hi:[1,0,1]
	v_pk_fma_f32 v[138:139], v[138:139], s[30:31], v[148:149] op_sel_hi:[1,0,1]
	v_fmac_f32_e32 v25, v142, v142
	v_fmac_f32_e32 v26, v144, v144
	v_add_f32_e32 v25, v25, v26
	v_mul_f32_e32 v26, v139, v139
	v_mul_f32_e32 v27, v141, v141
	v_fmac_f32_e32 v26, v138, v138
	v_fmac_f32_e32 v27, v140, v140
	v_add_f32_e32 v26, v26, v27
	v_add_f32_e32 v25, v25, v26
	v_cvt_pk_bf16_f32 v26, v142, v143
	v_mul_f32_e32 v148, 0x41000000, v142
	v_mul_f32_e32 v143, 0x41000000, v143
	v_mov_b32_e32 v142, 0
	v_cvt_pk_bf16_f32 v27, v144, v145
	v_cvt_pk_bf16_f32 v28, v138, v139
	v_cvt_pk_fp8_f32 v142, v148, v143
	v_mul_f32_e32 v138, 0x41000000, v138
	v_mul_f32_e32 v139, 0x41000000, v139
	v_mov_b32_e32 v143, 0
	v_cvt_pk_fp8_f32 v143, v138, v139
	v_mul_f32_e32 v138, 0x41000000, v140
	v_mul_f32_e32 v139, 0x41000000, v141
	v_cvt_pk_bf16_f32 v29, v140, v141
	v_mul_f32_e32 v144, 0x41000000, v144
	v_mul_f32_e32 v145, 0x41000000, v145
	v_cvt_pk_fp8_f32 v143, v138, v139 op_sel:[0,0,1]
	v_lshl_add_u64 v[138:139], v[30:31], 1, s[14:15]
	v_cvt_pk_fp8_f32 v142, v144, v145 op_sel:[0,0,1]
	global_store_dwordx4 v[138:139], v[26:29], off
	v_lshl_add_u64 v[30:31], s[16:17], 0, v[30:31]
	v_lshlrev_b32_e32 v140, 16, v198
	v_lshlrev_b32_e32 v26, 16, v196
	v_and_b32_e32 v27, 0xffff0000, v196
	v_lshlrev_b32_e32 v28, 16, v197
	v_and_b32_e32 v29, 0xffff0000, v197
	v_pk_fma_f32 v[28:29], v[136:137], s[30:31], v[28:29] op_sel_hi:[1,0,1]
	v_pk_fma_f32 v[134:135], v[134:135], s[30:31], v[26:27] op_sel_hi:[1,0,1]
	v_mul_f32_e32 v27, v29, v29
	v_mul_f32_e32 v26, v135, v135
	v_and_b32_e32 v141, 0xffff0000, v198
	v_fmac_f32_e32 v26, v134, v134
	v_fmac_f32_e32 v27, v28, v28
	global_store_dwordx2 v[30:31], v[142:143], off
	v_lshlrev_b32_e32 v142, 16, v199
	v_and_b32_e32 v143, 0xffff0000, v199
	v_pk_fma_f32 v[130:131], v[130:131], s[30:31], v[140:141] op_sel_hi:[1,0,1]
	v_add_f32_e32 v136, v26, v27
	v_cvt_pk_bf16_f32 v26, v134, v135
	v_mul_f32_e32 v141, 0x41000000, v134
	v_mul_f32_e32 v135, 0x41000000, v135
	v_mov_b32_e32 v134, 0
	v_pk_fma_f32 v[132:133], v[132:133], s[30:31], v[142:143] op_sel_hi:[1,0,1]
	v_cvt_pk_fp8_f32 v134, v141, v135
	v_mul_f32_e32 v141, 0x41000000, v130
	v_mul_f32_e32 v142, 0x41000000, v131
	v_mov_b32_e32 v135, 0
	v_cvt_pk_fp8_f32 v135, v141, v142
	v_cvt_pk_bf16_f32 v27, v28, v29
	v_mul_f32_e32 v28, 0x41000000, v28
	v_mul_f32_e32 v29, 0x41000000, v29
	v_cvt_pk_fp8_f32 v134, v28, v29 op_sel:[0,0,1]
	v_mul_f32_e32 v28, 0x41000000, v132
	v_mul_f32_e32 v29, 0x41000000, v133
	v_cvt_pk_fp8_f32 v135, v28, v29 op_sel:[0,0,1]
	v_mul_f32_e32 v137, v131, v131
	v_fmac_f32_e32 v137, v130, v130
	v_cvt_pk_bf16_f32 v28, v130, v131
	v_cvt_pk_bf16_f32 v29, v132, v133
	v_lshl_add_u64 v[130:131], v[18:19], 0, v[20:21]
	v_lshlrev_b32_e32 v18, 16, v12
	v_and_b32_e32 v19, 0xffff0000, v12
	global_store_dwordx4 v[138:139], v[26:29], off offset:256
	global_store_dwordx2 v[30:31], v[134:135], off offset:128
	v_pk_fma_f32 v[18:19], v[126:127], s[30:31], v[18:19] op_sel_hi:[1,0,1]
	v_lshlrev_b32_e32 v26, 16, v14
	v_and_b32_e32 v27, 0xffff0000, v14
	v_lshlrev_b32_e32 v14, 16, v15
	v_and_b32_e32 v15, 0xffff0000, v15
	v_pk_fma_f32 v[14:15], v[124:125], s[30:31], v[14:15] op_sel_hi:[1,0,1]
	v_pk_fma_f32 v[26:27], v[122:123], s[30:31], v[26:27] op_sel_hi:[1,0,1]
	v_mul_f32_e32 v123, 0x41000000, v18
	v_mul_f32_e32 v124, 0x41000000, v19
	v_mov_b32_e32 v122, 0
	v_cvt_pk_fp8_f32 v122, v123, v124
	v_mul_f32_e32 v124, 0x41000000, v26
	v_mul_f32_e32 v127, 0x41000000, v27
	v_mov_b32_e32 v123, 0
	v_lshlrev_b32_e32 v12, 16, v13
	v_and_b32_e32 v13, 0xffff0000, v13
	v_cvt_pk_fp8_f32 v123, v124, v127
	v_pk_fma_f32 v[12:13], v[128:129], s[30:31], v[12:13] op_sel_hi:[1,0,1]
	v_mul_f32_e32 v124, 0x41000000, v14
	v_mul_f32_e32 v125, 0x41000000, v12
	v_mul_f32_e32 v126, 0x41000000, v13
	v_cvt_pk_fp8_f32 v122, v125, v126 op_sel:[0,0,1]
	v_mul_f32_e32 v125, 0x41000000, v15
	v_cvt_pk_bf16_f32 v28, v18, v19
	v_cvt_pk_bf16_f32 v29, v12, v13
	v_cvt_pk_fp8_f32 v123, v124, v125 op_sel:[0,0,1]
	v_lshl_add_u64 v[124:125], v[130:131], 1, s[14:15]
	v_cvt_pk_bf16_f32 v30, v26, v27
	v_cvt_pk_bf16_f32 v31, v14, v15
	global_store_dwordx4 v[124:125], v[28:31], off
	v_lshl_add_u64 v[126:127], s[16:17], 0, v[130:131]
	global_store_dwordx2 v[126:127], v[122:123], off
	v_lshlrev_b32_e32 v28, 16, v8
	v_and_b32_e32 v29, 0xffff0000, v8
	v_lshlrev_b32_e32 v30, 16, v10
	v_and_b32_e32 v31, 0xffff0000, v10
	v_lshlrev_b32_e32 v10, 16, v11
	v_and_b32_e32 v11, 0xffff0000, v11
	v_pk_fma_f32 v[28:29], v[118:119], s[30:31], v[28:29] op_sel_hi:[1,0,1]
	v_pk_fma_f32 v[10:11], v[116:117], s[30:31], v[10:11] op_sel_hi:[1,0,1]
	v_pk_fma_f32 v[30:31], v[114:115], s[30:31], v[30:31] op_sel_hi:[1,0,1]
	v_mul_f32_e32 v116, 0x41000000, v28
	v_mul_f32_e32 v117, 0x41000000, v29
	v_mov_b32_e32 v118, 0
	v_cvt_pk_fp8_f32 v118, v116, v117
	v_mul_f32_e32 v116, 0x41000000, v30
	v_mul_f32_e32 v117, 0x41000000, v31
	v_mov_b32_e32 v119, 0
	v_cvt_pk_fp8_f32 v119, v116, v117
	v_lshlrev_b32_e32 v8, 16, v9
	v_and_b32_e32 v9, 0xffff0000, v9
	v_pk_fma_f32 v[8:9], v[120:121], s[30:31], v[8:9] op_sel_hi:[1,0,1]
	v_mul_f32_e32 v116, 0x41000000, v10
	v_mul_f32_e32 v120, 0x41000000, v8
	v_mul_f32_e32 v121, 0x41000000, v9
	v_mul_f32_e32 v117, 0x41000000, v11
	v_cvt_pk_fp8_f32 v118, v120, v121 op_sel:[0,0,1]
	v_cvt_pk_fp8_f32 v119, v116, v117 op_sel:[0,0,1]
	v_cvt_pk_bf16_f32 v114, v28, v29
	v_cvt_pk_bf16_f32 v115, v8, v9
	v_cvt_pk_bf16_f32 v116, v30, v31
	v_cvt_pk_bf16_f32 v117, v10, v11
	global_store_dwordx4 v[124:125], v[114:117], off offset:256
	global_store_dwordx2 v[126:127], v[118:119], off offset:128
	v_mul_f32_e32 v9, v9, v9
	v_lshlrev_b32_e32 v114, 16, v4
	v_and_b32_e32 v115, 0xffff0000, v4
	v_lshlrev_b32_e32 v116, 16, v6
	v_and_b32_e32 v117, 0xffff0000, v6
	v_pk_fma_f32 v[110:111], v[110:111], s[30:31], v[114:115] op_sel_hi:[1,0,1]
	v_pk_fma_f32 v[106:107], v[106:107], s[30:31], v[116:117] op_sel_hi:[1,0,1]
	v_mul_f32_e32 v115, 0x41000000, v110
	v_mul_f32_e32 v116, 0x41000000, v111
	v_mov_b32_e32 v114, 0
	v_cvt_pk_fp8_f32 v114, v115, v116
	v_mul_f32_e32 v116, 0x41000000, v106
	v_mul_f32_e32 v119, 0x41000000, v107
	v_mov_b32_e32 v115, 0
	v_lshlrev_b32_e32 v4, 16, v5
	v_and_b32_e32 v5, 0xffff0000, v5
	v_cvt_pk_fp8_f32 v115, v116, v119
	v_lshlrev_b32_e32 v6, 16, v7
	v_and_b32_e32 v7, 0xffff0000, v7
	v_pk_fma_f32 v[112:113], v[112:113], s[30:31], v[4:5] op_sel_hi:[1,0,1]
	v_pk_fma_f32 v[108:109], v[108:109], s[30:31], v[6:7] op_sel_hi:[1,0,1]
	v_mul_f32_e32 v117, 0x41000000, v112
	v_mul_f32_e32 v118, 0x41000000, v113
	v_cvt_pk_fp8_f32 v114, v117, v118 op_sel:[0,0,1]
	v_mul_f32_e32 v116, 0x41000000, v108
	v_mul_f32_e32 v117, 0x41000000, v109
	v_cvt_pk_fp8_f32 v115, v116, v117 op_sel:[0,0,1]
	v_cvt_pk_bf16_f32 v4, v110, v111
	v_cvt_pk_bf16_f32 v5, v112, v113
	v_cvt_pk_bf16_f32 v6, v106, v107
	v_cvt_pk_bf16_f32 v7, v108, v109
	v_lshl_add_u64 v[116:117], v[16:17], 1, s[14:15]
	global_store_dwordx4 v[116:117], v[4:7], off
	v_fmac_f32_e32 v9, v8, v8
	v_mul_f32_e32 v8, v31, v31
	v_lshlrev_b32_e32 v6, 16, v0
	v_and_b32_e32 v7, 0xffff0000, v0
	v_lshl_add_u64 v[4:5], s[16:17], 0, v[16:17]
	v_lshlrev_b32_e32 v16, 16, v2
	v_and_b32_e32 v17, 0xffff0000, v2
	v_lshlrev_b32_e32 v2, 16, v3
	v_and_b32_e32 v3, 0xffff0000, v3
	v_pk_fma_f32 v[6:7], v[102:103], s[30:31], v[6:7] op_sel_hi:[1,0,1]
	global_store_dwordx2 v[4:5], v[114:115], off
	v_pk_fma_f32 v[114:115], v[100:101], s[30:31], v[2:3] op_sel_hi:[1,0,1]
	v_pk_fma_f32 v[16:17], v[98:99], s[30:31], v[16:17] op_sel_hi:[1,0,1]
	v_mul_f32_e32 v2, 0x41000000, v6
	v_mul_f32_e32 v3, 0x41000000, v7
	v_mov_b32_e32 v98, 0
	v_cvt_pk_fp8_f32 v98, v2, v3
	v_mul_f32_e32 v2, 0x41000000, v16
	v_mul_f32_e32 v3, 0x41000000, v17
	v_mov_b32_e32 v99, 0
	v_cvt_pk_fp8_f32 v99, v2, v3
	v_lshlrev_b32_e32 v0, 16, v1
	v_and_b32_e32 v1, 0xffff0000, v1
	v_pk_fma_f32 v[104:105], v[104:105], s[30:31], v[0:1] op_sel_hi:[1,0,1]
	v_mul_f32_e32 v2, 0x41000000, v114
	v_mul_f32_e32 v100, 0x41000000, v104
	v_mul_f32_e32 v101, 0x41000000, v105
	v_mul_f32_e32 v3, 0x41000000, v115
	v_cvt_pk_fp8_f32 v98, v100, v101 op_sel:[0,0,1]
	v_cvt_pk_fp8_f32 v99, v2, v3 op_sel:[0,0,1]
	v_cvt_pk_bf16_f32 v0, v6, v7
	v_cvt_pk_bf16_f32 v1, v104, v105
	v_cvt_pk_bf16_f32 v2, v16, v17
	v_cvt_pk_bf16_f32 v3, v114, v115
	global_store_dwordx4 v[116:117], v[0:3], off offset:256
	global_store_dwordx2 v[4:5], v[98:99], off offset:128
	v_add_u32_e32 v116, 0x80, v24
	v_ashrrev_i32_e32 v117, 31, v116
	v_lshlrev_b64 v[0:1], 11, v[116:117]
	v_lshl_add_u64 v[0:1], v[22:23], 0, v[0:1]
	global_load_dwordx4 v[100:103], v[0:1], off
	v_mul_f32_e32 v4, v19, v19
	v_mul_f32_e32 v5, v13, v13
	v_fmac_f32_e32 v4, v18, v18
	v_fmac_f32_e32 v5, v12, v12
	v_add_f32_e32 v4, v4, v5
	v_mul_f32_e32 v5, v27, v27
	v_mul_f32_e32 v12, v15, v15
	v_fmac_f32_e32 v5, v26, v26
	v_fmac_f32_e32 v12, v14, v14
	v_add_f32_e32 v5, v5, v12
	v_add_f32_e32 v4, v4, v5
	v_mul_f32_e32 v5, v29, v29
	v_fmac_f32_e32 v5, v28, v28
	v_add_f32_e32 v5, v5, v9
	v_mul_f32_e32 v9, v11, v11
	v_fmac_f32_e32 v8, v30, v30
	v_fmac_f32_e32 v9, v10, v10
	v_add_f32_e32 v8, v8, v9
	v_add_f32_e32 v5, v5, v8
	v_mul_f32_e32 v8, v111, v111
	v_mul_f32_e32 v9, v113, v113
	v_fmac_f32_e32 v8, v110, v110
	v_fmac_f32_e32 v9, v112, v112
	v_mul_f32_e32 v7, v7, v7
	v_add_f32_e32 v8, v8, v9
	v_mul_f32_e32 v9, v107, v107
	v_fmac_f32_e32 v7, v6, v6
	v_mul_f32_e32 v6, v105, v105
	v_fmac_f32_e32 v9, v106, v106
	v_fmac_f32_e32 v6, v104, v104
	global_load_dwordx4 v[104:107], v[0:1], off offset:256
	v_mul_f32_e32 v10, v109, v109
	v_mul_f32_e32 v0, v17, v17
	v_mul_f32_e32 v1, v115, v115
	v_fmac_f32_e32 v10, v108, v108
	v_fmac_f32_e32 v0, v16, v16
	v_fmac_f32_e32 v1, v114, v114
	v_add_f32_e32 v9, v9, v10
	v_add_f32_e32 v6, v7, v6
	v_add_f32_e32 v0, v0, v1
	v_add_f32_e32 v8, v8, v9
	v_add_f32_e32 v0, v6, v0
	v_add_f32_e32 v0, v8, v0
	ds_bpermute_b32 v1, v184, v0
	v_add_u32_e32 v112, 0x90, v24
	v_ashrrev_i32_e32 v113, 31, v112
	v_add_u32_e32 v26, 0xa0, v24
	v_ashrrev_i32_e32 v27, 31, v26
	s_waitcnt lgkmcnt(0)
	v_add_f32_e32 v98, v0, v1
	v_lshlrev_b64 v[0:1], 11, v[112:113]
	v_lshl_add_u64 v[0:1], v[22:23], 0, v[0:1]
	global_load_dwordx4 v[108:111], v[0:1], off
	global_load_dwordx4 v[16:19], v[0:1], off offset:256
	v_lshlrev_b64 v[0:1], 11, v[26:27]
	v_lshl_add_u64 v[0:1], v[22:23], 0, v[0:1]
	global_load_dwordx4 v[12:15], v[0:1], off
	global_load_dwordx4 v[8:11], v[0:1], off offset:256
	v_mul_f32_e32 v140, v133, v133
	v_fmac_f32_e32 v140, v132, v132
	v_add_f32_e32 v2, v137, v140
	v_add_f32_e32 v2, v136, v2
	v_add_u32_e32 v24, 0xb0, v24
	v_add_f32_e32 v2, v25, v2
	v_ashrrev_i32_e32 v25, 31, v24
	v_lshlrev_b64 v[0:1], 11, v[24:25]
	v_add_f32_e32 v4, v4, v5
	v_lshl_add_u64 v[0:1], v[22:23], 0, v[0:1]
	v_lshlrev_b64 v[22:23], 10, v[116:117]
	ds_bpermute_b32 v3, v184, v2
	ds_bpermute_b32 v5, v184, v4
	v_lshl_add_u64 v[22:23], v[22:23], 0, v[20:21]
	ds_bpermute_b32 v147, v185, v146
	ds_bpermute_b32 v99, v185, v98
	s_waitcnt lgkmcnt(3)
	v_add_f32_e32 v28, v2, v3
	s_waitcnt lgkmcnt(2)
	v_add_f32_e32 v30, v4, v5
	global_load_dwordx4 v[4:7], v[0:1], off
	s_nop 0
	global_load_dwordx4 v[0:3], v[0:1], off offset:256
	ds_bpermute_b32 v29, v185, v28
	ds_bpermute_b32 v31, v185, v30
	s_waitcnt vmcnt(7)
	v_lshlrev_b32_e32 v114, 16, v100
	v_and_b32_e32 v115, 0xffff0000, v100
	v_lshlrev_b32_e32 v100, 16, v101
	v_and_b32_e32 v101, 0xffff0000, v101
	v_lshlrev_b32_e32 v116, 16, v102
	v_and_b32_e32 v117, 0xffff0000, v102
	v_lshlrev_b32_e32 v102, 16, v103
	v_and_b32_e32 v103, 0xffff0000, v103
	v_pk_fma_f32 v[96:97], v[96:97], s[30:31], v[100:101] op_sel_hi:[1,0,1]
	v_pk_fma_f32 v[94:95], v[94:95], s[30:31], v[114:115] op_sel_hi:[1,0,1]
	v_pk_fma_f32 v[100:101], v[92:93], s[30:31], v[102:103] op_sel_hi:[1,0,1]
	v_pk_fma_f32 v[102:103], v[90:91], s[30:31], v[116:117] op_sel_hi:[1,0,1]
	v_mul_f32_e32 v90, v95, v95
	v_mul_f32_e32 v91, v97, v97
	v_fmac_f32_e32 v90, v94, v94
	v_fmac_f32_e32 v91, v96, v96
	v_add_f32_e32 v90, v90, v91
	v_mul_f32_e32 v91, v103, v103
	v_mul_f32_e32 v92, v101, v101
	v_fmac_f32_e32 v91, v102, v102
	v_fmac_f32_e32 v92, v100, v100
	v_add_f32_e32 v91, v91, v92
	v_add_f32_e32 v114, v90, v91
	v_cvt_pk_bf16_f32 v90, v94, v95
	v_mul_f32_e32 v115, 0x41000000, v94
	v_mul_f32_e32 v95, 0x41000000, v95
	v_mov_b32_e32 v94, 0
	v_cvt_pk_bf16_f32 v91, v96, v97
	v_cvt_pk_bf16_f32 v92, v102, v103
	v_cvt_pk_fp8_f32 v94, v115, v95
	v_mul_f32_e32 v102, 0x41000000, v102
	v_mul_f32_e32 v103, 0x41000000, v103
	v_mov_b32_e32 v95, 0
	v_cvt_pk_fp8_f32 v95, v102, v103
	v_mul_f32_e32 v96, 0x41000000, v96
	v_mul_f32_e32 v97, 0x41000000, v97
	v_cvt_pk_fp8_f32 v94, v96, v97 op_sel:[0,0,1]
	v_mul_f32_e32 v96, 0x41000000, v100
	v_mul_f32_e32 v97, 0x41000000, v101
	v_cvt_pk_fp8_f32 v95, v96, v97 op_sel:[0,0,1]
	v_cvt_pk_bf16_f32 v93, v100, v101
	v_lshl_add_u64 v[96:97], v[22:23], 1, s[14:15]
	global_store_dwordx4 v[96:97], v[90:93], off
	v_lshl_add_u64 v[22:23], s[16:17], 0, v[22:23]
	global_store_dwordx2 v[22:23], v[94:95], off
	s_waitcnt vmcnt(8)
	v_lshlrev_b32_e32 v90, 16, v104
	v_and_b32_e32 v91, 0xffff0000, v104
	v_lshlrev_b32_e32 v92, 16, v105
	v_and_b32_e32 v93, 0xffff0000, v105
	v_lshlrev_b32_e32 v94, 16, v106
	v_and_b32_e32 v95, 0xffff0000, v106
	v_lshlrev_b32_e32 v100, 16, v107
	v_and_b32_e32 v101, 0xffff0000, v107
	v_pk_fma_f32 v[88:89], v[88:89], s[30:31], v[92:93] op_sel_hi:[1,0,1]
	v_pk_fma_f32 v[86:87], v[86:87], s[30:31], v[90:91] op_sel_hi:[1,0,1]
	v_pk_fma_f32 v[90:91], v[84:85], s[30:31], v[100:101] op_sel_hi:[1,0,1]
	v_pk_fma_f32 v[84:85], v[82:83], s[30:31], v[94:95] op_sel_hi:[1,0,1]
	v_mul_f32_e32 v82, v87, v87
	v_mul_f32_e32 v83, v89, v89
	v_fmac_f32_e32 v82, v86, v86
	v_fmac_f32_e32 v83, v88, v88
	v_add_f32_e32 v82, v82, v83
	v_mul_f32_e32 v83, v85, v85
	v_mul_f32_e32 v92, v91, v91
	v_fmac_f32_e32 v83, v84, v84
	v_fmac_f32_e32 v92, v90, v90
	v_add_f32_e32 v83, v83, v92
	v_add_f32_e32 v82, v82, v83
	v_add_f32_e32 v92, v114, v82
	v_cvt_pk_bf16_f32 v82, v86, v87
	v_mul_f32_e32 v93, 0x41000000, v86
	v_mul_f32_e32 v87, 0x41000000, v87
	v_mov_b32_e32 v86, 0
	v_cvt_pk_fp8_f32 v86, v93, v87
	v_mul_f32_e32 v93, 0x41000000, v84
	v_mul_f32_e32 v94, 0x41000000, v85
	v_mov_b32_e32 v87, 0
	v_cvt_pk_fp8_f32 v87, v93, v94
	v_cvt_pk_bf16_f32 v83, v88, v89
	v_mul_f32_e32 v88, 0x41000000, v88
	v_mul_f32_e32 v89, 0x41000000, v89
	v_cvt_pk_fp8_f32 v86, v88, v89 op_sel:[0,0,1]
	v_mul_f32_e32 v88, 0x41000000, v90
	v_mul_f32_e32 v89, 0x41000000, v91
	v_cvt_pk_fp8_f32 v87, v88, v89 op_sel:[0,0,1]
	ds_bpermute_b32 v88, v184, v92
	v_cvt_pk_bf16_f32 v84, v84, v85
	v_cvt_pk_bf16_f32 v85, v90, v91
	global_store_dwordx4 v[96:97], v[82:85], off offset:256
	global_store_dwordx2 v[22:23], v[86:87], off offset:128
	s_waitcnt vmcnt(9)
	v_lshlrev_b32_e32 v86, 16, v109
	v_lshlrev_b32_e32 v84, 16, v108
	v_and_b32_e32 v85, 0xffff0000, v108
	v_and_b32_e32 v87, 0xffff0000, v109
	s_waitcnt lgkmcnt(0)
	v_add_f32_e32 v22, v92, v88
	v_lshlrev_b32_e32 v88, 16, v110
	v_and_b32_e32 v89, 0xffff0000, v110
	v_pk_fma_f32 v[80:81], v[80:81], s[30:31], v[86:87] op_sel_hi:[1,0,1]
	v_pk_fma_f32 v[78:79], v[78:79], s[30:31], v[84:85] op_sel_hi:[1,0,1]
	v_lshlrev_b32_e32 v90, 16, v111
	v_and_b32_e32 v91, 0xffff0000, v111
	v_pk_fma_f32 v[86:87], v[74:75], s[30:31], v[88:89] op_sel_hi:[1,0,1]
	v_mul_f32_e32 v74, v79, v79
	v_mul_f32_e32 v75, v81, v81
	v_pk_fma_f32 v[84:85], v[76:77], s[30:31], v[90:91] op_sel_hi:[1,0,1]
	v_fmac_f32_e32 v74, v78, v78
	v_fmac_f32_e32 v75, v80, v80
	v_add_f32_e32 v74, v74, v75
	v_mul_f32_e32 v75, v87, v87
	v_mul_f32_e32 v76, v85, v85
	v_fmac_f32_e32 v75, v86, v86
	v_fmac_f32_e32 v76, v84, v84
	v_add_f32_e32 v75, v75, v76
	v_add_f32_e32 v88, v74, v75
	v_cvt_pk_bf16_f32 v74, v78, v79
	v_mul_f32_e32 v89, 0x41000000, v78
	v_mul_f32_e32 v79, 0x41000000, v79
	v_mov_b32_e32 v78, 0
	v_cvt_pk_bf16_f32 v75, v80, v81
	v_cvt_pk_bf16_f32 v76, v86, v87
	v_cvt_pk_fp8_f32 v78, v89, v79
	v_mul_f32_e32 v86, 0x41000000, v86
	v_mul_f32_e32 v87, 0x41000000, v87
	v_mov_b32_e32 v79, 0
	v_cvt_pk_fp8_f32 v79, v86, v87
	v_mul_f32_e32 v80, 0x41000000, v80
	v_mul_f32_e32 v81, 0x41000000, v81
	v_lshlrev_b64 v[82:83], 10, v[112:113]
	v_cvt_pk_fp8_f32 v78, v80, v81 op_sel:[0,0,1]
	v_mul_f32_e32 v80, 0x41000000, v84
	v_mul_f32_e32 v81, 0x41000000, v85
	v_lshl_add_u64 v[82:83], v[82:83], 0, v[20:21]
	v_cvt_pk_fp8_f32 v79, v80, v81 op_sel:[0,0,1]
	v_cvt_pk_bf16_f32 v77, v84, v85
	v_lshl_add_u64 v[80:81], v[82:83], 1, s[14:15]
	global_store_dwordx4 v[80:81], v[74:77], off
	ds_bpermute_b32 v23, v185, v22
	s_waitcnt vmcnt(9)
	v_lshlrev_b32_e32 v76, 16, v16
	v_and_b32_e32 v77, 0xffff0000, v16
	v_lshlrev_b32_e32 v16, 16, v17
	v_and_b32_e32 v17, 0xffff0000, v17
	v_lshl_add_u64 v[74:75], s[16:17], 0, v[82:83]
	v_pk_fma_f32 v[72:73], v[72:73], s[30:31], v[16:17] op_sel_hi:[1,0,1]
	v_pk_fma_f32 v[70:71], v[70:71], s[30:31], v[76:77] op_sel_hi:[1,0,1]
	global_store_dwordx2 v[74:75], v[78:79], off
	v_lshlrev_b32_e32 v78, 16, v18
	v_and_b32_e32 v79, 0xffff0000, v18
	v_lshlrev_b32_e32 v18, 16, v19
	v_and_b32_e32 v19, 0xffff0000, v19
	v_mul_f32_e32 v16, v71, v71
	v_mul_f32_e32 v17, v73, v73
	v_pk_fma_f32 v[68:69], v[68:69], s[30:31], v[18:19] op_sel_hi:[1,0,1]
	v_pk_fma_f32 v[18:19], v[66:67], s[30:31], v[78:79] op_sel_hi:[1,0,1]
	v_fmac_f32_e32 v16, v70, v70
	v_fmac_f32_e32 v17, v72, v72
	v_add_f32_e32 v16, v16, v17
	v_mul_f32_e32 v17, v19, v19
	v_mul_f32_e32 v66, v69, v69
	v_fmac_f32_e32 v17, v18, v18
	v_fmac_f32_e32 v66, v68, v68
	v_add_f32_e32 v17, v17, v66
	v_add_f32_e32 v16, v16, v17
	v_add_f32_e32 v76, v88, v16
	v_cvt_pk_bf16_f32 v16, v70, v71
	v_mul_f32_e32 v67, 0x41000000, v70
	v_mul_f32_e32 v70, 0x41000000, v71
	v_mov_b32_e32 v66, 0
	v_cvt_pk_bf16_f32 v17, v72, v73
	v_mul_f32_e32 v71, 0x41000000, v72
	v_mul_f32_e32 v72, 0x41000000, v73
	v_cvt_pk_fp8_f32 v66, v67, v70
	v_mul_f32_e32 v70, 0x41000000, v18
	v_mul_f32_e32 v73, 0x41000000, v19
	v_mov_b32_e32 v67, 0
	v_cvt_pk_fp8_f32 v67, v70, v73
	v_cvt_pk_fp8_f32 v66, v71, v72 op_sel:[0,0,1]
	v_mul_f32_e32 v70, 0x41000000, v68
	v_mul_f32_e32 v71, 0x41000000, v69
	v_cvt_pk_fp8_f32 v67, v70, v71 op_sel:[0,0,1]
	v_cvt_pk_bf16_f32 v18, v18, v19
	v_cvt_pk_bf16_f32 v19, v68, v69
	global_store_dwordx4 v[80:81], v[16:19], off offset:256
	global_store_dwordx2 v[74:75], v[66:67], off offset:128
	s_waitcnt vmcnt(11)
	v_lshlrev_b32_e32 v66, 16, v14
	v_lshlrev_b64 v[18:19], 10, v[26:27]
	v_lshlrev_b32_e32 v26, 16, v12
	v_and_b32_e32 v27, 0xffff0000, v12
	v_lshlrev_b32_e32 v12, 16, v13
	v_and_b32_e32 v13, 0xffff0000, v13
	v_pk_fma_f32 v[60:61], v[60:61], s[30:31], v[12:13] op_sel_hi:[1,0,1]
	v_pk_fma_f32 v[26:27], v[58:59], s[30:31], v[26:27] op_sel_hi:[1,0,1]
	v_and_b32_e32 v67, 0xffff0000, v14
	v_lshlrev_b32_e32 v14, 16, v15
	v_and_b32_e32 v15, 0xffff0000, v15
	v_mul_f32_e32 v12, v27, v27
	v_mul_f32_e32 v13, v61, v61
	v_pk_fma_f32 v[52:53], v[52:53], s[30:31], v[14:15] op_sel_hi:[1,0,1]
	v_pk_fma_f32 v[50:51], v[50:51], s[30:31], v[66:67] op_sel_hi:[1,0,1]
	v_fmac_f32_e32 v12, v26, v26
	v_fmac_f32_e32 v13, v60, v60
	v_add_f32_e32 v12, v12, v13
	v_mul_f32_e32 v13, v51, v51
	v_mul_f32_e32 v14, v53, v53
	v_fmac_f32_e32 v13, v50, v50
	v_fmac_f32_e32 v14, v52, v52
	v_add_f32_e32 v13, v13, v14
	v_add_f32_e32 v58, v12, v13
	v_cvt_pk_bf16_f32 v12, v26, v27
	v_mul_f32_e32 v59, 0x41000000, v26
	v_mul_f32_e32 v27, 0x41000000, v27
	v_mov_b32_e32 v26, 0
	v_cvt_pk_bf16_f32 v13, v60, v61
	v_cvt_pk_bf16_f32 v14, v50, v51
	v_cvt_pk_fp8_f32 v26, v59, v27
	v_mul_f32_e32 v50, 0x41000000, v50
	v_mul_f32_e32 v51, 0x41000000, v51
	v_mov_b32_e32 v27, 0
	v_cvt_pk_fp8_f32 v27, v50, v51
	v_mul_f32_e32 v60, 0x41000000, v60
	v_mul_f32_e32 v61, 0x41000000, v61
	v_mul_f32_e32 v50, 0x41000000, v52
	v_mul_f32_e32 v51, 0x41000000, v53
	v_cvt_pk_fp8_f32 v26, v60, v61 op_sel:[0,0,1]
	v_cvt_pk_fp8_f32 v27, v50, v51 op_sel:[0,0,1]
	v_lshl_add_u64 v[18:19], v[18:19], 0, v[20:21]
	v_cvt_pk_bf16_f32 v15, v52, v53
	v_lshl_add_u64 v[50:51], v[18:19], 1, s[14:15]
	global_store_dwordx4 v[50:51], v[12:15], off
	ds_bpermute_b32 v70, v184, v76
	s_waitcnt lgkmcnt(0)
	v_add_f32_e32 v16, v76, v70
	v_lshl_add_u64 v[12:13], s[16:17], 0, v[18:19]
	s_waitcnt vmcnt(11)
	v_lshlrev_b32_e32 v14, 16, v8
	v_and_b32_e32 v15, 0xffff0000, v8
	v_lshlrev_b32_e32 v8, 16, v9
	v_and_b32_e32 v9, 0xffff0000, v9
	global_store_dwordx2 v[12:13], v[26:27], off
	v_pk_fma_f32 v[26:27], v[64:65], s[30:31], v[8:9] op_sel_hi:[1,0,1]
	v_pk_fma_f32 v[14:15], v[62:63], s[30:31], v[14:15] op_sel_hi:[1,0,1]
	v_lshlrev_b32_e32 v18, 16, v10
	v_and_b32_e32 v19, 0xffff0000, v10
	v_lshlrev_b32_e32 v10, 16, v11
	v_and_b32_e32 v11, 0xffff0000, v11
	v_mul_f32_e32 v8, v15, v15
	v_mul_f32_e32 v9, v27, v27
	v_pk_fma_f32 v[52:53], v[56:57], s[30:31], v[10:11] op_sel_hi:[1,0,1]
	v_pk_fma_f32 v[10:11], v[54:55], s[30:31], v[18:19] op_sel_hi:[1,0,1]
	v_fmac_f32_e32 v8, v14, v14
	v_fmac_f32_e32 v9, v26, v26
	v_add_f32_e32 v8, v8, v9
	v_mul_f32_e32 v9, v11, v11
	v_mul_f32_e32 v18, v53, v53
	v_fmac_f32_e32 v9, v10, v10
	v_fmac_f32_e32 v18, v52, v52
	v_add_f32_e32 v9, v9, v18
	v_add_f32_e32 v8, v8, v9
	v_add_f32_e32 v18, v58, v8
	v_cvt_pk_bf16_f32 v8, v14, v15
	v_mul_f32_e32 v19, 0x41000000, v14
	v_mul_f32_e32 v15, 0x41000000, v15
	v_mov_b32_e32 v14, 0
	v_cvt_pk_fp8_f32 v14, v19, v15
	v_mul_f32_e32 v19, 0x41000000, v10
	v_mul_f32_e32 v54, 0x41000000, v11
	v_mov_b32_e32 v15, 0
	v_cvt_pk_fp8_f32 v15, v19, v54
	v_cvt_pk_bf16_f32 v9, v26, v27
	v_mul_f32_e32 v26, 0x41000000, v26
	v_mul_f32_e32 v27, 0x41000000, v27
	v_cvt_pk_fp8_f32 v14, v26, v27 op_sel:[0,0,1]
	v_mul_f32_e32 v19, 0x41000000, v52
	v_mul_f32_e32 v26, 0x41000000, v53
	v_cvt_pk_fp8_f32 v15, v19, v26 op_sel:[0,0,1]
	ds_bpermute_b32 v19, v184, v18
	v_cvt_pk_bf16_f32 v10, v10, v11
	v_cvt_pk_bf16_f32 v11, v52, v53
	global_store_dwordx4 v[50:51], v[8:11], off offset:256
	global_store_dwordx2 v[12:13], v[14:15], off offset:128
	s_waitcnt vmcnt(13)
	v_lshlrev_b32_e32 v12, 16, v4
	v_and_b32_e32 v13, 0xffff0000, v4
	v_lshlrev_b32_e32 v4, 16, v5
	v_and_b32_e32 v5, 0xffff0000, v5
	s_waitcnt lgkmcnt(0)
	v_add_f32_e32 v8, v18, v19
	v_pk_fma_f32 v[18:19], v[40:41], s[30:31], v[4:5] op_sel_hi:[1,0,1]
	v_pk_fma_f32 v[12:13], v[38:39], s[30:31], v[12:13] op_sel_hi:[1,0,1]
	v_lshlrev_b64 v[10:11], 10, v[24:25]
	v_lshlrev_b32_e32 v14, 16, v6
	v_and_b32_e32 v15, 0xffff0000, v6
	v_lshlrev_b32_e32 v6, 16, v7
	v_and_b32_e32 v7, 0xffff0000, v7
	v_mul_f32_e32 v4, v13, v13
	v_mul_f32_e32 v5, v19, v19
	v_lshl_add_u64 v[10:11], v[10:11], 0, v[20:21]
	v_pk_fma_f32 v[20:21], v[36:37], s[30:31], v[6:7] op_sel_hi:[1,0,1]
	v_pk_fma_f32 v[14:15], v[34:35], s[30:31], v[14:15] op_sel_hi:[1,0,1]
	v_fmac_f32_e32 v4, v12, v12
	v_fmac_f32_e32 v5, v18, v18
	v_add_f32_e32 v4, v4, v5
	v_mul_f32_e32 v5, v15, v15
	v_mul_f32_e32 v6, v21, v21
	v_fmac_f32_e32 v5, v14, v14
	v_fmac_f32_e32 v6, v20, v20
	v_add_f32_e32 v5, v5, v6
	v_add_f32_e32 v24, v4, v5
	v_cvt_pk_bf16_f32 v4, v12, v13
	v_mul_f32_e32 v25, 0x41000000, v12
	v_mul_f32_e32 v13, 0x41000000, v13
	v_mov_b32_e32 v12, 0
	v_cvt_pk_bf16_f32 v5, v18, v19
	v_cvt_pk_bf16_f32 v6, v14, v15
	v_cvt_pk_fp8_f32 v12, v25, v13
	v_mul_f32_e32 v14, 0x41000000, v14
	v_mul_f32_e32 v15, 0x41000000, v15
	v_mov_b32_e32 v13, 0
	v_cvt_pk_fp8_f32 v13, v14, v15
	v_mul_f32_e32 v18, 0x41000000, v18
	v_mul_f32_e32 v19, 0x41000000, v19
	v_mul_f32_e32 v14, 0x41000000, v20
	v_mul_f32_e32 v15, 0x41000000, v21
	v_cvt_pk_fp8_f32 v12, v18, v19 op_sel:[0,0,1]
	v_cvt_pk_fp8_f32 v13, v14, v15 op_sel:[0,0,1]
	v_lshl_add_u64 v[14:15], v[10:11], 1, s[14:15]
	v_cvt_pk_bf16_f32 v7, v20, v21
	global_store_dwordx4 v[14:15], v[4:7], off
	v_mov_b32_e32 v19, 0
	ds_bpermute_b32 v17, v185, v16
	s_waitcnt vmcnt(13)
	v_lshlrev_b32_e32 v4, 16, v0
	v_and_b32_e32 v5, 0xffff0000, v0
	v_lshlrev_b32_e32 v0, 16, v1
	v_and_b32_e32 v1, 0xffff0000, v1
	v_lshl_add_u64 v[6:7], s[16:17], 0, v[10:11]
	v_lshlrev_b32_e32 v10, 16, v2
	v_and_b32_e32 v11, 0xffff0000, v2
	v_lshlrev_b32_e32 v2, 16, v3
	v_and_b32_e32 v3, 0xffff0000, v3
	v_pk_fma_f32 v[0:1], v[48:49], s[30:31], v[0:1] op_sel_hi:[1,0,1]
	v_pk_fma_f32 v[4:5], v[46:47], s[30:31], v[4:5] op_sel_hi:[1,0,1]
	global_store_dwordx2 v[6:7], v[12:13], off
	v_pk_fma_f32 v[12:13], v[44:45], s[30:31], v[2:3] op_sel_hi:[1,0,1]
	v_mul_f32_e32 v2, v5, v5
	v_mul_f32_e32 v3, v1, v1
	v_pk_fma_f32 v[10:11], v[42:43], s[30:31], v[10:11] op_sel_hi:[1,0,1]
	v_fmac_f32_e32 v2, v4, v4
	v_fmac_f32_e32 v3, v0, v0
	v_add_f32_e32 v2, v2, v3
	v_mul_f32_e32 v3, v11, v11
	v_mul_f32_e32 v18, v13, v13
	v_fmac_f32_e32 v3, v10, v10
	v_fmac_f32_e32 v18, v12, v12
	v_add_f32_e32 v3, v3, v18
	v_add_f32_e32 v2, v2, v3
	v_add_f32_e32 v20, v24, v2
	v_cvt_pk_bf16_f32 v2, v4, v5
	v_mul_f32_e32 v4, 0x41000000, v4
	v_mul_f32_e32 v5, 0x41000000, v5
	v_mov_b32_e32 v18, 0
	v_cvt_pk_fp8_f32 v18, v4, v5
	v_mul_f32_e32 v4, 0x41000000, v10
	v_mul_f32_e32 v5, 0x41000000, v11
	v_cvt_pk_fp8_f32 v19, v4, v5
	ds_bpermute_b32 v4, v184, v20
	v_cvt_pk_bf16_f32 v3, v0, v1
	v_mul_f32_e32 v0, 0x41000000, v0
	v_mul_f32_e32 v1, 0x41000000, v1
	v_cvt_pk_fp8_f32 v18, v0, v1 op_sel:[0,0,1]
	v_mul_f32_e32 v0, 0x41000000, v12
	v_mul_f32_e32 v1, 0x41000000, v13
	v_cvt_pk_fp8_f32 v19, v0, v1 op_sel:[0,0,1]
	s_waitcnt lgkmcnt(0)
	v_add_f32_e32 v0, v20, v4
	ds_bpermute_b32 v9, v185, v8
	ds_bpermute_b32 v1, v185, v0
	v_cvt_pk_bf16_f32 v4, v10, v11
	v_cvt_pk_bf16_f32 v5, v12, v13
	global_store_dwordx4 v[14:15], v[2:5], off offset:256
	global_store_dwordx2 v[6:7], v[18:19], off offset:128
	s_and_saveexec_b64 s[36:37], s[2:3]
	s_cbranch_execz .LBB0_678
	v_add_f32_e32 v2, v146, v147
	v_add_f32_e32 v4, v28, v29
	v_mul_f32_e32 v2, 0x49800000, v2
	v_add_f32_e32 v6, v30, v31
	v_trunc_f32_e32 v2, v2
	v_mul_f32_e32 v4, 0x49800000, v4
	s_waitcnt lgkmcnt(1)
	v_add_f32_e32 v11, v8, v9
	v_add_f32_e32 v8, v98, v99
	v_mul_f32_e32 v3, 0x2f800000, v2
	v_trunc_f32_e32 v4, v4
	v_mul_f32_e32 v6, 0x49800000, v6
	v_floor_f32_e32 v3, v3
	v_mul_f32_e32 v5, 0x2f800000, v4
	v_trunc_f32_e32 v6, v6
	v_mul_f32_e32 v8, 0x49800000, v8
	v_fmac_f32_e32 v2, 0xcf800000, v3
	v_floor_f32_e32 v5, v5
	v_mul_f32_e32 v7, 0x2f800000, v6
	v_trunc_f32_e32 v8, v8
	v_cvt_u32_f32_e32 v2, v2
	v_cvt_u32_f32_e32 v3, v3
	v_fmac_f32_e32 v4, 0xcf800000, v5
	v_floor_f32_e32 v7, v7
	v_mul_f32_e32 v9, 0x2f800000, v8
	v_cvt_u32_f32_e32 v4, v4
	v_cvt_u32_f32_e32 v5, v5
	v_fmac_f32_e32 v6, 0xcf800000, v7
	v_floor_f32_e32 v9, v9
	s_ashr_i32 s29, s28, 31
	v_cvt_u32_f32_e32 v6, v6
	v_cvt_u32_f32_e32 v7, v7
	v_fmac_f32_e32 v8, 0xcf800000, v9
	s_waitcnt lgkmcnt(0)
	v_add_f32_e32 v10, v0, v1
	v_add_f32_e32 v13, v22, v23
	v_lshl_add_u64 v[0:1], s[28:29], 3, v[168:169]
	v_cvt_u32_f32_e32 v8, v8
	v_cvt_u32_f32_e32 v9, v9
	v_add_f32_e32 v12, v16, v17
	global_atomic_add_x2 v[0:1], v[2:3], off
	global_atomic_add_x2 v[0:1], v[4:5], off offset:128
	global_atomic_add_x2 v[0:1], v[6:7], off offset:256
	global_atomic_add_x2 v[0:1], v[8:9], off offset:384
	v_mul_f32_e32 v2, 0x49800000, v13
	v_trunc_f32_e32 v2, v2
	v_mul_f32_e32 v4, 0x49800000, v12
	v_mul_f32_e32 v3, 0x2f800000, v2
	v_trunc_f32_e32 v4, v4
	v_mul_f32_e32 v6, 0x49800000, v11
	v_floor_f32_e32 v3, v3
	v_mul_f32_e32 v5, 0x2f800000, v4
	v_trunc_f32_e32 v6, v6
	v_mul_f32_e32 v8, 0x49800000, v10
	v_fmac_f32_e32 v2, 0xcf800000, v3
	v_floor_f32_e32 v5, v5
	v_mul_f32_e32 v7, 0x2f800000, v6
	v_trunc_f32_e32 v8, v8
	v_cvt_u32_f32_e32 v2, v2
	v_cvt_u32_f32_e32 v3, v3
	v_fmac_f32_e32 v4, 0xcf800000, v5
	v_floor_f32_e32 v7, v7
	v_mul_f32_e32 v9, 0x2f800000, v8
	v_cvt_u32_f32_e32 v4, v4
	v_cvt_u32_f32_e32 v5, v5
	v_fmac_f32_e32 v6, 0xcf800000, v7
	v_floor_f32_e32 v9, v9
	v_cvt_u32_f32_e32 v6, v6
	v_cvt_u32_f32_e32 v7, v7
	v_fmac_f32_e32 v8, 0xcf800000, v9
	v_cvt_u32_f32_e32 v8, v8
	v_cvt_u32_f32_e32 v9, v9
	global_atomic_add_x2 v[0:1], v[2:3], off offset:1024
	global_atomic_add_x2 v[0:1], v[4:5], off offset:1152
	global_atomic_add_x2 v[0:1], v[6:7], off offset:1280
	global_atomic_add_x2 v[0:1], v[8:9], off offset:1408

.LBB0_947:
	v_ashrrev_i32_e32 v1, 31, v9
	v_lshrrev_b32_e32 v1, 26, v1
	v_add_u32_e32 v1, v9, v1
	v_ashrrev_i32_e32 v10, 6, v1
	v_bfe_i32 v1, v9, 27, 1
	v_lshlrev_b32_e32 v0, 4, v9
	v_lshrrev_b32_e32 v1, 22, v1
	v_add_u32_e32 v1, v0, v1
	v_and_b32_e32 v1, 0xfffffc00, v1
	v_sub_u32_e32 v1, v0, v1
	v_lshrrev_b32_e32 v2, 4, v1
	v_bitop3_b32 v2, v2, v1, 32 bitop3:0x6c
	v_ashrrev_i32_e32 v1, 31, v1
	v_lshrrev_b32_e32 v1, 26, v1
	v_add_u32_e32 v1, v2, v1
	v_ashrrev_i32_e32 v11, 6, v1
	v_lshlrev_b32_e32 v3, 3, v10
	v_mul_i32_i24_e32 v4, 64, v11
	v_and_b32_e32 v3, -16, v3
	v_sub_u32_e32 v2, v2, v4
	v_mov_b32_e32 v4, 1
	v_add_u32_e32 v1, v11, v3
	v_lshlrev_b32_e32 v3, 5, v10
	v_ashrrev_i16_sdwa v2, v4, sext(v2) dst_sel:DWORD dst_unused:UNUSED_PAD src0_sel:DWORD src1_sel:BYTE_0
	v_and_b32_e32 v3, 32, v3
	v_bfe_i32 v12, v2, 0, 16
	v_and_b32_e32 v6, 3, v11
	s_mov_b32 s1, 0x3fffe0
	v_add_lshl_u32 v3, v3, v12, 1
	v_add_u32_e32 v0, 0x2000, v0
	v_lshlrev_b32_e32 v2, 1, v1
	v_lshrrev_b32_e32 v5, 2, v1
	v_and_or_b32 v6, v1, s1, v6
	v_lshl_add_u32 v32, v1, 10, v3
	v_ashrrev_i32_e32 v1, 31, v0
	v_lshrrev_b32_e32 v1, 22, v1
	v_add_u32_e32 v1, v0, v1
	v_ashrrev_i32_e32 v13, 10, v1
	v_mul_i32_i24_e32 v1, 0x400, v13
	v_sub_u32_e32 v0, v0, v1
	v_and_b32_e32 v2, 24, v2
	v_and_b32_e32 v5, 4, v5
	v_lshrrev_b32_e32 v1, 4, v0
	v_or3_b32 v2, v6, v5, v2
	v_bitop3_b32 v0, v1, v0, 32 bitop3:0x6c
	v_lshl_add_u32 v162, v2, 10, v3
	v_ashrrev_i32_e32 v2, 31, v0
	s_ashr_i32 s0, s3, 3
	v_lshrrev_b32_e32 v2, 26, v2
	s_add_u32 s42, s54, 0x16200000
	v_add_u32_e32 v2, v0, v2
	s_addc_u32 s43, s55, 0
	v_lshlrev_b32_e32 v1, 3, v13
	v_ashrrev_i32_e32 v14, 6, v2
	v_and_b32_e32 v2, 0xc0, v2
	s_add_u32 s46, s54, 0x3700000
	v_and_b32_e32 v1, -16, v1
	v_sub_u32_e32 v0, v0, v2
	s_addc_u32 s47, s55, 0
	v_add_u32_e32 v1, v14, v1
	v_ashrrev_i16_sdwa v0, v4, sext(v0) dst_sel:DWORD dst_unused:UNUSED_PAD src0_sel:DWORD src1_sel:BYTE_0
	v_and_b32_e32 v4, 3, v14
	s_add_i32 s0, s5, s0
	v_and_or_b32 v4, v1, s1, v4
	s_ashr_i32 s1, s0, 31
	s_lshr_b32 s1, s1, 27
	s_add_i32 s1, s0, s1
	s_ashr_i32 s5, s1, 5
	s_andn2_b32 s1, s1, 31
	s_sub_i32 s1, s0, s1
	s_bfe_i32 s0, s1, 0x80000
	s_bfe_u32 s0, s0, 0x3000c
	s_add_i32 s8, s1, s0
	s_bfe_i32 s0, s8, 0x80000
	s_and_b32 s8, s8, 0xf8
	s_sub_i32 s1, s1, s8
	s_lshl_b32 s5, s5, 3
	s_sext_i32_i16 s0, s0
	s_sext_i32_i8 s1, s1
	s_lshr_b32 s0, s0, 3
	s_add_i32 s28, s5, s1
	s_ashr_i32 s4, s2, 6
	s_ashr_i32 s29, s28, 31
	s_bfe_i64 s[10:11], s[0:1], 0x100000
	s_ashr_i32 s3, s2, 8
	s_lshl_b32 s48, s4, 10
	s_lshl_b64 s[8:9], s[28:29], 18
	s_lshl_b64 s[10:11], s[10:11], 18
	s_add_u32 s38, s46, s10
	v_lshlrev_b32_e32 v3, 5, v13
	v_bfe_i32 v15, v0, 0, 16
	v_lshlrev_b32_e32 v0, 1, v1
	v_lshrrev_b32_e32 v2, 2, v1
	s_addc_u32 s39, s47, s11
	s_add_i32 s49, s48, 0
	v_and_b32_e32 v3, 32, v3
	v_and_b32_e32 v0, 24, v0
	v_and_b32_e32 v2, 4, v2
	s_add_i32 m0, s49, 0x10000
	v_or3_b32 v0, v4, v2, v0
	v_add_lshl_u32 v2, v3, v15, 1
	global_load_lds_dwordx4 v162, s[38:39]
	s_add_i32 m0, s49, 0x12000
	v_lshl_add_u32 v166, v0, 10, v2
	s_add_u32 s10, s38, 0x20000
	global_load_lds_dwordx4 v166, s[38:39]
	s_addc_u32 s11, s39, 0
	s_add_i32 m0, s49, 0x14000
	v_lshl_add_u32 v164, v1, 10, v2
	global_load_lds_dwordx4 v162, s[10:11]
	s_add_i32 m0, s49, 0x16000
	s_add_u32 s40, s42, s8
	s_addc_u32 s41, s43, s9
	s_add_i32 s50, s49, 0x2000
	global_load_lds_dwordx4 v166, s[10:11]
	s_mov_b32 m0, s49
	s_add_u32 s8, s40, 0x20000
	global_load_lds_dwordx4 v32, s[40:41]
	s_mov_b32 m0, s50
	s_addc_u32 s9, s41, 0
	s_add_i32 s51, s49, 0x4000
	global_load_lds_dwordx4 v164, s[40:41]
	s_mov_b32 m0, s51
	s_add_i32 s56, s49, 0x6000
	global_load_lds_dwordx4 v32, s[8:9]
	s_mov_b32 m0, s56
	v_mov_b32_e32 v163, 0
	global_load_lds_dwordx4 v164, s[8:9]
	v_mov_b32_e32 v167, v163
	v_mov_b32_e32 v33, v163
	v_mov_b32_e32 v165, v163
	s_cmp_eq_u32 s3, 1
	s_mov_b32 s1, 0
	v_lshl_add_u64 v[6:7], s[38:39], 0, v[162:163]
	v_lshl_add_u64 v[4:5], s[38:39], 0, v[166:167]
	v_lshl_add_u64 v[0:1], s[40:41], 0, v[32:33]
	s_cselect_b64 s[8:9], -1, 0
	s_cmp_lg_u32 s3, 1
	v_lshl_add_u64 v[2:3], s[40:41], 0, v[164:165]
	s_cbranch_scc1 .LBB0_949
	s_barrier

.LBB0_958:
	s_ashr_i32 s23, s22, 31
	s_lshl_b64 s[30:31], s[22:23], 18
	s_add_u32 s30, s42, s30
	s_addc_u32 s31, s43, s31
	s_ashr_i32 s21, s20, 31
	s_lshl_b64 s[34:35], s[20:21], 18
	s_add_u32 s34, s46, s34
	v_mov_b32_e32 v66, 0
	s_addc_u32 s35, s47, s35
	v_lshl_add_u64 v[178:179], s[40:41], 0, v[170:171]
	v_lshl_add_u64 v[180:181], s[40:41], 0, v[172:173]
	s_mov_b32 s21, 0
	v_mov_b32_e32 v67, v66
	v_mov_b32_e32 v68, v66
	v_mov_b32_e32 v69, v66
	v_mov_b32_e32 v70, v66
	v_mov_b32_e32 v71, v66
	v_mov_b32_e32 v72, v66
	v_mov_b32_e32 v73, v66
	v_mov_b32_e32 v82, v66
	v_mov_b32_e32 v83, v66
	v_mov_b32_e32 v84, v66
	v_mov_b32_e32 v85, v66
	v_mov_b32_e32 v86, v66
	v_mov_b32_e32 v87, v66
	v_mov_b32_e32 v88, v66
	v_mov_b32_e32 v89, v66
	v_mov_b32_e32 v34, v66
	v_mov_b32_e32 v35, v66
	v_mov_b32_e32 v36, v66
	v_mov_b32_e32 v37, v66
	v_mov_b32_e32 v38, v66
	v_mov_b32_e32 v39, v66
	v_mov_b32_e32 v40, v66
	v_mov_b32_e32 v41, v66
	v_mov_b32_e32 v50, v66
	v_mov_b32_e32 v51, v66
	v_mov_b32_e32 v52, v66
	v_mov_b32_e32 v53, v66
	v_mov_b32_e32 v58, v66
	v_mov_b32_e32 v59, v66
	v_mov_b32_e32 v60, v66
	v_mov_b32_e32 v61, v66
	v_mov_b32_e32 v74, v66
	v_mov_b32_e32 v75, v66
	v_mov_b32_e32 v76, v66
	v_mov_b32_e32 v77, v66
	v_mov_b32_e32 v78, v66
	v_mov_b32_e32 v79, v66
	v_mov_b32_e32 v80, v66
	v_mov_b32_e32 v81, v66
	v_mov_b32_e32 v90, v66
	v_mov_b32_e32 v91, v66
	v_mov_b32_e32 v92, v66
	v_mov_b32_e32 v93, v66
	v_mov_b32_e32 v94, v66
	v_mov_b32_e32 v95, v66
	v_mov_b32_e32 v96, v66
	v_mov_b32_e32 v97, v66
	v_mov_b32_e32 v98, v66
	v_mov_b32_e32 v99, v66
	v_mov_b32_e32 v100, v66
	v_mov_b32_e32 v101, v66
	v_mov_b32_e32 v102, v66
	v_mov_b32_e32 v103, v66
	v_mov_b32_e32 v104, v66
	v_mov_b32_e32 v105, v66
	v_mov_b32_e32 v114, v66
	v_mov_b32_e32 v115, v66
	v_mov_b32_e32 v116, v66
	v_mov_b32_e32 v117, v66
	v_mov_b32_e32 v118, v66
	v_mov_b32_e32 v119, v66
	v_mov_b32_e32 v120, v66
	v_mov_b32_e32 v121, v66
	v_mov_b32_e32 v130, v66
	v_mov_b32_e32 v131, v66
	v_mov_b32_e32 v132, v66
	v_mov_b32_e32 v133, v66
	v_mov_b32_e32 v134, v66
	v_mov_b32_e32 v135, v66
	v_mov_b32_e32 v136, v66
	v_mov_b32_e32 v137, v66
	v_mov_b32_e32 v146, v66
	v_mov_b32_e32 v147, v66
	v_mov_b32_e32 v148, v66
	v_mov_b32_e32 v149, v66
	v_mov_b32_e32 v150, v66
	v_mov_b32_e32 v151, v66
	v_mov_b32_e32 v152, v66
	v_mov_b32_e32 v153, v66
	v_mov_b32_e32 v106, v66
	v_mov_b32_e32 v107, v66
	v_mov_b32_e32 v108, v66
	v_mov_b32_e32 v109, v66
	v_mov_b32_e32 v110, v66
	v_mov_b32_e32 v111, v66
	v_mov_b32_e32 v112, v66
	v_mov_b32_e32 v113, v66
	v_mov_b32_e32 v122, v66
	v_mov_b32_e32 v123, v66
	v_mov_b32_e32 v124, v66
	v_mov_b32_e32 v125, v66
	v_mov_b32_e32 v126, v66
	v_mov_b32_e32 v127, v66
	v_mov_b32_e32 v128, v66
	v_mov_b32_e32 v129, v66
	v_mov_b32_e32 v138, v66
	v_mov_b32_e32 v139, v66
	v_mov_b32_e32 v140, v66
	v_mov_b32_e32 v141, v66
	v_mov_b32_e32 v142, v66
	v_mov_b32_e32 v143, v66
	v_mov_b32_e32 v144, v66
	v_mov_b32_e32 v145, v66
	v_mov_b32_e32 v154, v66
	v_mov_b32_e32 v155, v66
	v_mov_b32_e32 v156, v66
	v_mov_b32_e32 v157, v66
	v_mov_b32_e32 v158, v66
	v_mov_b32_e32 v159, v66
	v_mov_b32_e32 v160, v66
	v_mov_b32_e32 v161, v66
	v_mov_b32_e32 v62, v66
	v_mov_b32_e32 v63, v66
	v_mov_b32_e32 v64, v66
	v_mov_b32_e32 v65, v66
	v_mov_b32_e32 v54, v66
	v_mov_b32_e32 v55, v66
	v_mov_b32_e32 v56, v66
	v_mov_b32_e32 v57, v66
	v_mov_b32_e32 v46, v66
	v_mov_b32_e32 v47, v66
	v_mov_b32_e32 v48, v66
	v_mov_b32_e32 v49, v66
	v_mov_b32_e32 v42, v66
	v_mov_b32_e32 v43, v66
	v_mov_b32_e32 v44, v66
	v_mov_b32_e32 v45, v66
.LBB0_959:
	ds_read_b128 v[24:27], v187
	ds_read_b128 v[28:31], v187 offset:1024
	ds_read_b128 v[16:19], v187 offset:2048
	ds_read_b128 v[20:23], v187 offset:3072
	s_waitcnt lgkmcnt(0)
	ds_read_b128 v[8:11], v188
	ds_read_b128 v[12:15], v188 offset:1024
	ds_read_b128 v[0:3], v188 offset:2048
	ds_read_b128 v[4:7], v188 offset:3072
	s_add_i32 m0, s49, 0xc000
	ds_read_b128 v[192:195], v189
	ds_read_b128 v[196:199], v189 offset:1024
	ds_read_b128 v[200:203], v189 offset:2048
	ds_read_b128 v[204:207], v189 offset:3072
	ds_read_b128 v[208:211], v189 offset:4096
	ds_read_b128 v[212:215], v189 offset:5120
	ds_read_b128 v[224:227], v189 offset:6144
	ds_read_b128 v[228:231], v189 offset:7168
	global_load_lds_dwordx4 v[178:179], off
	s_add_i32 m0, s49, 0xe000
	s_nop 0
	global_load_lds_dwordx4 v[180:181], off
	s_waitcnt vmcnt(8)
	s_waitcnt lgkmcnt(0)
	s_barrier
	s_setprio 1
	s_waitcnt lgkmcnt(0)
	v_mfma_scale_f32_16x16x128_f8f6f4 v[158:161], v[24:31], v[192:199], v[158:161], v190, v190 op_sel_hi:[0,0,0]
	v_mfma_scale_f32_16x16x128_f8f6f4 v[154:157], v[16:23], v[192:199], v[154:157], v190, v190 op_sel_hi:[0,0,0]
	v_mfma_scale_f32_16x16x128_f8f6f4 v[142:145], v[24:31], v[200:207], v[142:145], v190, v190 op_sel_hi:[0,0,0]
	v_mfma_scale_f32_16x16x128_f8f6f4 v[138:141], v[16:23], v[200:207], v[138:141], v190, v190 op_sel_hi:[0,0,0]
	v_mfma_scale_f32_16x16x128_f8f6f4 v[126:129], v[24:31], v[208:215], v[126:129], v190, v190 op_sel_hi:[0,0,0]
	v_mfma_scale_f32_16x16x128_f8f6f4 v[122:125], v[16:23], v[208:215], v[122:125], v190, v190 op_sel_hi:[0,0,0]
	v_mfma_scale_f32_16x16x128_f8f6f4 v[110:113], v[24:31], v[224:231], v[110:113], v190, v190 op_sel_hi:[0,0,0]
	v_mfma_scale_f32_16x16x128_f8f6f4 v[106:109], v[16:23], v[224:231], v[106:109], v190, v190 op_sel_hi:[0,0,0]
	s_setprio 0
	s_setprio 1
	v_mfma_scale_f32_16x16x128_f8f6f4 v[150:153], v[8:15], v[192:199], v[150:153], v190, v190 op_sel_hi:[0,0,0]
	v_mfma_scale_f32_16x16x128_f8f6f4 v[146:149], v[0:7], v[192:199], v[146:149], v190, v190 op_sel_hi:[0,0,0]
	v_mfma_scale_f32_16x16x128_f8f6f4 v[134:137], v[8:15], v[200:207], v[134:137], v190, v190 op_sel_hi:[0,0,0]
	v_mfma_scale_f32_16x16x128_f8f6f4 v[130:133], v[0:7], v[200:207], v[130:133], v190, v190 op_sel_hi:[0,0,0]
	v_mfma_scale_f32_16x16x128_f8f6f4 v[118:121], v[8:15], v[208:215], v[118:121], v190, v190 op_sel_hi:[0,0,0]
	v_mfma_scale_f32_16x16x128_f8f6f4 v[114:117], v[0:7], v[208:215], v[114:117], v190, v190 op_sel_hi:[0,0,0]
	v_mfma_scale_f32_16x16x128_f8f6f4 v[102:105], v[8:15], v[224:231], v[102:105], v190, v190 op_sel_hi:[0,0,0]
	v_mfma_scale_f32_16x16x128_f8f6f4 v[98:101], v[0:7], v[224:231], v[98:101], v190, v190 op_sel_hi:[0,0,0]
	s_setprio 0
	s_barrier
	s_add_i32 s23, s21, 2
	s_cmp_lt_u32 s21, 6
	s_cselect_b64 s[36:37], -1, 0
	s_and_b64 s[64:65], s[36:37], exec
	s_cselect_b32 s0, 0, -8
	s_cselect_b32 s63, s39, s35
	s_cselect_b32 s66, s38, s34
	s_add_i32 s0, s23, s0
	s_lshl_b64 s[64:65], s[0:1], 7
	s_add_u32 s66, s66, s64
	s_addc_u32 s67, s63, s65
	s_add_i32 s0, s60, s48
	v_lshl_add_u64 v[216:217], s[66:67], 0, v[162:163]
	s_mov_b32 m0, s0
	ds_read_b128 v[192:195], v189 offset:16384
	ds_read_b128 v[196:199], v189 offset:17408
	ds_read_b128 v[200:203], v189 offset:18432
	ds_read_b128 v[204:207], v189 offset:19456
	ds_read_b128 v[208:211], v189 offset:20480
	ds_read_b128 v[212:215], v189 offset:21504
	ds_read_b128 v[224:227], v189 offset:22528
	ds_read_b128 v[228:231], v189 offset:23552
	global_load_lds_dwordx4 v[216:217], off
	s_add_i32 m0, s0, 0x2000
	v_lshl_add_u64 v[216:217], s[66:67], 0, v[166:167]
	s_add_u32 s66, s66, 0x20000
	s_addc_u32 s67, s67, 0
	s_add_i32 s0, s61, s48
	global_load_lds_dwordx4 v[216:217], off
	v_lshl_add_u64 v[216:217], s[66:67], 0, v[162:163]
	s_mov_b32 m0, s0
	s_nop 0
	global_load_lds_dwordx4 v[216:217], off
	s_add_i32 m0, s0, 0x2000
	s_and_b64 vcc, s[36:37], exec
	s_cselect_b32 s36, s40, s30
	s_cselect_b32 s0, s41, s31
	s_add_u32 s36, s36, s64
	v_lshl_add_u64 v[216:217], s[66:67], 0, v[166:167]
	s_addc_u32 s37, s0, s65
	global_load_lds_dwordx4 v[216:217], off
	v_lshl_add_u64 v[216:217], s[36:37], 0, v[32:33]
	s_mov_b32 m0, s49
	s_nop 0
	global_load_lds_dwordx4 v[216:217], off
	v_lshl_add_u64 v[216:217], s[36:37], 0, v[164:165]
	s_mov_b32 m0, s50
	s_nop 0
	global_load_lds_dwordx4 v[216:217], off
	s_waitcnt vmcnt(8)
	s_waitcnt lgkmcnt(0)
	s_barrier
	s_setprio 1
	s_waitcnt lgkmcnt(0)
	v_mfma_scale_f32_16x16x128_f8f6f4 v[94:97], v[24:31], v[192:199], v[94:97], v190, v190 op_sel_hi:[0,0,0]
	v_mfma_scale_f32_16x16x128_f8f6f4 v[90:93], v[16:23], v[192:199], v[90:93], v190, v190 op_sel_hi:[0,0,0]
	v_mfma_scale_f32_16x16x128_f8f6f4 v[78:81], v[24:31], v[200:207], v[78:81], v190, v190 op_sel_hi:[0,0,0]
	v_mfma_scale_f32_16x16x128_f8f6f4 v[74:77], v[16:23], v[200:207], v[74:77], v190, v190 op_sel_hi:[0,0,0]
	v_mfma_scale_f32_16x16x128_f8f6f4 v[58:61], v[24:31], v[208:215], v[58:61], v190, v190 op_sel_hi:[0,0,0]
	v_mfma_scale_f32_16x16x128_f8f6f4 v[50:53], v[16:23], v[208:215], v[50:53], v190, v190 op_sel_hi:[0,0,0]
	v_mfma_scale_f32_16x16x128_f8f6f4 v[38:41], v[24:31], v[224:231], v[38:41], v190, v190 op_sel_hi:[0,0,0]
	v_mfma_scale_f32_16x16x128_f8f6f4 v[34:37], v[16:23], v[224:231], v[34:37], v190, v190 op_sel_hi:[0,0,0]
	s_setprio 0
	s_setprio 1
	v_mfma_scale_f32_16x16x128_f8f6f4 v[86:89], v[8:15], v[192:199], v[86:89], v190, v190 op_sel_hi:[0,0,0]
	v_mfma_scale_f32_16x16x128_f8f6f4 v[82:85], v[0:7], v[192:199], v[82:85], v190, v190 op_sel_hi:[0,0,0]
	v_mfma_scale_f32_16x16x128_f8f6f4 v[70:73], v[8:15], v[200:207], v[70:73], v190, v190 op_sel_hi:[0,0,0]
	v_mfma_scale_f32_16x16x128_f8f6f4 v[66:69], v[0:7], v[200:207], v[66:69], v190, v190 op_sel_hi:[0,0,0]
	v_mfma_scale_f32_16x16x128_f8f6f4 v[62:65], v[8:15], v[208:215], v[62:65], v190, v190 op_sel_hi:[0,0,0]
	v_mfma_scale_f32_16x16x128_f8f6f4 v[54:57], v[0:7], v[208:215], v[54:57], v190, v190 op_sel_hi:[0,0,0]
	v_mfma_scale_f32_16x16x128_f8f6f4 v[46:49], v[8:15], v[224:231], v[46:49], v190, v190 op_sel_hi:[0,0,0]
	v_mfma_scale_f32_16x16x128_f8f6f4 v[42:45], v[0:7], v[224:231], v[42:45], v190, v190 op_sel_hi:[0,0,0]
	s_setprio 0
	s_barrier
	s_add_i32 s63, 0, 0x18000
	s_add_i32 s68, 0, 0x1c000
	v_add_u32_e32 v0, s63, v183
	v_add_u32_e32 v4, s68, v183
	ds_read_b128 v[24:27], v0
	ds_read_b128 v[28:31], v0 offset:1024
	ds_read_b128 v[16:19], v0 offset:2048
	ds_read_b128 v[20:23], v0 offset:3072
	ds_read_b128 v[8:11], v4
	ds_read_b128 v[12:15], v4 offset:1024
	ds_read_b128 v[0:3], v4 offset:2048
	ds_read_b128 v[4:7], v4 offset:3072
	s_add_u32 s36, s36, 0x20000
	s_addc_u32 s37, s37, 0
	s_mov_b32 m0, s51
	v_lshl_add_u64 v[216:217], s[36:37], 0, v[32:33]
	ds_read_b128 v[192:195], v189 offset:32768
	ds_read_b128 v[196:199], v189 offset:33792
	ds_read_b128 v[200:203], v189 offset:34816
	ds_read_b128 v[204:207], v189 offset:35840
	ds_read_b128 v[208:211], v189 offset:36864
	ds_read_b128 v[212:215], v189 offset:37888
	ds_read_b128 v[224:227], v189 offset:38912
	ds_read_b128 v[228:231], v189 offset:39936
	global_load_lds_dwordx4 v[216:217], off
	v_lshl_add_u64 v[216:217], s[36:37], 0, v[164:165]
	s_mov_b32 m0, s56
	s_nop 0
	global_load_lds_dwordx4 v[216:217], off
	s_waitcnt vmcnt(8)
	s_waitcnt lgkmcnt(0)
	s_barrier
	s_setprio 1
	s_waitcnt lgkmcnt(0)
	v_mfma_scale_f32_16x16x128_f8f6f4 v[158:161], v[24:31], v[192:199], v[158:161], v190, v190 op_sel_hi:[0,0,0]
	v_mfma_scale_f32_16x16x128_f8f6f4 v[154:157], v[16:23], v[192:199], v[154:157], v190, v190 op_sel_hi:[0,0,0]
	v_mfma_scale_f32_16x16x128_f8f6f4 v[142:145], v[24:31], v[200:207], v[142:145], v190, v190 op_sel_hi:[0,0,0]
	v_mfma_scale_f32_16x16x128_f8f6f4 v[138:141], v[16:23], v[200:207], v[138:141], v190, v190 op_sel_hi:[0,0,0]
	v_mfma_scale_f32_16x16x128_f8f6f4 v[126:129], v[24:31], v[208:215], v[126:129], v190, v190 op_sel_hi:[0,0,0]
	v_mfma_scale_f32_16x16x128_f8f6f4 v[122:125], v[16:23], v[208:215], v[122:125], v190, v190 op_sel_hi:[0,0,0]
	v_mfma_scale_f32_16x16x128_f8f6f4 v[110:113], v[24:31], v[224:231], v[110:113], v190, v190 op_sel_hi:[0,0,0]
	v_mfma_scale_f32_16x16x128_f8f6f4 v[106:109], v[16:23], v[224:231], v[106:109], v190, v190 op_sel_hi:[0,0,0]
	s_setprio 0
	s_setprio 1
	v_mfma_scale_f32_16x16x128_f8f6f4 v[150:153], v[8:15], v[192:199], v[150:153], v190, v190 op_sel_hi:[0,0,0]
	v_mfma_scale_f32_16x16x128_f8f6f4 v[146:149], v[0:7], v[192:199], v[146:149], v190, v190 op_sel_hi:[0,0,0]
	v_mfma_scale_f32_16x16x128_f8f6f4 v[134:137], v[8:15], v[200:207], v[134:137], v190, v190 op_sel_hi:[0,0,0]
	v_mfma_scale_f32_16x16x128_f8f6f4 v[130:133], v[0:7], v[200:207], v[130:133], v190, v190 op_sel_hi:[0,0,0]
	v_mfma_scale_f32_16x16x128_f8f6f4 v[118:121], v[8:15], v[208:215], v[118:121], v190, v190 op_sel_hi:[0,0,0]
	v_mfma_scale_f32_16x16x128_f8f6f4 v[114:117], v[0:7], v[208:215], v[114:117], v190, v190 op_sel_hi:[0,0,0]
	v_mfma_scale_f32_16x16x128_f8f6f4 v[102:105], v[8:15], v[224:231], v[102:105], v190, v190 op_sel_hi:[0,0,0]
	v_mfma_scale_f32_16x16x128_f8f6f4 v[98:101], v[0:7], v[224:231], v[98:101], v190, v190 op_sel_hi:[0,0,0]
	s_setprio 0
	s_barrier
	s_cmp_lt_u32 s21, 5
	s_cselect_b64 s[36:37], -1, 0
	s_and_b64 s[64:65], s[36:37], exec
	s_cselect_b32 s0, 0, -8
	s_cselect_b32 s67, s39, s35
	s_cselect_b32 s66, s38, s34
	s_add_i32 s0, s0, s21
	s_add_i32 s0, s0, 3
	s_lshl_b64 s[64:65], s[0:1], 7
	s_add_u32 s66, s66, s64
	s_addc_u32 s67, s67, s65
	s_add_i32 s0, s63, s48
	v_lshl_add_u64 v[216:217], s[66:67], 0, v[162:163]
	s_mov_b32 m0, s0
	ds_read_b128 v[192:195], v189 offset:49152
	ds_read_b128 v[196:199], v189 offset:50176
	ds_read_b128 v[200:203], v189 offset:51200
	ds_read_b128 v[204:207], v189 offset:52224
	ds_read_b128 v[208:211], v189 offset:53248
	ds_read_b128 v[212:215], v189 offset:54272
	ds_read_b128 v[224:227], v189 offset:55296
	ds_read_b128 v[228:231], v189 offset:56320
	global_load_lds_dwordx4 v[216:217], off
	s_add_i32 m0, s0, 0x2000
	v_lshl_add_u64 v[216:217], s[66:67], 0, v[166:167]
	s_add_u32 s66, s66, 0x20000
	s_addc_u32 s67, s67, 0
	s_add_i32 s0, s68, s48
	global_load_lds_dwordx4 v[216:217], off
	v_lshl_add_u64 v[216:217], s[66:67], 0, v[162:163]
	s_mov_b32 m0, s0
	s_nop 0
	global_load_lds_dwordx4 v[216:217], off
	s_add_i32 m0, s0, 0x2000
	s_and_b64 s[36:37], s[36:37], exec
	s_cselect_b32 s21, s40, s30
	s_cselect_b32 s0, s41, s31
	s_add_u32 s36, s21, s64
	v_lshl_add_u64 v[216:217], s[66:67], 0, v[166:167]
	s_addc_u32 s37, s0, s65
	global_load_lds_dwordx4 v[216:217], off
	v_lshl_add_u64 v[216:217], s[36:37], 0, v[32:33]
	s_mov_b32 m0, s57
	s_nop 0
	global_load_lds_dwordx4 v[216:217], off
	v_lshl_add_u64 v[216:217], s[36:37], 0, v[164:165]
	s_mov_b32 m0, s58
	s_nop 0
	global_load_lds_dwordx4 v[216:217], off
	s_waitcnt vmcnt(8)
	s_waitcnt lgkmcnt(0)
	s_barrier
	s_setprio 1
	s_waitcnt lgkmcnt(0)
	v_mfma_scale_f32_16x16x128_f8f6f4 v[94:97], v[24:31], v[192:199], v[94:97], v190, v190 op_sel_hi:[0,0,0]
	v_mfma_scale_f32_16x16x128_f8f6f4 v[90:93], v[16:23], v[192:199], v[90:93], v190, v190 op_sel_hi:[0,0,0]
	v_mfma_scale_f32_16x16x128_f8f6f4 v[78:81], v[24:31], v[200:207], v[78:81], v190, v190 op_sel_hi:[0,0,0]
	v_mfma_scale_f32_16x16x128_f8f6f4 v[74:77], v[16:23], v[200:207], v[74:77], v190, v190 op_sel_hi:[0,0,0]
	v_mfma_scale_f32_16x16x128_f8f6f4 v[58:61], v[24:31], v[208:215], v[58:61], v190, v190 op_sel_hi:[0,0,0]
	v_mfma_scale_f32_16x16x128_f8f6f4 v[50:53], v[16:23], v[208:215], v[50:53], v190, v190 op_sel_hi:[0,0,0]
	v_mfma_scale_f32_16x16x128_f8f6f4 v[38:41], v[24:31], v[224:231], v[38:41], v190, v190 op_sel_hi:[0,0,0]
	v_mfma_scale_f32_16x16x128_f8f6f4 v[34:37], v[16:23], v[224:231], v[34:37], v190, v190 op_sel_hi:[0,0,0]
	s_setprio 0
	s_setprio 1
	v_mfma_scale_f32_16x16x128_f8f6f4 v[86:89], v[8:15], v[192:199], v[86:89], v190, v190 op_sel_hi:[0,0,0]
	v_mfma_scale_f32_16x16x128_f8f6f4 v[82:85], v[0:7], v[192:199], v[82:85], v190, v190 op_sel_hi:[0,0,0]
	v_mfma_scale_f32_16x16x128_f8f6f4 v[70:73], v[8:15], v[200:207], v[70:73], v190, v190 op_sel_hi:[0,0,0]
	v_mfma_scale_f32_16x16x128_f8f6f4 v[66:69], v[0:7], v[200:207], v[66:69], v190, v190 op_sel_hi:[0,0,0]
	v_mfma_scale_f32_16x16x128_f8f6f4 v[62:65], v[8:15], v[208:215], v[62:65], v190, v190 op_sel_hi:[0,0,0]
	v_mfma_scale_f32_16x16x128_f8f6f4 v[54:57], v[0:7], v[208:215], v[54:57], v190, v190 op_sel_hi:[0,0,0]
	v_mfma_scale_f32_16x16x128_f8f6f4 v[46:49], v[8:15], v[224:231], v[46:49], v190, v190 op_sel_hi:[0,0,0]
	v_mfma_scale_f32_16x16x128_f8f6f4 v[42:45], v[0:7], v[224:231], v[42:45], v190, v190 op_sel_hi:[0,0,0]
	s_setprio 0
	s_barrier
	v_lshl_add_u64 v[178:179], v[178:179], 0, s[16:17]
	v_lshl_add_u64 v[180:181], v[180:181], 0, s[16:17]
	s_mov_b32 s21, s23
	s_cbranch_vccnz .LBB0_959
	s_andn2_b64 vcc, exec, s[14:15]
	s_cbranch_vccnz .LBB0_962
	s_barrier
.LBB0_962:
	s_lshl_b32 s28, s28, 8
	v_lshl_or_b32 v20, s29, 8, v186
	v_add_u32_e32 v24, s28, v182
	v_ashrrev_i32_e32 v21, 31, v20
	v_ashrrev_i32_e32 v25, 31, v24
	v_lshl_add_u64 v[22:23], v[20:21], 1, s[10:11]
	v_lshlrev_b64 v[0:1], 11, v[24:25]
	s_nop 15
	s_nop 7
	v_lshl_add_u64 v[204:205], v[22:23], 0, v[0:1]
	global_load_dwordx4 v[178:181], v[204:205], off
	global_load_dwordx4 v[192:195], v[204:205], off offset:256
	v_or_b32_e32 v208, 16, v24
	v_or_b32_e32 v28, 32, v24
	v_or_b32_e32 v18, 48, v24
	v_ashrrev_i32_e32 v209, 31, v208
	v_ashrrev_i32_e32 v29, 31, v28
	v_ashrrev_i32_e32 v19, 31, v18
	v_lshlrev_b64 v[0:1], 10, v[24:25]
	v_lshlrev_b64 v[2:3], 11, v[208:209]
	v_lshlrev_b64 v[4:5], 11, v[28:29]
	v_lshlrev_b64 v[6:7], 11, v[18:19]
	v_lshl_add_u64 v[0:1], v[0:1], 0, v[20:21]
	v_lshl_add_u64 v[30:31], v[22:23], 0, v[2:3]
	v_lshl_add_u64 v[26:27], v[22:23], 0, v[4:5]
	v_lshl_add_u64 v[16:17], v[22:23], 0, v[6:7]
	v_lshl_add_u64 v[210:211], s[12:13], 0, v[0:1]
	global_load_dwordx4 v[196:199], v[30:31], off
	global_load_dwordx4 v[200:203], v[30:31], off offset:256
	global_load_dwordx4 v[12:15], v[26:27], off
	global_load_dwordx4 v[8:11], v[26:27], off offset:256
	global_load_dwordx4 v[4:7], v[16:17], off
	global_load_dwordx4 v[0:3], v[16:17], off offset:256
	v_mov_b32_e32 v206, 0
	v_mov_b32_e32 v207, 0
	v_lshlrev_b64 v[28:29], 10, v[28:29]
	v_lshlrev_b64 v[18:19], 10, v[18:19]
	v_lshl_add_u64 v[18:19], v[18:19], 0, v[20:21]
	s_waitcnt vmcnt(0)
	v_lshlrev_b32_e32 v212, 16, v178
	v_and_b32_e32 v213, 0xffff0000, v178
	v_lshlrev_b32_e32 v214, 16, v180
	v_and_b32_e32 v215, 0xffff0000, v180
	v_lshlrev_b32_e32 v178, 16, v179
	v_and_b32_e32 v179, 0xffff0000, v179
	v_lshlrev_b32_e32 v180, 16, v181
	v_and_b32_e32 v181, 0xffff0000, v181
	v_lshlrev_b32_e32 v216, 16, v192
	v_and_b32_e32 v217, 0xffff0000, v192
	v_lshlrev_b32_e32 v192, 16, v193
	v_and_b32_e32 v193, 0xffff0000, v193
	v_lshlrev_b32_e32 v218, 16, v194
	v_and_b32_e32 v219, 0xffff0000, v194
	v_lshlrev_b32_e32 v194, 16, v195
	v_and_b32_e32 v195, 0xffff0000, v195
	v_pk_fma_f32 v[158:159], v[158:159], s[18:19], v[212:213] op_sel_hi:[1,0,1]
	v_pk_fma_f32 v[154:155], v[154:155], s[18:19], v[214:215] op_sel_hi:[1,0,1]
	v_pk_fma_f32 v[160:161], v[160:161], s[18:19], v[178:179] op_sel_hi:[1,0,1]
	v_pk_fma_f32 v[156:157], v[156:157], s[18:19], v[180:181] op_sel_hi:[1,0,1]
	v_pk_fma_f32 v[152:153], v[152:153], s[18:19], v[192:193] op_sel_hi:[1,0,1]
	v_pk_fma_f32 v[178:179], v[148:149], s[18:19], v[194:195] op_sel_hi:[1,0,1]
	v_pk_fma_f32 v[180:181], v[146:147], s[18:19], v[218:219] op_sel_hi:[1,0,1]
	v_mul_f32_e32 v25, v159, v159
	v_mul_f32_e32 v192, v155, v155
	v_cvt_pk_bf16_f32 v146, v158, v159
	v_cvt_pk_bf16_f32 v147, v160, v161
	v_cvt_pk_bf16_f32 v148, v154, v155
	v_mul_f32_e32 v194, 0x41000000, v158
	v_mul_f32_e32 v159, 0x41000000, v159
	v_mul_f32_e32 v212, 0x41000000, v154
	v_mul_f32_e32 v155, 0x41000000, v155
	v_cvt_pk_fp8_f32 v206, v194, v159
	v_cvt_pk_fp8_f32 v207, v212, v155
	v_pk_fma_f32 v[150:151], v[150:151], s[18:19], v[216:217] op_sel_hi:[1,0,1]
	v_mul_f32_e32 v191, v161, v161
	v_mul_f32_e32 v193, v157, v157
	v_cvt_pk_bf16_f32 v149, v156, v157
	v_mul_f32_e32 v195, 0x41000000, v160
	v_mul_f32_e32 v161, 0x41000000, v161
	v_mul_f32_e32 v213, 0x41000000, v156
	v_mul_f32_e32 v157, 0x41000000, v157
	v_mul_f32_e32 v214, v151, v151
	v_mul_f32_e32 v215, v153, v153
	v_mul_f32_e32 v216, v181, v181
	v_mul_f32_e32 v217, v179, v179
	v_cvt_pk_fp8_f32 v206, v195, v161 op_sel:[0,0,1]
	v_cvt_pk_fp8_f32 v207, v213, v157 op_sel:[0,0,1]
	v_fmac_f32_e32 v25, v158, v158
	v_fmac_f32_e32 v191, v160, v160
	v_fmac_f32_e32 v192, v154, v154
	v_fmac_f32_e32 v193, v156, v156
	v_fmac_f32_e32 v214, v150, v150
	v_fmac_f32_e32 v215, v152, v152
	v_fmac_f32_e32 v216, v180, v180
	v_fmac_f32_e32 v217, v178, v178
	global_store_dwordx4 v[204:205], v[146:149], off
	v_add_f32_e32 v25, v25, v191
	global_store_dwordx2 v[210:211], v[206:207], off
	v_add_f32_e32 v146, v192, v193
	v_add_f32_e32 v147, v214, v215
	v_add_f32_e32 v148, v216, v217
	v_add_f32_e32 v25, v25, v146
	v_add_f32_e32 v146, v147, v148
	v_add_f32_e32 v25, v25, v146
	v_cvt_pk_bf16_f32 v146, v150, v151
	v_mul_f32_e32 v148, 0x41000000, v150
	v_mul_f32_e32 v149, 0x41000000, v151
	v_mov_b32_e32 v150, 0
	v_cvt_pk_fp8_f32 v150, v148, v149
	v_mul_f32_e32 v148, 0x41000000, v180
	v_mul_f32_e32 v149, 0x41000000, v181
	v_mov_b32_e32 v151, 0
	v_cvt_pk_fp8_f32 v151, v148, v149
	v_cvt_pk_bf16_f32 v147, v152, v153
	v_mul_f32_e32 v152, 0x41000000, v152
	v_mul_f32_e32 v153, 0x41000000, v153
	v_cvt_pk_fp8_f32 v150, v152, v153 op_sel:[0,0,1]
	ds_bpermute_b32 v152, v184, v25
	v_mul_f32_e32 v148, 0x41000000, v178
	v_mul_f32_e32 v149, 0x41000000, v179
	v_cvt_pk_fp8_f32 v151, v148, v149 op_sel:[0,0,1]
	v_cvt_pk_bf16_f32 v148, v180, v181
	v_cvt_pk_bf16_f32 v149, v178, v179
	global_store_dwordx4 v[204:205], v[146:149], off offset:256
	global_store_dwordx2 v[210:211], v[150:151], off offset:128
	v_lshlrev_b32_e32 v150, 16, v196
	s_waitcnt lgkmcnt(0)
	v_add_f32_e32 v146, v25, v152
	v_and_b32_e32 v151, 0xffff0000, v196
	v_lshlrev_b32_e32 v152, 16, v197
	v_and_b32_e32 v153, 0xffff0000, v197
	v_lshlrev_b32_e32 v154, 16, v198
	v_and_b32_e32 v155, 0xffff0000, v198
	v_pk_fma_f32 v[144:145], v[144:145], s[18:19], v[152:153] op_sel_hi:[1,0,1]
	v_pk_fma_f32 v[142:143], v[142:143], s[18:19], v[150:151] op_sel_hi:[1,0,1]
	v_lshlrev_b32_e32 v156, 16, v199
	v_and_b32_e32 v157, 0xffff0000, v199
	v_pk_fma_f32 v[152:153], v[138:139], s[18:19], v[154:155] op_sel_hi:[1,0,1]
	v_mul_f32_e32 v25, v143, v143
	v_mul_f32_e32 v138, v145, v145
	v_pk_fma_f32 v[150:151], v[140:141], s[18:19], v[156:157] op_sel_hi:[1,0,1]
	v_fmac_f32_e32 v25, v142, v142
	v_fmac_f32_e32 v138, v144, v144
	v_add_f32_e32 v25, v25, v138
	v_mul_f32_e32 v138, v153, v153
	v_mul_f32_e32 v139, v151, v151
	v_fmac_f32_e32 v138, v152, v152
	v_fmac_f32_e32 v139, v150, v150
	v_add_f32_e32 v138, v138, v139
	v_add_f32_e32 v25, v25, v138
	v_cvt_pk_bf16_f32 v138, v142, v143
	v_mul_f32_e32 v141, 0x41000000, v142
	v_mul_f32_e32 v143, 0x41000000, v143
	v_mov_b32_e32 v142, 0
	v_cvt_pk_bf16_f32 v139, v144, v145
	v_cvt_pk_bf16_f32 v140, v152, v153
	v_cvt_pk_fp8_f32 v142, v141, v143
	v_mul_f32_e32 v141, 0x41000000, v152
	v_mul_f32_e32 v152, 0x41000000, v153
	v_mov_b32_e32 v143, 0
	v_cvt_pk_fp8_f32 v143, v141, v152
	v_mul_f32_e32 v144, 0x41000000, v144
	v_mul_f32_e32 v145, 0x41000000, v145
	v_cvt_pk_fp8_f32 v142, v144, v145 op_sel:[0,0,1]
	v_mul_f32_e32 v141, 0x41000000, v150
	v_mul_f32_e32 v144, 0x41000000, v151
	v_cvt_pk_fp8_f32 v143, v141, v144 op_sel:[0,0,1]
	v_lshlrev_b64 v[148:149], 10, v[208:209]
	v_lshl_add_u64 v[148:149], v[148:149], 0, v[20:21]
	v_cvt_pk_bf16_f32 v141, v150, v151
	global_store_dwordx4 v[30:31], v[138:141], off
	v_lshlrev_b32_e32 v144, 16, v202
	v_and_b32_e32 v145, 0xffff0000, v202
	v_lshl_add_u64 v[138:139], s[12:13], 0, v[148:149]
	global_store_dwordx2 v[138:139], v[142:143], off
	v_lshlrev_b32_e32 v140, 16, v200
	v_and_b32_e32 v141, 0xffff0000, v200
	v_lshlrev_b32_e32 v142, 16, v201
	v_and_b32_e32 v143, 0xffff0000, v201
	v_lshlrev_b32_e32 v148, 16, v203
	v_and_b32_e32 v149, 0xffff0000, v203
	v_pk_fma_f32 v[136:137], v[136:137], s[18:19], v[142:143] op_sel_hi:[1,0,1]
	v_pk_fma_f32 v[134:135], v[134:135], s[18:19], v[140:141] op_sel_hi:[1,0,1]
	v_pk_fma_f32 v[140:141], v[132:133], s[18:19], v[148:149] op_sel_hi:[1,0,1]
	v_pk_fma_f32 v[132:133], v[130:131], s[18:19], v[144:145] op_sel_hi:[1,0,1]
	v_mul_f32_e32 v130, v135, v135
	v_mul_f32_e32 v131, v137, v137
	v_fmac_f32_e32 v130, v134, v134
	v_fmac_f32_e32 v131, v136, v136
	v_add_f32_e32 v142, v130, v131
	v_cvt_pk_bf16_f32 v130, v134, v135
	v_mul_f32_e32 v145, 0x41000000, v134
	v_mul_f32_e32 v135, 0x41000000, v135
	v_mov_b32_e32 v134, 0
	v_cvt_pk_fp8_f32 v134, v145, v135
	v_mul_f32_e32 v145, 0x41000000, v132
	v_mul_f32_e32 v148, 0x41000000, v133
	v_mov_b32_e32 v135, 0
	v_cvt_pk_fp8_f32 v135, v145, v148
	v_cvt_pk_bf16_f32 v131, v136, v137
	v_mul_f32_e32 v136, 0x41000000, v136
	v_mul_f32_e32 v137, 0x41000000, v137
	v_cvt_pk_fp8_f32 v134, v136, v137 op_sel:[0,0,1]
	v_mul_f32_e32 v136, 0x41000000, v140
	v_mul_f32_e32 v137, 0x41000000, v141
	v_cvt_pk_fp8_f32 v135, v136, v137 op_sel:[0,0,1]
	v_mul_f32_e32 v143, v133, v133
	v_fmac_f32_e32 v143, v132, v132
	v_cvt_pk_bf16_f32 v132, v132, v133
	v_cvt_pk_bf16_f32 v133, v140, v141
	global_store_dwordx4 v[30:31], v[130:133], off offset:256
	global_store_dwordx2 v[138:139], v[134:135], off offset:128
	v_lshlrev_b32_e32 v30, 16, v14
	v_lshl_add_u64 v[130:131], v[28:29], 0, v[20:21]
	v_lshlrev_b32_e32 v28, 16, v12
	v_and_b32_e32 v29, 0xffff0000, v12
	v_and_b32_e32 v31, 0xffff0000, v14
	v_lshlrev_b32_e32 v14, 16, v15
	v_and_b32_e32 v15, 0xffff0000, v15
	v_pk_fma_f32 v[28:29], v[126:127], s[18:19], v[28:29] op_sel_hi:[1,0,1]
	v_pk_fma_f32 v[14:15], v[124:125], s[18:19], v[14:15] op_sel_hi:[1,0,1]
	v_pk_fma_f32 v[30:31], v[122:123], s[18:19], v[30:31] op_sel_hi:[1,0,1]
	v_mul_f32_e32 v125, 0x41000000, v28
	v_mul_f32_e32 v127, 0x41000000, v29
	v_mov_b32_e32 v126, 0
	v_cvt_pk_fp8_f32 v126, v125, v127
	v_mul_f32_e32 v125, 0x41000000, v30
	v_mul_f32_e32 v132, 0x41000000, v31
	v_mov_b32_e32 v127, 0
	v_lshlrev_b32_e32 v12, 16, v13
	v_and_b32_e32 v13, 0xffff0000, v13
	v_cvt_pk_fp8_f32 v127, v125, v132
	v_pk_fma_f32 v[12:13], v[128:129], s[18:19], v[12:13] op_sel_hi:[1,0,1]
	v_mul_f32_e32 v125, 0x41000000, v14
	v_mul_f32_e32 v128, 0x41000000, v12
	v_mul_f32_e32 v129, 0x41000000, v13
	v_cvt_pk_fp8_f32 v126, v128, v129 op_sel:[0,0,1]
	v_mul_f32_e32 v128, 0x41000000, v15
	v_cvt_pk_fp8_f32 v127, v125, v128 op_sel:[0,0,1]
	v_cvt_pk_bf16_f32 v122, v28, v29
	v_cvt_pk_bf16_f32 v123, v12, v13
	v_cvt_pk_bf16_f32 v124, v30, v31
	v_cvt_pk_bf16_f32 v125, v14, v15
	global_store_dwordx4 v[26:27], v[122:125], off
	v_mul_f32_e32 v144, v141, v141
	v_fmac_f32_e32 v144, v140, v140
	v_lshl_add_u64 v[124:125], s[12:13], 0, v[130:131]
	v_lshlrev_b32_e32 v122, 16, v8
	v_and_b32_e32 v123, 0xffff0000, v8
	global_store_dwordx2 v[124:125], v[126:127], off
	v_lshlrev_b32_e32 v126, 16, v10
	v_and_b32_e32 v127, 0xffff0000, v10
	v_lshlrev_b32_e32 v10, 16, v11
	v_and_b32_e32 v11, 0xffff0000, v11
	v_pk_fma_f32 v[118:119], v[118:119], s[18:19], v[122:123] op_sel_hi:[1,0,1]
	v_pk_fma_f32 v[10:11], v[116:117], s[18:19], v[10:11] op_sel_hi:[1,0,1]
	v_pk_fma_f32 v[114:115], v[114:115], s[18:19], v[126:127] op_sel_hi:[1,0,1]
	v_mul_f32_e32 v117, 0x41000000, v118
	v_mul_f32_e32 v122, 0x41000000, v119
	v_mov_b32_e32 v116, 0
	v_cvt_pk_fp8_f32 v116, v117, v122
	v_mul_f32_e32 v122, 0x41000000, v114
	v_mul_f32_e32 v127, 0x41000000, v115
	v_mov_b32_e32 v117, 0
	v_lshlrev_b32_e32 v8, 16, v9
	v_and_b32_e32 v9, 0xffff0000, v9
	v_cvt_pk_fp8_f32 v117, v122, v127
	v_pk_fma_f32 v[8:9], v[120:121], s[18:19], v[8:9] op_sel_hi:[1,0,1]
	v_mul_f32_e32 v122, 0x41000000, v10
	v_mul_f32_e32 v123, 0x41000000, v8
	v_mul_f32_e32 v126, 0x41000000, v9
	v_cvt_pk_fp8_f32 v116, v123, v126 op_sel:[0,0,1]
	v_mul_f32_e32 v123, 0x41000000, v11
	v_cvt_pk_fp8_f32 v117, v122, v123 op_sel:[0,0,1]
	v_cvt_pk_bf16_f32 v120, v118, v119
	v_cvt_pk_bf16_f32 v121, v8, v9
	v_cvt_pk_bf16_f32 v122, v114, v115
	v_cvt_pk_bf16_f32 v123, v10, v11
	global_store_dwordx4 v[26:27], v[120:123], off offset:256
	global_store_dwordx2 v[124:125], v[116:117], off offset:128
	v_lshlrev_b32_e32 v26, 16, v4
	v_and_b32_e32 v27, 0xffff0000, v4
	v_lshlrev_b32_e32 v116, 16, v6
	v_and_b32_e32 v117, 0xffff0000, v6
	v_lshlrev_b32_e32 v6, 16, v7
	v_and_b32_e32 v7, 0xffff0000, v7
	v_pk_fma_f32 v[26:27], v[110:111], s[18:19], v[26:27] op_sel_hi:[1,0,1]
	v_pk_fma_f32 v[108:109], v[108:109], s[18:19], v[6:7] op_sel_hi:[1,0,1]
	v_pk_fma_f32 v[110:111], v[106:107], s[18:19], v[116:117] op_sel_hi:[1,0,1]
	v_mul_f32_e32 v7, 0x41000000, v26
	v_mul_f32_e32 v107, 0x41000000, v27
	v_mov_b32_e32 v106, 0
	v_cvt_pk_fp8_f32 v106, v7, v107
	v_mul_f32_e32 v7, 0x41000000, v110
	v_mul_f32_e32 v120, 0x41000000, v111
	v_mov_b32_e32 v107, 0
	v_lshlrev_b32_e32 v4, 16, v5
	v_and_b32_e32 v5, 0xffff0000, v5
	v_cvt_pk_fp8_f32 v107, v7, v120
	v_pk_fma_f32 v[112:113], v[112:113], s[18:19], v[4:5] op_sel_hi:[1,0,1]
	v_mul_f32_e32 v7, 0x41000000, v108
	v_mul_f32_e32 v116, 0x41000000, v112
	v_mul_f32_e32 v117, 0x41000000, v113
	v_cvt_pk_fp8_f32 v106, v116, v117 op_sel:[0,0,1]
	v_mul_f32_e32 v116, 0x41000000, v109
	v_cvt_pk_bf16_f32 v4, v26, v27
	v_cvt_pk_bf16_f32 v5, v112, v113
	v_cvt_pk_bf16_f32 v6, v110, v111
	v_cvt_pk_fp8_f32 v107, v7, v116 op_sel:[0,0,1]
	v_cvt_pk_bf16_f32 v7, v108, v109
	global_store_dwordx4 v[16:17], v[4:7], off
	v_add_u32_e32 v120, 0x80, v24
	v_ashrrev_i32_e32 v121, 31, v120
	v_lshlrev_b32_e32 v6, 16, v0
	v_and_b32_e32 v7, 0xffff0000, v0
	v_lshl_add_u64 v[4:5], s[12:13], 0, v[18:19]
	v_lshlrev_b32_e32 v18, 16, v2
	v_and_b32_e32 v19, 0xffff0000, v2
	v_lshlrev_b32_e32 v2, 16, v3
	v_and_b32_e32 v3, 0xffff0000, v3
	v_pk_fma_f32 v[6:7], v[102:103], s[18:19], v[6:7] op_sel_hi:[1,0,1]
	v_pk_fma_f32 v[100:101], v[100:101], s[18:19], v[2:3] op_sel_hi:[1,0,1]
	v_pk_fma_f32 v[18:19], v[98:99], s[18:19], v[18:19] op_sel_hi:[1,0,1]
	v_mul_f32_e32 v2, 0x41000000, v6
	v_mul_f32_e32 v3, 0x41000000, v7
	v_mov_b32_e32 v98, 0
	v_cvt_pk_fp8_f32 v98, v2, v3
	v_mul_f32_e32 v2, 0x41000000, v18
	v_mul_f32_e32 v3, 0x41000000, v19
	v_mov_b32_e32 v99, 0
	v_cvt_pk_fp8_f32 v99, v2, v3
	v_lshlrev_b32_e32 v0, 16, v1
	v_and_b32_e32 v1, 0xffff0000, v1
	v_pk_fma_f32 v[116:117], v[104:105], s[18:19], v[0:1] op_sel_hi:[1,0,1]
	v_mul_f32_e32 v2, 0x41000000, v100
	v_mul_f32_e32 v102, 0x41000000, v116
	v_mul_f32_e32 v103, 0x41000000, v117
	v_mul_f32_e32 v3, 0x41000000, v101
	v_cvt_pk_fp8_f32 v98, v102, v103 op_sel:[0,0,1]
	v_cvt_pk_fp8_f32 v99, v2, v3 op_sel:[0,0,1]
	global_store_dwordx2 v[4:5], v[106:107], off
	v_cvt_pk_bf16_f32 v0, v6, v7
	v_cvt_pk_bf16_f32 v1, v116, v117
	v_cvt_pk_bf16_f32 v2, v18, v19
	v_cvt_pk_bf16_f32 v3, v100, v101
	global_store_dwordx4 v[16:17], v[0:3], off offset:256
	global_store_dwordx2 v[4:5], v[98:99], off offset:128
	v_mul_f32_e32 v4, v15, v15
	v_lshlrev_b64 v[0:1], 11, v[120:121]
	v_lshl_add_u64 v[122:123], v[22:23], 0, v[0:1]
	global_load_dwordx4 v[104:107], v[122:123], off
	v_mul_f32_e32 v2, v29, v29
	v_mul_f32_e32 v3, v13, v13
	v_fmac_f32_e32 v2, v28, v28
	v_fmac_f32_e32 v3, v12, v12
	v_add_f32_e32 v2, v2, v3
	v_mul_f32_e32 v3, v31, v31
	v_fmac_f32_e32 v3, v30, v30
	v_fmac_f32_e32 v4, v14, v14
	v_add_f32_e32 v3, v3, v4
	v_add_f32_e32 v2, v2, v3
	v_mul_f32_e32 v3, v119, v119
	v_mul_f32_e32 v4, v9, v9
	v_fmac_f32_e32 v3, v118, v118
	v_fmac_f32_e32 v4, v8, v8
	v_add_f32_e32 v3, v3, v4
	v_mul_f32_e32 v4, v115, v115
	v_mul_f32_e32 v5, v11, v11
	v_fmac_f32_e32 v4, v114, v114
	v_fmac_f32_e32 v5, v10, v10
	v_add_f32_e32 v4, v4, v5
	v_add_f32_e32 v3, v3, v4
	v_mul_f32_e32 v4, v27, v27
	v_mul_f32_e32 v5, v113, v113
	v_fmac_f32_e32 v4, v26, v26
	v_fmac_f32_e32 v5, v112, v112
	v_add_f32_e32 v4, v4, v5
	v_mul_f32_e32 v5, v111, v111
	v_mul_f32_e32 v8, v109, v109
	v_fmac_f32_e32 v5, v110, v110
	v_fmac_f32_e32 v8, v108, v108
	global_load_dwordx4 v[108:111], v[122:123], off offset:256
	v_add_f32_e32 v0, v143, v144
	v_add_f32_e32 v0, v142, v0
	v_add_f32_e32 v0, v25, v0
	ds_bpermute_b32 v1, v184, v0
	v_add_f32_e32 v5, v5, v8
	v_add_f32_e32 v4, v4, v5
	v_mul_f32_e32 v5, v7, v7
	v_fmac_f32_e32 v5, v6, v6
	v_mul_f32_e32 v6, v117, v117
	v_fmac_f32_e32 v6, v116, v116
	v_add_u32_e32 v116, 0x90, v24
	v_ashrrev_i32_e32 v117, 31, v116
	s_waitcnt lgkmcnt(0)
	v_add_f32_e32 v98, v0, v1
	v_lshlrev_b64 v[0:1], 11, v[116:117]
	v_add_f32_e32 v5, v5, v6
	v_mul_f32_e32 v6, v19, v19
	v_lshl_add_u64 v[30:31], v[22:23], 0, v[0:1]
	v_fmac_f32_e32 v6, v18, v18
	global_load_dwordx4 v[112:115], v[30:31], off
	global_load_dwordx4 v[16:19], v[30:31], off offset:256
	v_add_u32_e32 v28, 0xa0, v24
	v_ashrrev_i32_e32 v29, 31, v28
	v_lshlrev_b64 v[0:1], 11, v[28:29]
	v_lshl_add_u64 v[26:27], v[22:23], 0, v[0:1]
	global_load_dwordx4 v[12:15], v[26:27], off
	global_load_dwordx4 v[8:11], v[26:27], off offset:256
	v_mul_f32_e32 v7, v101, v101
	v_fmac_f32_e32 v7, v100, v100
	v_add_f32_e32 v6, v6, v7
	v_add_f32_e32 v5, v5, v6
	v_lshlrev_b64 v[118:119], 10, v[120:121]
	v_add_f32_e32 v2, v2, v3
	v_add_f32_e32 v4, v4, v5
	ds_bpermute_b32 v3, v184, v2
	ds_bpermute_b32 v5, v184, v4
	v_add_u32_e32 v24, 0xb0, v24
	v_ashrrev_i32_e32 v25, 31, v24
	v_lshlrev_b64 v[0:1], 11, v[24:25]
	v_lshl_add_u64 v[22:23], v[22:23], 0, v[0:1]
	s_waitcnt lgkmcnt(1)
	v_add_f32_e32 v100, v2, v3
	s_waitcnt lgkmcnt(0)
	v_add_f32_e32 v102, v4, v5
	global_load_dwordx4 v[4:7], v[22:23], off
	global_load_dwordx4 v[0:3], v[22:23], off offset:256
	v_lshl_add_u64 v[118:119], v[118:119], 0, v[20:21]
	ds_bpermute_b32 v147, v185, v146
	ds_bpermute_b32 v99, v185, v98
	ds_bpermute_b32 v101, v185, v100
	ds_bpermute_b32 v103, v185, v102
	s_waitcnt vmcnt(7)
	v_lshlrev_b32_e32 v120, 16, v104
	v_and_b32_e32 v121, 0xffff0000, v104
	v_lshlrev_b32_e32 v104, 16, v105
	v_and_b32_e32 v105, 0xffff0000, v105
	v_lshlrev_b32_e32 v124, 16, v106
	v_and_b32_e32 v125, 0xffff0000, v106
	v_lshlrev_b32_e32 v106, 16, v107
	v_and_b32_e32 v107, 0xffff0000, v107
	v_pk_fma_f32 v[96:97], v[96:97], s[18:19], v[104:105] op_sel_hi:[1,0,1]
	v_pk_fma_f32 v[94:95], v[94:95], s[18:19], v[120:121] op_sel_hi:[1,0,1]
	v_pk_fma_f32 v[104:105], v[92:93], s[18:19], v[106:107] op_sel_hi:[1,0,1]
	v_pk_fma_f32 v[106:107], v[90:91], s[18:19], v[124:125] op_sel_hi:[1,0,1]
	v_mul_f32_e32 v90, v95, v95
	v_mul_f32_e32 v91, v97, v97
	v_fmac_f32_e32 v90, v94, v94
	v_fmac_f32_e32 v91, v96, v96
	v_add_f32_e32 v90, v90, v91
	v_mul_f32_e32 v91, v107, v107
	v_mul_f32_e32 v92, v105, v105
	v_fmac_f32_e32 v91, v106, v106
	v_fmac_f32_e32 v92, v104, v104
	v_add_f32_e32 v91, v91, v92
	v_add_f32_e32 v120, v90, v91
	v_cvt_pk_bf16_f32 v90, v94, v95
	v_mul_f32_e32 v93, 0x41000000, v94
	v_mul_f32_e32 v95, 0x41000000, v95
	v_mov_b32_e32 v94, 0
	v_cvt_pk_bf16_f32 v91, v96, v97
	v_cvt_pk_bf16_f32 v92, v106, v107
	v_cvt_pk_fp8_f32 v94, v93, v95
	v_mul_f32_e32 v93, 0x41000000, v106
	v_mul_f32_e32 v106, 0x41000000, v107
	v_mov_b32_e32 v95, 0
	v_cvt_pk_fp8_f32 v95, v93, v106
	v_mul_f32_e32 v96, 0x41000000, v96
	v_mul_f32_e32 v97, 0x41000000, v97
	v_cvt_pk_fp8_f32 v94, v96, v97 op_sel:[0,0,1]
	v_mul_f32_e32 v93, 0x41000000, v104
	v_mul_f32_e32 v96, 0x41000000, v105
	v_cvt_pk_fp8_f32 v95, v93, v96 op_sel:[0,0,1]
	v_cvt_pk_bf16_f32 v93, v104, v105
	global_store_dwordx4 v[122:123], v[90:93], off
	s_waitcnt vmcnt(7)
	v_lshlrev_b32_e32 v96, 16, v110
	v_and_b32_e32 v97, 0xffff0000, v110
	v_lshl_add_u64 v[90:91], s[12:13], 0, v[118:119]
	global_store_dwordx2 v[90:91], v[94:95], off
	v_lshlrev_b32_e32 v92, 16, v108
	v_and_b32_e32 v93, 0xffff0000, v108
	v_lshlrev_b32_e32 v94, 16, v109
	v_and_b32_e32 v95, 0xffff0000, v109
	v_lshlrev_b32_e32 v104, 16, v111
	v_and_b32_e32 v105, 0xffff0000, v111
	v_pk_fma_f32 v[88:89], v[88:89], s[18:19], v[94:95] op_sel_hi:[1,0,1]
	v_pk_fma_f32 v[86:87], v[86:87], s[18:19], v[92:93] op_sel_hi:[1,0,1]
	v_pk_fma_f32 v[92:93], v[84:85], s[18:19], v[104:105] op_sel_hi:[1,0,1]
	v_pk_fma_f32 v[84:85], v[82:83], s[18:19], v[96:97] op_sel_hi:[1,0,1]
	v_mul_f32_e32 v82, v87, v87
	v_mul_f32_e32 v83, v89, v89
	v_fmac_f32_e32 v82, v86, v86
	v_fmac_f32_e32 v83, v88, v88
	v_add_f32_e32 v82, v82, v83
	v_mul_f32_e32 v83, v85, v85
	v_mul_f32_e32 v94, v93, v93
	v_fmac_f32_e32 v83, v84, v84
	v_fmac_f32_e32 v94, v92, v92
	v_add_f32_e32 v83, v83, v94
	v_add_f32_e32 v82, v82, v83
	v_add_f32_e32 v94, v120, v82
	v_cvt_pk_bf16_f32 v82, v86, v87
	v_mul_f32_e32 v95, 0x41000000, v86
	v_mul_f32_e32 v87, 0x41000000, v87
	v_mov_b32_e32 v86, 0
	v_cvt_pk_fp8_f32 v86, v95, v87
	v_mul_f32_e32 v95, 0x41000000, v84
	v_mul_f32_e32 v96, 0x41000000, v85
	v_mov_b32_e32 v87, 0
	v_cvt_pk_fp8_f32 v87, v95, v96
	v_cvt_pk_bf16_f32 v83, v88, v89
	v_mul_f32_e32 v88, 0x41000000, v88
	v_mul_f32_e32 v89, 0x41000000, v89
	v_cvt_pk_fp8_f32 v86, v88, v89 op_sel:[0,0,1]
	v_mul_f32_e32 v88, 0x41000000, v92
	v_mul_f32_e32 v89, 0x41000000, v93
	v_cvt_pk_fp8_f32 v87, v88, v89 op_sel:[0,0,1]
	ds_bpermute_b32 v88, v184, v94
	v_cvt_pk_bf16_f32 v84, v84, v85
	v_cvt_pk_bf16_f32 v85, v92, v93
	global_store_dwordx4 v[122:123], v[82:85], off offset:256
	global_store_dwordx2 v[90:91], v[86:87], off offset:128
	s_waitcnt vmcnt(9)
	v_lshlrev_b32_e32 v86, 16, v112
	s_waitcnt lgkmcnt(0)
	v_add_f32_e32 v82, v94, v88
	v_and_b32_e32 v87, 0xffff0000, v112
	v_lshlrev_b32_e32 v88, 16, v113
	v_and_b32_e32 v89, 0xffff0000, v113
	v_lshlrev_b32_e32 v90, 16, v114
	v_and_b32_e32 v91, 0xffff0000, v114
	v_pk_fma_f32 v[80:81], v[80:81], s[18:19], v[88:89] op_sel_hi:[1,0,1]
	v_pk_fma_f32 v[78:79], v[78:79], s[18:19], v[86:87] op_sel_hi:[1,0,1]
	v_lshlrev_b32_e32 v92, 16, v115
	v_and_b32_e32 v93, 0xffff0000, v115
	v_pk_fma_f32 v[88:89], v[74:75], s[18:19], v[90:91] op_sel_hi:[1,0,1]
	v_mul_f32_e32 v74, v79, v79
	v_mul_f32_e32 v75, v81, v81
	v_pk_fma_f32 v[86:87], v[76:77], s[18:19], v[92:93] op_sel_hi:[1,0,1]
	v_fmac_f32_e32 v74, v78, v78
	v_fmac_f32_e32 v75, v80, v80
	v_add_f32_e32 v74, v74, v75
	v_mul_f32_e32 v75, v89, v89
	v_mul_f32_e32 v76, v87, v87
	v_fmac_f32_e32 v75, v88, v88
	v_fmac_f32_e32 v76, v86, v86
	v_add_f32_e32 v75, v75, v76
	v_add_f32_e32 v90, v74, v75
	v_cvt_pk_bf16_f32 v74, v78, v79
	v_mul_f32_e32 v77, 0x41000000, v78
	v_mul_f32_e32 v79, 0x41000000, v79
	v_mov_b32_e32 v78, 0
	v_cvt_pk_bf16_f32 v75, v80, v81
	v_cvt_pk_bf16_f32 v76, v88, v89
	v_cvt_pk_fp8_f32 v78, v77, v79
	v_mul_f32_e32 v77, 0x41000000, v88
	v_mul_f32_e32 v88, 0x41000000, v89
	v_mov_b32_e32 v79, 0
	v_cvt_pk_fp8_f32 v79, v77, v88
	v_mul_f32_e32 v80, 0x41000000, v80
	v_mul_f32_e32 v81, 0x41000000, v81
	v_cvt_pk_fp8_f32 v78, v80, v81 op_sel:[0,0,1]
	v_mul_f32_e32 v77, 0x41000000, v86
	v_mul_f32_e32 v80, 0x41000000, v87
	v_cvt_pk_fp8_f32 v79, v77, v80 op_sel:[0,0,1]
	v_lshlrev_b64 v[84:85], 10, v[116:117]
	v_cvt_pk_bf16_f32 v77, v86, v87
	v_lshl_add_u64 v[84:85], v[84:85], 0, v[20:21]
	global_store_dwordx4 v[30:31], v[74:77], off
	ds_bpermute_b32 v83, v185, v82
	s_waitcnt vmcnt(9)
	v_lshlrev_b32_e32 v76, 16, v16
	v_and_b32_e32 v77, 0xffff0000, v16
	v_lshlrev_b32_e32 v16, 16, v17
	v_and_b32_e32 v17, 0xffff0000, v17
	v_lshl_add_u64 v[74:75], s[12:13], 0, v[84:85]
	v_pk_fma_f32 v[72:73], v[72:73], s[18:19], v[16:17] op_sel_hi:[1,0,1]
	v_pk_fma_f32 v[70:71], v[70:71], s[18:19], v[76:77] op_sel_hi:[1,0,1]
	global_store_dwordx2 v[74:75], v[78:79], off
	v_lshlrev_b32_e32 v78, 16, v18
	v_and_b32_e32 v79, 0xffff0000, v18
	v_lshlrev_b32_e32 v18, 16, v19
	v_and_b32_e32 v19, 0xffff0000, v19
	v_mul_f32_e32 v16, v71, v71
	v_mul_f32_e32 v17, v73, v73
	v_pk_fma_f32 v[68:69], v[68:69], s[18:19], v[18:19] op_sel_hi:[1,0,1]
	v_pk_fma_f32 v[18:19], v[66:67], s[18:19], v[78:79] op_sel_hi:[1,0,1]
	v_fmac_f32_e32 v16, v70, v70
	v_fmac_f32_e32 v17, v72, v72
	v_add_f32_e32 v16, v16, v17
	v_mul_f32_e32 v17, v19, v19
	v_mul_f32_e32 v66, v69, v69
	v_fmac_f32_e32 v17, v18, v18
	v_fmac_f32_e32 v66, v68, v68
	v_add_f32_e32 v17, v17, v66
	v_add_f32_e32 v16, v16, v17
	v_add_f32_e32 v76, v90, v16
	v_cvt_pk_bf16_f32 v16, v70, v71
	v_mul_f32_e32 v67, 0x41000000, v70
	v_mul_f32_e32 v70, 0x41000000, v71
	v_mov_b32_e32 v66, 0
	v_cvt_pk_bf16_f32 v17, v72, v73
	v_mul_f32_e32 v71, 0x41000000, v72
	v_mul_f32_e32 v72, 0x41000000, v73
	v_cvt_pk_fp8_f32 v66, v67, v70
	v_mul_f32_e32 v70, 0x41000000, v18
	v_mul_f32_e32 v73, 0x41000000, v19
	v_mov_b32_e32 v67, 0
	v_cvt_pk_fp8_f32 v67, v70, v73
	v_cvt_pk_fp8_f32 v66, v71, v72 op_sel:[0,0,1]
	v_mul_f32_e32 v70, 0x41000000, v68
	v_mul_f32_e32 v71, 0x41000000, v69
	v_cvt_pk_fp8_f32 v67, v70, v71 op_sel:[0,0,1]
	v_cvt_pk_bf16_f32 v18, v18, v19
	v_cvt_pk_bf16_f32 v19, v68, v69
	global_store_dwordx4 v[30:31], v[16:19], off offset:256
	global_store_dwordx2 v[74:75], v[66:67], off offset:128
	s_waitcnt vmcnt(11)
	v_lshlrev_b32_e32 v30, 16, v14
	v_lshlrev_b64 v[18:19], 10, v[28:29]
	v_lshlrev_b32_e32 v28, 16, v12
	v_and_b32_e32 v29, 0xffff0000, v12
	v_lshlrev_b32_e32 v12, 16, v13
	v_and_b32_e32 v13, 0xffff0000, v13
	v_pk_fma_f32 v[60:61], v[60:61], s[18:19], v[12:13] op_sel_hi:[1,0,1]
	v_pk_fma_f32 v[28:29], v[58:59], s[18:19], v[28:29] op_sel_hi:[1,0,1]
	v_and_b32_e32 v31, 0xffff0000, v14
	v_lshlrev_b32_e32 v14, 16, v15
	v_and_b32_e32 v15, 0xffff0000, v15
	v_mul_f32_e32 v12, v29, v29
	v_mul_f32_e32 v13, v61, v61
	v_pk_fma_f32 v[52:53], v[52:53], s[18:19], v[14:15] op_sel_hi:[1,0,1]
	v_pk_fma_f32 v[30:31], v[50:51], s[18:19], v[30:31] op_sel_hi:[1,0,1]
	v_fmac_f32_e32 v12, v28, v28
	v_fmac_f32_e32 v13, v60, v60
	v_add_f32_e32 v12, v12, v13
	v_mul_f32_e32 v13, v31, v31
	v_mul_f32_e32 v14, v53, v53
	v_fmac_f32_e32 v13, v30, v30
	v_fmac_f32_e32 v14, v52, v52
	v_add_f32_e32 v13, v13, v14
	v_add_f32_e32 v50, v12, v13
	v_cvt_pk_bf16_f32 v12, v28, v29
	v_mul_f32_e32 v15, 0x41000000, v28
	v_mul_f32_e32 v29, 0x41000000, v29
	v_mov_b32_e32 v28, 0
	v_cvt_pk_bf16_f32 v13, v60, v61
	v_cvt_pk_bf16_f32 v14, v30, v31
	v_cvt_pk_fp8_f32 v28, v15, v29
	v_mul_f32_e32 v15, 0x41000000, v30
	v_mul_f32_e32 v30, 0x41000000, v31
	v_mov_b32_e32 v29, 0
	v_cvt_pk_fp8_f32 v29, v15, v30
	v_mul_f32_e32 v51, 0x41000000, v60
	v_mul_f32_e32 v58, 0x41000000, v61
	v_mul_f32_e32 v15, 0x41000000, v52
	v_mul_f32_e32 v30, 0x41000000, v53
	v_cvt_pk_fp8_f32 v28, v51, v58 op_sel:[0,0,1]
	v_cvt_pk_fp8_f32 v29, v15, v30 op_sel:[0,0,1]
	v_lshl_add_u64 v[18:19], v[18:19], 0, v[20:21]
	v_cvt_pk_bf16_f32 v15, v52, v53
	global_store_dwordx4 v[26:27], v[12:15], off
	ds_bpermute_b32 v70, v184, v76
	s_waitcnt lgkmcnt(0)
	v_add_f32_e32 v16, v76, v70
	v_lshl_add_u64 v[12:13], s[12:13], 0, v[18:19]
	s_waitcnt vmcnt(11)
	v_lshlrev_b32_e32 v14, 16, v8
	v_and_b32_e32 v15, 0xffff0000, v8
	v_lshlrev_b32_e32 v8, 16, v9
	v_and_b32_e32 v9, 0xffff0000, v9
	global_store_dwordx2 v[12:13], v[28:29], off
	v_pk_fma_f32 v[28:29], v[64:65], s[18:19], v[8:9] op_sel_hi:[1,0,1]
	v_pk_fma_f32 v[14:15], v[62:63], s[18:19], v[14:15] op_sel_hi:[1,0,1]
	v_lshlrev_b32_e32 v18, 16, v10
	v_and_b32_e32 v19, 0xffff0000, v10
	v_lshlrev_b32_e32 v10, 16, v11
	v_and_b32_e32 v11, 0xffff0000, v11
	v_mul_f32_e32 v8, v15, v15
	v_mul_f32_e32 v9, v29, v29
	v_pk_fma_f32 v[30:31], v[56:57], s[18:19], v[10:11] op_sel_hi:[1,0,1]
	v_pk_fma_f32 v[10:11], v[54:55], s[18:19], v[18:19] op_sel_hi:[1,0,1]
	v_fmac_f32_e32 v8, v14, v14
	v_fmac_f32_e32 v9, v28, v28
	v_add_f32_e32 v8, v8, v9
	v_mul_f32_e32 v9, v11, v11
	v_mul_f32_e32 v18, v31, v31
	v_fmac_f32_e32 v9, v10, v10
	v_fmac_f32_e32 v18, v30, v30
	v_add_f32_e32 v9, v9, v18
	v_add_f32_e32 v8, v8, v9
	v_add_f32_e32 v18, v50, v8
	v_cvt_pk_bf16_f32 v8, v14, v15
	v_mul_f32_e32 v19, 0x41000000, v14
	v_mul_f32_e32 v15, 0x41000000, v15
	v_mov_b32_e32 v14, 0
	v_cvt_pk_fp8_f32 v14, v19, v15
	v_mul_f32_e32 v19, 0x41000000, v10
	v_mul_f32_e32 v50, 0x41000000, v11
	v_mov_b32_e32 v15, 0
	v_cvt_pk_fp8_f32 v15, v19, v50
	v_cvt_pk_bf16_f32 v9, v28, v29
	v_mul_f32_e32 v28, 0x41000000, v28
	v_mul_f32_e32 v29, 0x41000000, v29
	v_cvt_pk_fp8_f32 v14, v28, v29 op_sel:[0,0,1]
	v_mul_f32_e32 v19, 0x41000000, v30
	v_mul_f32_e32 v28, 0x41000000, v31
	v_cvt_pk_fp8_f32 v15, v19, v28 op_sel:[0,0,1]
	ds_bpermute_b32 v19, v184, v18
	v_cvt_pk_bf16_f32 v10, v10, v11
	v_cvt_pk_bf16_f32 v11, v30, v31
	global_store_dwordx4 v[26:27], v[8:11], off offset:256
	global_store_dwordx2 v[12:13], v[14:15], off offset:128
	s_waitcnt vmcnt(13)
	v_lshlrev_b32_e32 v12, 16, v4
	v_and_b32_e32 v13, 0xffff0000, v4
	v_lshlrev_b32_e32 v4, 16, v5
	v_and_b32_e32 v5, 0xffff0000, v5
	s_waitcnt lgkmcnt(0)
	v_add_f32_e32 v8, v18, v19
	v_pk_fma_f32 v[18:19], v[40:41], s[18:19], v[4:5] op_sel_hi:[1,0,1]
	v_pk_fma_f32 v[12:13], v[38:39], s[18:19], v[12:13] op_sel_hi:[1,0,1]
	v_lshlrev_b64 v[10:11], 10, v[24:25]
	v_lshlrev_b32_e32 v14, 16, v6
	v_and_b32_e32 v15, 0xffff0000, v6
	v_lshlrev_b32_e32 v6, 16, v7
	v_and_b32_e32 v7, 0xffff0000, v7
	v_mul_f32_e32 v4, v13, v13
	v_mul_f32_e32 v5, v19, v19
	v_lshl_add_u64 v[10:11], v[10:11], 0, v[20:21]
	v_pk_fma_f32 v[20:21], v[36:37], s[18:19], v[6:7] op_sel_hi:[1,0,1]
	v_pk_fma_f32 v[14:15], v[34:35], s[18:19], v[14:15] op_sel_hi:[1,0,1]
	v_fmac_f32_e32 v4, v12, v12
	v_fmac_f32_e32 v5, v18, v18
	v_add_f32_e32 v4, v4, v5
	v_mul_f32_e32 v5, v15, v15
	v_mul_f32_e32 v6, v21, v21
	v_fmac_f32_e32 v5, v14, v14
	v_fmac_f32_e32 v6, v20, v20
	v_add_f32_e32 v5, v5, v6
	v_add_f32_e32 v24, v4, v5
	v_cvt_pk_bf16_f32 v4, v12, v13
	v_mul_f32_e32 v7, 0x41000000, v12
	v_mul_f32_e32 v13, 0x41000000, v13
	v_mov_b32_e32 v12, 0
	v_cvt_pk_bf16_f32 v5, v18, v19
	v_cvt_pk_bf16_f32 v6, v14, v15
	v_cvt_pk_fp8_f32 v12, v7, v13
	v_mul_f32_e32 v7, 0x41000000, v14
	v_mul_f32_e32 v14, 0x41000000, v15
	v_mov_b32_e32 v13, 0
	v_cvt_pk_fp8_f32 v13, v7, v14
	v_mul_f32_e32 v18, 0x41000000, v18
	v_mul_f32_e32 v19, 0x41000000, v19
	v_mul_f32_e32 v7, 0x41000000, v20
	v_mul_f32_e32 v14, 0x41000000, v21
	v_cvt_pk_fp8_f32 v12, v18, v19 op_sel:[0,0,1]
	v_cvt_pk_fp8_f32 v13, v7, v14 op_sel:[0,0,1]
	v_cvt_pk_bf16_f32 v7, v20, v21
	global_store_dwordx4 v[22:23], v[4:7], off
	v_mov_b32_e32 v15, 0
	ds_bpermute_b32 v17, v185, v16
	s_waitcnt vmcnt(13)
	v_lshlrev_b32_e32 v4, 16, v0
	v_and_b32_e32 v5, 0xffff0000, v0
	v_lshlrev_b32_e32 v0, 16, v1
	v_and_b32_e32 v1, 0xffff0000, v1
	v_lshl_add_u64 v[6:7], s[12:13], 0, v[10:11]
	v_lshlrev_b32_e32 v10, 16, v2
	v_and_b32_e32 v11, 0xffff0000, v2
	v_lshlrev_b32_e32 v2, 16, v3
	v_and_b32_e32 v3, 0xffff0000, v3
	v_pk_fma_f32 v[0:1], v[48:49], s[18:19], v[0:1] op_sel_hi:[1,0,1]
	v_pk_fma_f32 v[4:5], v[46:47], s[18:19], v[4:5] op_sel_hi:[1,0,1]
	global_store_dwordx2 v[6:7], v[12:13], off
	v_pk_fma_f32 v[12:13], v[44:45], s[18:19], v[2:3] op_sel_hi:[1,0,1]
	v_mul_f32_e32 v2, v5, v5
	v_mul_f32_e32 v3, v1, v1
	v_pk_fma_f32 v[10:11], v[42:43], s[18:19], v[10:11] op_sel_hi:[1,0,1]
	v_fmac_f32_e32 v2, v4, v4
	v_fmac_f32_e32 v3, v0, v0
	v_add_f32_e32 v2, v2, v3
	v_mul_f32_e32 v3, v11, v11
	v_mul_f32_e32 v14, v13, v13
	v_fmac_f32_e32 v3, v10, v10
	v_fmac_f32_e32 v14, v12, v12
	v_add_f32_e32 v3, v3, v14
	v_add_f32_e32 v2, v2, v3
	v_add_f32_e32 v18, v24, v2
	v_cvt_pk_bf16_f32 v2, v4, v5
	v_mul_f32_e32 v4, 0x41000000, v4
	v_mul_f32_e32 v5, 0x41000000, v5
	v_mov_b32_e32 v14, 0
	v_cvt_pk_fp8_f32 v14, v4, v5
	v_mul_f32_e32 v4, 0x41000000, v10
	v_mul_f32_e32 v5, 0x41000000, v11
	v_cvt_pk_fp8_f32 v15, v4, v5
	ds_bpermute_b32 v4, v184, v18
	v_cvt_pk_bf16_f32 v3, v0, v1
	v_mul_f32_e32 v0, 0x41000000, v0
	v_mul_f32_e32 v1, 0x41000000, v1
	v_cvt_pk_fp8_f32 v14, v0, v1 op_sel:[0,0,1]
	v_mul_f32_e32 v0, 0x41000000, v12
	v_mul_f32_e32 v1, 0x41000000, v13
	v_cvt_pk_fp8_f32 v15, v0, v1 op_sel:[0,0,1]
	s_waitcnt lgkmcnt(0)
	v_add_f32_e32 v0, v18, v4
	ds_bpermute_b32 v9, v185, v8
	ds_bpermute_b32 v1, v185, v0
	v_cvt_pk_bf16_f32 v4, v10, v11
	v_cvt_pk_bf16_f32 v5, v12, v13
	global_store_dwordx4 v[22:23], v[2:5], off offset:256
	global_store_dwordx2 v[6:7], v[14:15], off offset:128
	s_and_saveexec_b64 s[36:37], s[2:3]
	s_cbranch_execz .LBB0_964
	v_add_f32_e32 v2, v146, v147
	v_add_f32_e32 v4, v98, v99
	v_mul_f32_e32 v2, 0x49800000, v2
	v_add_f32_e32 v6, v100, v101
	v_trunc_f32_e32 v2, v2
	v_mul_f32_e32 v4, 0x49800000, v4
	s_waitcnt lgkmcnt(1)
	v_add_f32_e32 v11, v8, v9
	v_add_f32_e32 v8, v102, v103
	v_mul_f32_e32 v3, 0x2f800000, v2
	v_trunc_f32_e32 v4, v4
	v_mul_f32_e32 v6, 0x49800000, v6
	v_floor_f32_e32 v3, v3
	v_mul_f32_e32 v5, 0x2f800000, v4
	v_trunc_f32_e32 v6, v6
	v_mul_f32_e32 v8, 0x49800000, v8
	v_fmac_f32_e32 v2, 0xcf800000, v3
	v_floor_f32_e32 v5, v5
	v_mul_f32_e32 v7, 0x2f800000, v6
	v_trunc_f32_e32 v8, v8
	v_cvt_u32_f32_e32 v2, v2
	v_cvt_u32_f32_e32 v3, v3
	v_fmac_f32_e32 v4, 0xcf800000, v5
	v_floor_f32_e32 v7, v7
	v_mul_f32_e32 v9, 0x2f800000, v8
	v_cvt_u32_f32_e32 v4, v4
	v_cvt_u32_f32_e32 v5, v5
	v_fmac_f32_e32 v6, 0xcf800000, v7
	v_floor_f32_e32 v9, v9
	s_ashr_i32 s29, s28, 31
	v_cvt_u32_f32_e32 v6, v6
	v_cvt_u32_f32_e32 v7, v7
	v_fmac_f32_e32 v8, 0xcf800000, v9
	s_waitcnt lgkmcnt(0)
	v_add_f32_e32 v10, v0, v1
	v_add_f32_e32 v13, v82, v83
	v_lshl_add_u64 v[0:1], s[28:29], 3, v[168:169]
	v_cvt_u32_f32_e32 v8, v8
	v_cvt_u32_f32_e32 v9, v9
	v_add_f32_e32 v12, v16, v17
	global_atomic_add_x2 v[0:1], v[2:3], off
	global_atomic_add_x2 v[0:1], v[4:5], off offset:128
	global_atomic_add_x2 v[0:1], v[6:7], off offset:256
	global_atomic_add_x2 v[0:1], v[8:9], off offset:384
	v_mul_f32_e32 v2, 0x49800000, v13
	v_trunc_f32_e32 v2, v2
	v_mul_f32_e32 v4, 0x49800000, v12
	v_mul_f32_e32 v3, 0x2f800000, v2
	v_trunc_f32_e32 v4, v4
	v_mul_f32_e32 v6, 0x49800000, v11
	v_floor_f32_e32 v3, v3
	v_mul_f32_e32 v5, 0x2f800000, v4
	v_trunc_f32_e32 v6, v6
	v_mul_f32_e32 v8, 0x49800000, v10
	v_fmac_f32_e32 v2, 0xcf800000, v3
	v_floor_f32_e32 v5, v5
	v_mul_f32_e32 v7, 0x2f800000, v6
	v_trunc_f32_e32 v8, v8
	v_cvt_u32_f32_e32 v2, v2
	v_cvt_u32_f32_e32 v3, v3
	v_fmac_f32_e32 v4, 0xcf800000, v5
	v_floor_f32_e32 v7, v7
	v_mul_f32_e32 v9, 0x2f800000, v8
	v_cvt_u32_f32_e32 v4, v4
	v_cvt_u32_f32_e32 v5, v5
	v_fmac_f32_e32 v6, 0xcf800000, v7
	v_floor_f32_e32 v9, v9
	v_cvt_u32_f32_e32 v6, v6
	v_cvt_u32_f32_e32 v7, v7
	v_fmac_f32_e32 v8, 0xcf800000, v9
	v_cvt_u32_f32_e32 v8, v8
	v_cvt_u32_f32_e32 v9, v9
	global_atomic_add_x2 v[0:1], v[2:3], off offset:1024
	global_atomic_add_x2 v[0:1], v[4:5], off offset:1152
	global_atomic_add_x2 v[0:1], v[6:7], off offset:1280
	global_atomic_add_x2 v[0:1], v[8:9], off offset:1408

.LBB0_1168:
	v_mul_i32_i24_e32 v14, 64, v0
	v_sub_u32_e32 v3, v3, v14
	v_mov_b32_e32 v14, 1
	v_lshlrev_b32_e32 v2, 5, v2
	v_ashrrev_i16_sdwa v3, v14, sext(v3) dst_sel:DWORD dst_unused:UNUSED_PAD src0_sel:DWORD src1_sel:BYTE_0
	v_and_b32_e32 v2, 32, v2
	v_bfe_i32 v3, v3, 0, 16
	v_add_lshl_u32 v218, v2, v3, 1
	v_lshlrev_b32_e32 v3, 6, v1
	v_sub_u32_e32 v3, v9, v3
	v_lshlrev_b32_e32 v2, 5, v8
	v_ashrrev_i16_sdwa v3, v14, sext(v3) dst_sel:DWORD dst_unused:UNUSED_PAD src0_sel:DWORD src1_sel:BYTE_0
	s_cmp_ge_i32 s81, s46
	v_and_b32_e32 v2, 32, v2
	v_bfe_i32 v3, v3, 0, 16
	s_cselect_b64 s[0:1], -1, 0
	s_cmp_ge_i32 s81, s47
	v_add_lshl_u32 v219, v2, v3, 1
	v_cndmask_b32_e64 v2, 0, 1, s[0:1]
	s_cselect_b64 s[0:1], -1, 0
	s_cmp_ge_i32 s81, s48
	v_cndmask_b32_e64 v3, 0, 1, s[0:1]
	s_cselect_b64 vcc, -1, 0
	s_cmp_ge_i32 s81, s49
	v_addc_co_u32_e32 v2, vcc, v3, v2, vcc
	s_cselect_b64 s[0:1], -1, 0
	s_cmp_ge_i32 s81, s50
	v_cndmask_b32_e64 v3, 0, 1, s[0:1]
	s_cselect_b64 vcc, -1, 0
	s_cmp_ge_i32 s81, s51
	v_addc_co_u32_e32 v2, vcc, v2, v3, vcc
	s_cselect_b64 s[0:1], -1, 0
	s_cmp_ge_i32 s81, s62
	v_cndmask_b32_e64 v3, 0, 1, s[0:1]
	s_cselect_b64 vcc, -1, 0
	v_addc_co_u32_e32 v221, vcc, v2, v3, vcc
	s_waitcnt vmcnt(0)
	v_max_i32_e32 v2, 0, v10
	v_lshl_add_u32 v206, v2, 10, v218
	v_max_i32_e32 v2, 0, v11
	v_lshl_add_u32 v208, v2, 10, v219
	v_max_i32_e32 v2, 0, v12
	v_lshl_add_u32 v64, v2, 10, v218
	v_max_i32_e32 v2, 0, v13
	s_mov_b32 s6, 0x700000
	v_lshl_add_u32 v210, v2, 10, v219
	v_mul_hi_u32 v3, v221, s6
	v_mul_lo_u32 v2, v221, s6
	s_ashr_i32 s29, s28, 31
	v_lshl_add_u64 v[2:3], s[10:11], 0, v[2:3]
	s_lshl_b64 s[0:1], s[28:29], 18
	v_lshl_add_u64 v[212:213], v[2:3], 0, s[0:1]
	v_lshlrev_b32_e32 v2, 1, v4
	v_lshrrev_b32_e32 v3, 2, v4
	v_and_b32_e32 v0, 3, v0
	s_mov_b32 s0, 0x3fffe0
	v_and_b32_e32 v2, 24, v2
	v_and_b32_e32 v3, 4, v3
	v_and_or_b32 v0, v4, s0, v0
	v_or3_b32 v0, v0, v3, v2
	v_lshl_add_u32 v194, v0, 10, v218
	v_lshlrev_b32_e32 v0, 1, v5
	v_lshrrev_b32_e32 v2, 2, v5
	v_and_b32_e32 v1, 3, v1
	s_lshl_b32 s7, s18, 10
	v_and_b32_e32 v0, 24, v0
	v_and_b32_e32 v2, 4, v2
	v_and_or_b32 v1, v5, s0, v1
	s_add_i32 s29, s7, 0
	v_or3_b32 v0, v1, v2, v0
	s_add_i32 m0, s29, 0x10000
	v_readfirstlane_b32 s0, v212
	v_readfirstlane_b32 s1, v213
	v_lshl_add_u32 v196, v0, 10, v219
	s_add_i32 s56, s29, 0x2000
	s_add_i32 s57, s29, 0x4000
	s_add_i32 s58, s29, 0x6000
	s_ashr_i32 s19, s30, 8
	global_load_lds_dwordx4 v194, s[0:1]
	s_add_i32 m0, s29, 0x12000
	v_mov_b32_e32 v65, 0
	global_load_lds_dwordx4 v196, s[0:1]
	s_mov_b64 s[0:1], 0x20000
	v_lshl_add_u64 v[0:1], v[212:213], 0, s[0:1]
	s_add_i32 m0, s29, 0x14000
	v_readfirstlane_b32 s16, v0
	v_readfirstlane_b32 s17, v1
	v_writelane_b32 v255, s84, 4
	v_mov_b32_e32 v195, v65
	v_mov_b32_e32 v197, v65
	v_writelane_b32 v254, s37, 27
	v_writelane_b32 v255, s85, 5
	global_load_lds_dwordx4 v194, s[16:17]
	s_add_i32 m0, s29, 0x16000
	s_cmp_eq_u32 s19, 1
	global_load_lds_dwordx4 v196, s[16:17]
	s_mov_b32 m0, s29
	v_lshl_add_u64 v[2:3], v[212:213], 0, v[194:195]
	global_load_lds_dwordx4 v206, s[8:9]
	s_mov_b32 m0, s56
	v_lshl_add_u64 v[0:1], v[212:213], 0, v[196:197]
	global_load_lds_dwordx4 v208, s[8:9]
	s_mov_b32 m0, s57
	v_mov_b32_e32 v207, v65
	global_load_lds_dwordx4 v64, s[8:9]
	s_mov_b32 m0, s58
	s_cselect_b64 s[16:17], -1, 0
	global_load_lds_dwordx4 v210, s[8:9]
	s_cmp_lg_u32 s19, 1
	v_mov_b32_e32 v209, v65
	s_cbranch_scc1 .LBB0_1170
	s_barrier
.LBB0_1170:
	s_mov_b64 s[34:35], 0x80
	s_add_i32 m0, s29, 0x18000
	v_lshl_add_u64 v[2:3], v[2:3], 0, s[34:35]
	s_waitcnt vmcnt(2)
	s_barrier
	global_load_lds_dwordx4 v[2:3], off
	v_lshl_add_u64 v[0:1], v[0:1], 0, s[34:35]
	s_add_i32 m0, s29, 0x1a000
	s_add_i32 s59, s29, 0x8000
	global_load_lds_dwordx4 v[0:1], off
	v_lshl_add_u64 v[0:1], s[12:13], 0, v[206:207]
	s_mov_b32 m0, s59
	s_add_i32 s61, s29, 0xa000
	global_load_lds_dwordx4 v[0:1], off
	v_lshl_add_u64 v[0:1], s[12:13], 0, v[208:209]
	s_mov_b32 m0, s61
	s_mov_b64 s[34:35], 0x20080
	global_load_lds_dwordx4 v[0:1], off
	v_lshl_add_u64 v[0:1], v[212:213], 0, s[34:35]
	s_add_i32 m0, s29, 0x1c000
	v_lshl_add_u64 v[2:3], v[0:1], 0, v[194:195]
	global_load_lds_dwordx4 v[2:3], off
	v_lshl_add_u64 v[0:1], v[0:1], 0, v[196:197]
	s_add_i32 m0, s29, 0x1e000
	v_and_b32_e32 v8, 15, v7
	global_load_lds_dwordx4 v[0:1], off
	v_lshrrev_b32_e32 v7, 1, v7
	v_and_b32_e32 v7, 24, v7
	v_lshlrev_b32_e32 v9, 1, v7
	v_lshl_or_b32 v220, s19, 6, v8
	v_lshl_or_b32 v9, v8, 6, v9
	v_lshlrev_b32_e32 v8, 2, v8
	s_lshl_b32 s19, s19, 13
	v_and_b32_e32 v10, 32, v8
	v_bitop3_b32 v11, v9, s19, v10 bitop3:0xde
	s_lshl_b32 s19, s18, 5
	s_and_b32 s31, s19, 0x60
	s_and_b32 s34, s30, 0xffffffc0
	s_lshl_b32 s19, s31, 7
	s_lshl_b32 s66, s18, 8
	s_add_i32 s36, 0, 0x20400
	s_ashr_i32 s35, s34, 31
	v_bitop3_b32 v222, v9, s19, v10 bitop3:0xde
	s_add_i32 s67, s36, s66
	s_lshl_b64 s[18:19], s[34:35], 2
	s_add_u32 s18, s20, s18
	s_addc_u32 s19, s21, s19
	v_or_b32_e32 v0, s34, v6
	v_lshlrev_b32_e32 v2, 2, v6
	v_mov_b32_e32 v3, v65
	s_cmpk_lt_u32 s30, 0x100
	s_waitcnt vmcnt(6)
	v_lshlrev_b32_e32 v0, 2, v0
	v_lshl_add_u64 v[198:199], s[18:19], 0, v[2:3]
	s_cselect_b64 s[18:19], -1, 0
	s_and_b32 s30, s30, 0xffffff00
	s_mov_b32 s27, 0
	v_ashrrev_i32_e32 v1, 31, v0
	s_add_i32 s36, s36, s30
	v_lshlrev_b32_e32 v207, 2, v4
	v_lshlrev_b32_e32 v209, 2, v5
	v_lshl_add_u64 v[200:201], s[24:25], 0, v[0:1]
	v_or_b32_e32 v224, s31, v7
	v_add_u32_e32 v225, s36, v8
	v_mov_b64_e32 v[202:203], s[26:27]
	s_add_i32 s68, 0, 0x20200
	s_add_i32 s69, 0, 0x10000
	s_add_i32 s70, 0, 0x14000
	v_add_u32_e32 v226, 0, v11
	v_mov_b32_e32 v227, 0x7f7f7f7f
	s_mov_b32 s71, 0xc3dc0000
	s_movk_i32 s78, 0xe00
	v_mov_b32_e32 v228, 0x43dc0000
	s_mov_b32 s80, s81
	s_barrier
	s_branch .LBB0_1173

.LBB0_1172:
	s_andn2_b64 vcc, exec, s[26:27]
	v_mov_b32_e32 v210, v232
	v_mov_b32_e32 v64, v231
	v_mov_b32_e32 v208, v230
	v_mov_b32_e32 v206, v229
	s_mov_b32 s28, s24
	s_mov_b32 s81, s80
	v_mov_b64_e32 v[212:213], v[204:205]
	s_mov_b32 s27, s79
	s_cbranch_vccz .LBB0_1190

.LBB0_1181:
	v_mul_hi_u32 v1, v221, s6
	v_mul_lo_u32 v0, v221, s6
	s_ashr_i32 s25, s24, 31
	v_lshl_add_u64 v[0:1], s[10:11], 0, v[0:1]
	s_lshl_b64 s[30:31], s[24:25], 18
	v_mov_b32_e32 v110, 0
	v_lshl_add_u64 v[204:205], v[0:1], 0, s[30:31]
	v_mov_b32_e32 v211, v65
	s_mov_b32 s25, 0
	s_xor_b64 s[30:31], s[36:37], -1
	s_mov_b64 s[34:35], s[12:13]
	v_mov_b32_e32 v232, v210
	v_mov_b32_e32 v231, v64
	v_mov_b32_e32 v230, v208
	v_mov_b32_e32 v229, v206
	v_mov_b32_e32 v111, v110
	v_mov_b32_e32 v112, v110
	v_mov_b32_e32 v113, v110
	v_mov_b32_e32 v118, v110
	v_mov_b32_e32 v119, v110
	v_mov_b32_e32 v120, v110
	v_mov_b32_e32 v121, v110
	v_mov_b32_e32 v130, v110
	v_mov_b32_e32 v131, v110
	v_mov_b32_e32 v132, v110
	v_mov_b32_e32 v133, v110
	v_mov_b32_e32 v138, v110
	v_mov_b32_e32 v139, v110
	v_mov_b32_e32 v140, v110
	v_mov_b32_e32 v141, v110
	v_mov_b32_e32 v146, v110
	v_mov_b32_e32 v147, v110
	v_mov_b32_e32 v148, v110
	v_mov_b32_e32 v149, v110
	v_mov_b32_e32 v154, v110
	v_mov_b32_e32 v155, v110
	v_mov_b32_e32 v156, v110
	v_mov_b32_e32 v157, v110
	v_mov_b32_e32 v162, v110
	v_mov_b32_e32 v163, v110
	v_mov_b32_e32 v164, v110
	v_mov_b32_e32 v165, v110
	v_mov_b32_e32 v170, v110
	v_mov_b32_e32 v171, v110
	v_mov_b32_e32 v172, v110
	v_mov_b32_e32 v173, v110
	v_mov_b32_e32 v178, v110
	v_mov_b32_e32 v179, v110
	v_mov_b32_e32 v180, v110
	v_mov_b32_e32 v181, v110
	v_mov_b32_e32 v186, v110
	v_mov_b32_e32 v187, v110
	v_mov_b32_e32 v188, v110
	v_mov_b32_e32 v189, v110
	v_mov_b32_e32 v134, v110
	v_mov_b32_e32 v135, v110
	v_mov_b32_e32 v136, v110
	v_mov_b32_e32 v137, v110
	v_mov_b32_e32 v142, v110
	v_mov_b32_e32 v143, v110
	v_mov_b32_e32 v144, v110
	v_mov_b32_e32 v145, v110
	v_mov_b32_e32 v150, v110
	v_mov_b32_e32 v151, v110
	v_mov_b32_e32 v152, v110
	v_mov_b32_e32 v153, v110
	v_mov_b32_e32 v158, v110
	v_mov_b32_e32 v159, v110
	v_mov_b32_e32 v160, v110
	v_mov_b32_e32 v161, v110
	v_mov_b32_e32 v166, v110
	v_mov_b32_e32 v167, v110
	v_mov_b32_e32 v168, v110
	v_mov_b32_e32 v169, v110
	v_mov_b32_e32 v174, v110
	v_mov_b32_e32 v175, v110
	v_mov_b32_e32 v176, v110
	v_mov_b32_e32 v177, v110
	v_mov_b32_e32 v182, v110
	v_mov_b32_e32 v183, v110
	v_mov_b32_e32 v184, v110
	v_mov_b32_e32 v185, v110
	v_mov_b32_e32 v190, v110
	v_mov_b32_e32 v191, v110
	v_mov_b32_e32 v192, v110
	v_mov_b32_e32 v193, v110
	v_mov_b32_e32 v106, v110
	v_mov_b32_e32 v107, v110
	v_mov_b32_e32 v108, v110
	v_mov_b32_e32 v109, v110
	v_mov_b32_e32 v98, v110
	v_mov_b32_e32 v99, v110
	v_mov_b32_e32 v100, v110
	v_mov_b32_e32 v101, v110
	v_mov_b32_e32 v90, v110
	v_mov_b32_e32 v91, v110
	v_mov_b32_e32 v92, v110
	v_mov_b32_e32 v93, v110
	v_mov_b32_e32 v82, v110
	v_mov_b32_e32 v83, v110
	v_mov_b32_e32 v84, v110
	v_mov_b32_e32 v85, v110
	v_mov_b32_e32 v74, v110
	v_mov_b32_e32 v75, v110
	v_mov_b32_e32 v76, v110
	v_mov_b32_e32 v77, v110
	v_mov_b32_e32 v66, v110
	v_mov_b32_e32 v67, v110
	v_mov_b32_e32 v68, v110
	v_mov_b32_e32 v69, v110
	v_mov_b32_e32 v126, v110
	v_mov_b32_e32 v127, v110
	v_mov_b32_e32 v128, v110
	v_mov_b32_e32 v129, v110
	v_mov_b32_e32 v122, v110
	v_mov_b32_e32 v123, v110
	v_mov_b32_e32 v124, v110
	v_mov_b32_e32 v125, v110
	v_mov_b32_e32 v114, v110
	v_mov_b32_e32 v115, v110
	v_mov_b32_e32 v116, v110
	v_mov_b32_e32 v117, v110
	v_mov_b32_e32 v102, v110
	v_mov_b32_e32 v103, v110
	v_mov_b32_e32 v104, v110
	v_mov_b32_e32 v105, v110
	v_mov_b32_e32 v94, v110
	v_mov_b32_e32 v95, v110
	v_mov_b32_e32 v96, v110
	v_mov_b32_e32 v97, v110
	v_mov_b32_e32 v86, v110
	v_mov_b32_e32 v87, v110
	v_mov_b32_e32 v88, v110
	v_mov_b32_e32 v89, v110
	v_mov_b32_e32 v78, v110
	v_mov_b32_e32 v79, v110
	v_mov_b32_e32 v80, v110
	v_mov_b32_e32 v81, v110
	v_mov_b32_e32 v70, v110
	v_mov_b32_e32 v71, v110
	v_mov_b32_e32 v72, v110
	v_mov_b32_e32 v73, v110
	s_branch .LBB0_1183
.LBB0_1182:
	v_add_u32_e32 v0, s69, v222
	v_add_u32_e32 v4, s70, v222
	ds_read_b128 v[24:27], v0
	ds_read_b128 v[28:31], v0 offset:1024
	ds_read_b128 v[16:19], v0 offset:2048
	ds_read_b128 v[20:23], v0 offset:3072
	ds_read_b128 v[8:11], v4
	ds_read_b128 v[12:15], v4 offset:1024
	ds_read_b128 v[0:3], v4 offset:2048
	ds_read_b128 v[4:7], v4 offset:3072
	v_lshl_add_u64 v[214:215], s[34:35], 0, v[64:65]
	s_add_i32 m0, s29, 0xc000
	ds_read_b128 v[32:35], v226
	ds_read_b128 v[36:39], v226 offset:1024
	ds_read_b128 v[40:43], v226 offset:2048
	ds_read_b128 v[44:47], v226 offset:3072
	ds_read_b128 v[48:51], v226 offset:4096
	ds_read_b128 v[52:55], v226 offset:5120
	ds_read_b128 v[56:59], v226 offset:6144
	ds_read_b128 v[60:63], v226 offset:7168
	global_load_lds_dwordx4 v[214:215], off
	v_lshl_add_u64 v[214:215], s[34:35], 0, v[210:211]
	s_add_i32 m0, s29, 0xe000
	s_nop 0
	global_load_lds_dwordx4 v[214:215], off
	s_waitcnt vmcnt(8)
	s_waitcnt lgkmcnt(0)
	s_barrier
	s_setprio 1
	s_waitcnt lgkmcnt(0)
	v_mfma_scale_f32_16x16x128_f8f6f4 v[190:193], v[24:31], v[32:39], v[190:193], v227, v227 op_sel_hi:[0,0,0]
	v_mfma_scale_f32_16x16x128_f8f6f4 v[182:185], v[16:23], v[32:39], v[182:185], v227, v227 op_sel_hi:[0,0,0]
	v_mfma_scale_f32_16x16x128_f8f6f4 v[174:177], v[24:31], v[40:47], v[174:177], v227, v227 op_sel_hi:[0,0,0]
	v_mfma_scale_f32_16x16x128_f8f6f4 v[166:169], v[16:23], v[40:47], v[166:169], v227, v227 op_sel_hi:[0,0,0]
	v_mfma_scale_f32_16x16x128_f8f6f4 v[158:161], v[24:31], v[48:55], v[158:161], v227, v227 op_sel_hi:[0,0,0]
	v_mfma_scale_f32_16x16x128_f8f6f4 v[150:153], v[16:23], v[48:55], v[150:153], v227, v227 op_sel_hi:[0,0,0]
	v_mfma_scale_f32_16x16x128_f8f6f4 v[142:145], v[24:31], v[56:63], v[142:145], v227, v227 op_sel_hi:[0,0,0]
	v_mfma_scale_f32_16x16x128_f8f6f4 v[134:137], v[16:23], v[56:63], v[134:137], v227, v227 op_sel_hi:[0,0,0]
	s_setprio 0
	s_setprio 1
	v_mfma_scale_f32_16x16x128_f8f6f4 v[186:189], v[8:15], v[32:39], v[186:189], v227, v227 op_sel_hi:[0,0,0]
	v_mfma_scale_f32_16x16x128_f8f6f4 v[178:181], v[0:7], v[32:39], v[178:181], v227, v227 op_sel_hi:[0,0,0]
	v_mfma_scale_f32_16x16x128_f8f6f4 v[170:173], v[8:15], v[40:47], v[170:173], v227, v227 op_sel_hi:[0,0,0]
	v_mfma_scale_f32_16x16x128_f8f6f4 v[162:165], v[0:7], v[40:47], v[162:165], v227, v227 op_sel_hi:[0,0,0]
	v_mfma_scale_f32_16x16x128_f8f6f4 v[154:157], v[8:15], v[48:55], v[154:157], v227, v227 op_sel_hi:[0,0,0]
	v_mfma_scale_f32_16x16x128_f8f6f4 v[146:149], v[0:7], v[48:55], v[146:149], v227, v227 op_sel_hi:[0,0,0]
	v_mfma_scale_f32_16x16x128_f8f6f4 v[138:141], v[8:15], v[56:63], v[138:141], v227, v227 op_sel_hi:[0,0,0]
	v_mfma_scale_f32_16x16x128_f8f6f4 v[130:133], v[0:7], v[56:63], v[130:133], v227, v227 op_sel_hi:[0,0,0]
	s_setprio 0
	s_barrier
	s_cmp_gt_u32 s25, 5
	v_sub_co_u32_e64 v216, s[40:41], s25, 6
	s_cselect_b64 vcc, -1, 0
	v_add_u32_e32 v217, 8, v216
	v_cndmask_b32_e32 v216, v217, v216, vcc
	v_ashrrev_i32_e32 v217, 31, v216
	v_cndmask_b32_e32 v215, v213, v205, vcc
	v_cndmask_b32_e32 v214, v212, v204, vcc
	v_lshlrev_b64 v[216:217], 7, v[216:217]
	v_lshl_add_u64 v[214:215], v[214:215], 0, v[216:217]
	s_add_i32 s26, s69, s7
	s_add_i32 s38, s26, 0x2000
	v_lshl_add_u64 v[236:237], v[214:215], 0, v[194:195]
	s_mov_b32 m0, s26
	ds_read_b128 v[56:59], v226 offset:16384
	ds_read_b128 v[60:63], v226 offset:17408
	ds_read_b128 v[48:51], v226 offset:18432
	ds_read_b128 v[52:55], v226 offset:19456
	ds_read_b128 v[40:43], v226 offset:20480
	ds_read_b128 v[44:47], v226 offset:21504
	ds_read_b128 v[32:35], v226 offset:22528
	ds_read_b128 v[36:39], v226 offset:23552
	v_lshl_add_u64 v[234:235], v[214:215], 0, s[0:1]
	s_add_i32 s39, s70, s7
	global_load_lds_dwordx4 v[236:237], off
	v_lshl_add_u64 v[214:215], v[214:215], 0, v[196:197]
	s_mov_b32 m0, s38
	s_add_i32 s42, s39, 0x2000
	global_load_lds_dwordx4 v[214:215], off
	v_lshl_add_u64 v[214:215], v[234:235], 0, v[194:195]
	s_mov_b32 m0, s39
	v_lshl_add_u64 v[216:217], s[8:9], 0, v[216:217]
	global_load_lds_dwordx4 v[214:215], off
	v_lshl_add_u64 v[214:215], v[234:235], 0, v[196:197]
	s_mov_b32 m0, s42
	v_readfirstlane_b32 s44, v216
	global_load_lds_dwordx4 v[214:215], off
	v_cndmask_b32_e32 v214, v206, v229, vcc
	v_readfirstlane_b32 s45, v217
	s_mov_b32 m0, s29
	v_cndmask_b32_e32 v215, v208, v230, vcc
	s_add_i32 s85, 0, 0x18000
	s_add_i32 s82, 0, 0x1c000
	s_cmp_gt_u32 s25, 4
	global_load_lds_dwordx4 v214, s[44:45]
	s_mov_b32 m0, s56
	s_cselect_b64 s[38:39], -1, 0
	global_load_lds_dwordx4 v215, s[44:45]
	s_and_b64 s[42:43], s[38:39], exec
	s_cselect_b32 s26, -5, 3
	s_add_i32 s42, s26, s25
	s_ashr_i32 s43, s42, 31
	s_add_i32 s84, s85, s7
	s_add_i32 s26, s82, s7
	v_cndmask_b32_e64 v215, v213, v205, s[38:39]
	v_cndmask_b32_e64 v214, v212, v204, s[38:39]
	s_lshl_b64 s[42:43], s[42:43], 7
	s_add_i32 s83, s84, 0x2000
	s_add_i32 s60, s26, 0x2000
	v_lshl_add_u64 v[216:217], v[214:215], 0, s[42:43]
	s_add_u32 s42, s8, s42
	s_waitcnt vmcnt(8)
	s_addc_u32 s43, s9, s43
	s_waitcnt lgkmcnt(0)
	s_add_u32 s34, s34, 0x100
	s_addc_u32 s35, s35, 0
	s_add_i32 s25, s25, 2
	v_lshl_add_u64 v[214:215], v[216:217], 0, s[0:1]
	s_barrier
	s_setprio 1
	s_waitcnt lgkmcnt(0)
	v_mfma_scale_f32_16x16x128_f8f6f4 v[118:121], v[24:31], v[56:63], v[118:121], v227, v227 op_sel_hi:[0,0,0]
	v_mfma_scale_f32_16x16x128_f8f6f4 v[110:113], v[16:23], v[56:63], v[110:113], v227, v227 op_sel_hi:[0,0,0]
	v_mfma_scale_f32_16x16x128_f8f6f4 v[106:109], v[24:31], v[48:55], v[106:109], v227, v227 op_sel_hi:[0,0,0]
	v_mfma_scale_f32_16x16x128_f8f6f4 v[98:101], v[16:23], v[48:55], v[98:101], v227, v227 op_sel_hi:[0,0,0]
	v_mfma_scale_f32_16x16x128_f8f6f4 v[90:93], v[24:31], v[40:47], v[90:93], v227, v227 op_sel_hi:[0,0,0]
	v_mfma_scale_f32_16x16x128_f8f6f4 v[82:85], v[16:23], v[40:47], v[82:85], v227, v227 op_sel_hi:[0,0,0]
	v_mfma_scale_f32_16x16x128_f8f6f4 v[74:77], v[24:31], v[32:39], v[74:77], v227, v227 op_sel_hi:[0,0,0]
	v_mfma_scale_f32_16x16x128_f8f6f4 v[66:69], v[16:23], v[32:39], v[66:69], v227, v227 op_sel_hi:[0,0,0]
	s_setprio 0
	s_setprio 1
	v_mfma_scale_f32_16x16x128_f8f6f4 v[126:129], v[8:15], v[56:63], v[126:129], v227, v227 op_sel_hi:[0,0,0]
	v_mfma_scale_f32_16x16x128_f8f6f4 v[122:125], v[0:7], v[56:63], v[122:125], v227, v227 op_sel_hi:[0,0,0]
	v_mfma_scale_f32_16x16x128_f8f6f4 v[114:117], v[8:15], v[48:55], v[114:117], v227, v227 op_sel_hi:[0,0,0]
	v_mfma_scale_f32_16x16x128_f8f6f4 v[102:105], v[0:7], v[48:55], v[102:105], v227, v227 op_sel_hi:[0,0,0]
	v_mfma_scale_f32_16x16x128_f8f6f4 v[94:97], v[8:15], v[40:47], v[94:97], v227, v227 op_sel_hi:[0,0,0]
	v_mfma_scale_f32_16x16x128_f8f6f4 v[86:89], v[0:7], v[40:47], v[86:89], v227, v227 op_sel_hi:[0,0,0]
	v_mfma_scale_f32_16x16x128_f8f6f4 v[78:81], v[8:15], v[32:39], v[78:81], v227, v227 op_sel_hi:[0,0,0]
	v_mfma_scale_f32_16x16x128_f8f6f4 v[70:73], v[0:7], v[32:39], v[70:73], v227, v227 op_sel_hi:[0,0,0]
	s_setprio 0
	s_barrier
	v_add_u32_e32 v12, s85, v222
	v_add_u32_e32 v28, s82, v222
	ds_read_b128 v[0:3], v12
	ds_read_b128 v[4:7], v12 offset:1024
	ds_read_b128 v[8:11], v12 offset:2048
	ds_read_b128 v[12:15], v12 offset:3072
	ds_read_b128 v[16:19], v28
	ds_read_b128 v[20:23], v28 offset:1024
	ds_read_b128 v[24:27], v28 offset:2048
	ds_read_b128 v[28:31], v28 offset:3072
	s_mov_b32 m0, s57
	v_cndmask_b32_e32 v223, v64, v231, vcc
	ds_read_b128 v[32:35], v226 offset:32768
	ds_read_b128 v[36:39], v226 offset:33792
	ds_read_b128 v[40:43], v226 offset:34816
	ds_read_b128 v[44:47], v226 offset:35840
	ds_read_b128 v[48:51], v226 offset:36864
	ds_read_b128 v[52:55], v226 offset:37888
	ds_read_b128 v[56:59], v226 offset:38912
	ds_read_b128 v[60:63], v226 offset:39936
	v_cndmask_b32_e32 v233, v210, v232, vcc
	global_load_lds_dwordx4 v223, s[44:45]
	s_mov_b32 m0, s58
	s_nop 0
	global_load_lds_dwordx4 v233, s[44:45]
	s_waitcnt vmcnt(8)
	s_waitcnt lgkmcnt(0)
	s_barrier
	s_setprio 1
	s_waitcnt lgkmcnt(0)
	v_mfma_scale_f32_16x16x128_f8f6f4 v[190:193], v[0:7], v[32:39], v[190:193], v227, v227 op_sel_hi:[0,0,0]
	v_mfma_scale_f32_16x16x128_f8f6f4 v[182:185], v[8:15], v[32:39], v[182:185], v227, v227 op_sel_hi:[0,0,0]
	v_mfma_scale_f32_16x16x128_f8f6f4 v[174:177], v[0:7], v[40:47], v[174:177], v227, v227 op_sel_hi:[0,0,0]
	v_mfma_scale_f32_16x16x128_f8f6f4 v[166:169], v[8:15], v[40:47], v[166:169], v227, v227 op_sel_hi:[0,0,0]
	v_mfma_scale_f32_16x16x128_f8f6f4 v[158:161], v[0:7], v[48:55], v[158:161], v227, v227 op_sel_hi:[0,0,0]
	v_mfma_scale_f32_16x16x128_f8f6f4 v[150:153], v[8:15], v[48:55], v[150:153], v227, v227 op_sel_hi:[0,0,0]
	v_mfma_scale_f32_16x16x128_f8f6f4 v[142:145], v[0:7], v[56:63], v[142:145], v227, v227 op_sel_hi:[0,0,0]
	v_mfma_scale_f32_16x16x128_f8f6f4 v[134:137], v[8:15], v[56:63], v[134:137], v227, v227 op_sel_hi:[0,0,0]
	s_setprio 0
	s_setprio 1
	v_mfma_scale_f32_16x16x128_f8f6f4 v[186:189], v[16:23], v[32:39], v[186:189], v227, v227 op_sel_hi:[0,0,0]
	v_mfma_scale_f32_16x16x128_f8f6f4 v[178:181], v[24:31], v[32:39], v[178:181], v227, v227 op_sel_hi:[0,0,0]
	v_mfma_scale_f32_16x16x128_f8f6f4 v[170:173], v[16:23], v[40:47], v[170:173], v227, v227 op_sel_hi:[0,0,0]
	v_mfma_scale_f32_16x16x128_f8f6f4 v[162:165], v[24:31], v[40:47], v[162:165], v227, v227 op_sel_hi:[0,0,0]
	v_mfma_scale_f32_16x16x128_f8f6f4 v[154:157], v[16:23], v[48:55], v[154:157], v227, v227 op_sel_hi:[0,0,0]
	v_mfma_scale_f32_16x16x128_f8f6f4 v[146:149], v[24:31], v[48:55], v[146:149], v227, v227 op_sel_hi:[0,0,0]
	v_mfma_scale_f32_16x16x128_f8f6f4 v[138:141], v[16:23], v[56:63], v[138:141], v227, v227 op_sel_hi:[0,0,0]
	v_mfma_scale_f32_16x16x128_f8f6f4 v[130:133], v[24:31], v[56:63], v[130:133], v227, v227 op_sel_hi:[0,0,0]
	s_setprio 0
	s_barrier
	s_mov_b32 m0, s84
	v_lshl_add_u64 v[234:235], v[216:217], 0, v[194:195]
	ds_read_b128 v[32:35], v226 offset:49152
	ds_read_b128 v[36:39], v226 offset:50176
	ds_read_b128 v[40:43], v226 offset:51200
	ds_read_b128 v[44:47], v226 offset:52224
	ds_read_b128 v[48:51], v226 offset:53248
	ds_read_b128 v[52:55], v226 offset:54272
	ds_read_b128 v[56:59], v226 offset:55296
	ds_read_b128 v[60:63], v226 offset:56320
	global_load_lds_dwordx4 v[234:235], off
	v_lshl_add_u64 v[216:217], v[216:217], 0, v[196:197]
	s_mov_b32 m0, s83
	s_nop 0
	global_load_lds_dwordx4 v[216:217], off
	v_lshl_add_u64 v[216:217], v[214:215], 0, v[194:195]
	s_mov_b32 m0, s26
	v_lshl_add_u64 v[214:215], v[214:215], 0, v[196:197]
	global_load_lds_dwordx4 v[216:217], off
	s_mov_b32 m0, s60
	s_nop 0
	global_load_lds_dwordx4 v[214:215], off
	v_cndmask_b32_e64 v214, v206, v229, s[38:39]
	s_mov_b32 m0, s59
	v_cndmask_b32_e64 v215, v208, v230, s[38:39]
	global_load_lds_dwordx4 v214, s[42:43]
	s_mov_b32 m0, s61
	s_nop 0
	global_load_lds_dwordx4 v215, s[42:43]
	s_waitcnt vmcnt(8)
	s_waitcnt lgkmcnt(0)
	s_barrier
	s_setprio 1
	s_waitcnt lgkmcnt(0)
	v_mfma_scale_f32_16x16x128_f8f6f4 v[118:121], v[0:7], v[32:39], v[118:121], v227, v227 op_sel_hi:[0,0,0]
	v_mfma_scale_f32_16x16x128_f8f6f4 v[110:113], v[8:15], v[32:39], v[110:113], v227, v227 op_sel_hi:[0,0,0]
	v_mfma_scale_f32_16x16x128_f8f6f4 v[106:109], v[0:7], v[40:47], v[106:109], v227, v227 op_sel_hi:[0,0,0]
	v_mfma_scale_f32_16x16x128_f8f6f4 v[98:101], v[8:15], v[40:47], v[98:101], v227, v227 op_sel_hi:[0,0,0]
	v_mfma_scale_f32_16x16x128_f8f6f4 v[90:93], v[0:7], v[48:55], v[90:93], v227, v227 op_sel_hi:[0,0,0]
	v_mfma_scale_f32_16x16x128_f8f6f4 v[82:85], v[8:15], v[48:55], v[82:85], v227, v227 op_sel_hi:[0,0,0]
	v_mfma_scale_f32_16x16x128_f8f6f4 v[74:77], v[0:7], v[56:63], v[74:77], v227, v227 op_sel_hi:[0,0,0]
	v_mfma_scale_f32_16x16x128_f8f6f4 v[66:69], v[8:15], v[56:63], v[66:69], v227, v227 op_sel_hi:[0,0,0]
	s_setprio 0
	s_setprio 1
	v_mfma_scale_f32_16x16x128_f8f6f4 v[126:129], v[16:23], v[32:39], v[126:129], v227, v227 op_sel_hi:[0,0,0]
	v_mfma_scale_f32_16x16x128_f8f6f4 v[122:125], v[24:31], v[32:39], v[122:125], v227, v227 op_sel_hi:[0,0,0]
	v_mfma_scale_f32_16x16x128_f8f6f4 v[114:117], v[16:23], v[40:47], v[114:117], v227, v227 op_sel_hi:[0,0,0]
	v_mfma_scale_f32_16x16x128_f8f6f4 v[102:105], v[24:31], v[40:47], v[102:105], v227, v227 op_sel_hi:[0,0,0]
	v_mfma_scale_f32_16x16x128_f8f6f4 v[94:97], v[16:23], v[48:55], v[94:97], v227, v227 op_sel_hi:[0,0,0]
	v_mfma_scale_f32_16x16x128_f8f6f4 v[86:89], v[24:31], v[48:55], v[86:89], v227, v227 op_sel_hi:[0,0,0]
	v_mfma_scale_f32_16x16x128_f8f6f4 v[78:81], v[16:23], v[56:63], v[78:81], v227, v227 op_sel_hi:[0,0,0]
	v_mfma_scale_f32_16x16x128_f8f6f4 v[70:73], v[24:31], v[56:63], v[70:73], v227, v227 op_sel_hi:[0,0,0]
	s_setprio 0
	s_barrier
	s_andn2_b64 vcc, exec, s[40:41]
	s_cbranch_vccnz .LBB0_1185

.LBB0_1187:
	s_mul_hi_u32 s25, s27, 0xaaaaaaab
	s_lshr_b32 s25, s25, 1
	s_mul_i32 s25, s25, 3
	s_sub_i32 s25, s27, s25
	s_nop 15
	s_nop 7
	v_lshl_add_u32 v0, s25, 11, v225
	ds_read2_b32 v[12:13], v0 offset1:16
	ds_read2_b32 v[8:9], v0 offset0:32 offset1:48
	ds_read2_b32 v[6:7], v0 offset0:128 offset1:144
	ds_read2_b32 v[2:3], v0 offset0:160 offset1:176
	v_pk_mul_f32 v[14:15], v[192:193], v[188:189]
	s_waitcnt lgkmcnt(0)
	v_mul_f32_e32 v4, v12, v12
	v_mul_f32_e32 v12, 0xbfb8aa3b, v12
	v_pk_mul_f32 v[18:19], v[192:193], v[12:13] op_sel_hi:[1,0]
	v_pk_mul_f32 v[20:21], v[190:191], v[12:13] op_sel_hi:[1,0]
	v_exp_f32_e32 v18, v18
	v_exp_f32_e32 v20, v20
	v_exp_f32_e32 v21, v21
	v_exp_f32_e32 v19, v19
	v_mul_f32_e32 v4, 0x41000000, v4
	v_pk_mul_f32 v[16:17], v[190:191], v[186:187]
	v_pk_add_f32 v[20:21], v[20:21], 1.0 op_sel_hi:[1,0]
	v_pk_add_f32 v[18:19], v[18:19], 1.0 op_sel_hi:[1,0]
	v_rcp_f32_e32 v20, v20
	v_rcp_f32_e32 v21, v21
	v_rcp_f32_e32 v18, v18
	v_rcp_f32_e32 v19, v19
	v_pk_mul_f32 v[16:17], v[16:17], v[4:5] op_sel_hi:[1,0]
	v_pk_mul_f32 v[14:15], v[14:15], v[4:5] op_sel_hi:[1,0]
	v_pk_mul_f32 v[16:17], v[16:17], v[20:21]
	v_pk_mul_f32 v[14:15], v[14:15], v[18:19]
	v_pk_mul_f32 v[18:19], v[184:185], v[180:181]
	v_pk_mul_f32 v[20:21], v[182:183], v[178:179]
	v_pk_mul_f32 v[22:23], v[182:183], v[12:13] op_sel_hi:[1,0]
	v_pk_mul_f32 v[20:21], v[20:21], v[4:5] op_sel_hi:[1,0]
	v_pk_mul_f32 v[4:5], v[18:19], v[4:5] op_sel_hi:[1,0]
	v_pk_mul_f32 v[18:19], v[184:185], v[12:13] op_sel_hi:[1,0]
	v_exp_f32_e32 v22, v22
	v_exp_f32_e32 v23, v23
	v_exp_f32_e32 v18, v18
	v_exp_f32_e32 v19, v19
	v_med3_f32 v11, v16, s71, v228
	v_pk_add_f32 v[22:23], v[22:23], 1.0 op_sel_hi:[1,0]
	v_med3_f32 v12, v17, s71, v228
	v_pk_add_f32 v[18:19], v[18:19], 1.0 op_sel_hi:[1,0]
	v_rcp_f32_e32 v22, v22
	v_rcp_f32_e32 v23, v23
	v_rcp_f32_e32 v18, v18
	v_rcp_f32_e32 v19, v19
	v_med3_f32 v16, v14, s71, v228
	v_mov_b32_e32 v14, v65
	v_cvt_pk_fp8_f32 v14, v11, v12
	v_pk_mul_f32 v[4:5], v[4:5], v[18:19]
	v_pk_mul_f32 v[18:19], v[20:21], v[22:23]
	v_med3_f32 v15, v15, s71, v228
	v_cvt_pk_fp8_f32 v14, v16, v15 op_sel:[0,0,1]
	v_med3_f32 v11, v18, s71, v228
	v_med3_f32 v12, v19, s71, v228
	v_mov_b32_e32 v15, v65
	v_cvt_pk_fp8_f32 v15, v11, v12
	v_med3_f32 v4, v4, s71, v228
	v_med3_f32 v5, v5, s71, v228
	v_lshl_or_b32 v0, s28, 7, v224
	v_cvt_pk_fp8_f32 v15, v4, v5 op_sel:[0,0,1]
	v_lshl_add_u32 v10, s81, 8, v220
	v_mov_b64_e32 v[4:5], s[22:23]
	v_ashrrev_i32_e32 v1, 31, v0
	v_mad_i64_i32 v[16:17], s[26:27], v10, s78, v[4:5]
	v_lshl_add_u64 v[16:17], v[16:17], 0, v[0:1]
	global_store_dwordx2 v[16:17], v[14:15], off
	v_mul_f32_e32 v14, 0xbfb8aa3b, v13
	v_pk_mul_f32 v[20:21], v[176:177], v[14:15] op_sel_hi:[1,0]
	v_pk_mul_f32 v[22:23], v[174:175], v[14:15] op_sel_hi:[1,0]
	v_exp_f32_e32 v20, v20
	v_exp_f32_e32 v22, v22
	v_exp_f32_e32 v23, v23
	v_exp_f32_e32 v21, v21
	v_mul_f32_e32 v11, v13, v13
	v_mul_f32_e32 v12, 0x41000000, v11
	v_pk_add_f32 v[22:23], v[22:23], 1.0 op_sel_hi:[1,0]
	v_pk_add_f32 v[20:21], v[20:21], 1.0 op_sel_hi:[1,0]
	v_rcp_f32_e32 v22, v22
	v_rcp_f32_e32 v23, v23
	v_rcp_f32_e32 v20, v20
	v_rcp_f32_e32 v21, v21
	v_pk_mul_f32 v[16:17], v[176:177], v[172:173]
	v_pk_mul_f32 v[18:19], v[174:175], v[170:171]
	v_pk_mul_f32 v[16:17], v[16:17], v[12:13] op_sel_hi:[1,0]
	v_pk_mul_f32 v[18:19], v[18:19], v[12:13] op_sel_hi:[1,0]
	v_pk_mul_f32 v[16:17], v[16:17], v[20:21]
	v_pk_mul_f32 v[18:19], v[18:19], v[22:23]
	v_pk_mul_f32 v[20:21], v[168:169], v[164:165]
	v_pk_mul_f32 v[22:23], v[166:167], v[162:163]
	v_med3_f32 v18, v18, s71, v228
	v_pk_mul_f32 v[22:23], v[22:23], v[12:13] op_sel_hi:[1,0]
	v_pk_mul_f32 v[12:13], v[20:21], v[12:13] op_sel_hi:[1,0]
	v_pk_mul_f32 v[20:21], v[168:169], v[14:15] op_sel_hi:[1,0]
	v_pk_mul_f32 v[14:15], v[166:167], v[14:15] op_sel_hi:[1,0]
	v_exp_f32_e32 v20, v20
	v_exp_f32_e32 v21, v21
	v_exp_f32_e32 v14, v14
	v_exp_f32_e32 v15, v15
	v_med3_f32 v19, v19, s71, v228
	v_pk_add_f32 v[20:21], v[20:21], 1.0 op_sel_hi:[1,0]
	v_med3_f32 v17, v17, s71, v228
	v_rcp_f32_e32 v20, v20
	v_rcp_f32_e32 v21, v21
	v_pk_add_f32 v[14:15], v[14:15], 1.0 op_sel_hi:[1,0]
	v_or_b32_e32 v11, 16, v10
	v_rcp_f32_e32 v14, v14
	v_rcp_f32_e32 v15, v15
	v_pk_mul_f32 v[12:13], v[12:13], v[20:21]
	v_med3_f32 v20, v16, s71, v228
	v_mov_b32_e32 v16, v65
	v_cvt_pk_fp8_f32 v16, v18, v19
	v_pk_mul_f32 v[14:15], v[22:23], v[14:15]
	v_med3_f32 v12, v12, s71, v228
	v_med3_f32 v14, v14, s71, v228
	v_cvt_pk_fp8_f32 v16, v20, v17 op_sel:[0,0,1]
	v_med3_f32 v15, v15, s71, v228
	v_mov_b32_e32 v17, v65
	v_cvt_pk_fp8_f32 v17, v14, v15
	v_med3_f32 v13, v13, s71, v228
	v_pk_mul_f32 v[14:15], v[160:161], v[156:157]
	s_andn2_b64 vcc, exec, s[36:37]
	v_cvt_pk_fp8_f32 v17, v12, v13 op_sel:[0,0,1]
	v_mad_i64_i32 v[12:13], s[26:27], v11, s78, v[4:5]
	v_mul_f32_e32 v11, v8, v8
	v_mul_f32_e32 v8, 0xbfb8aa3b, v8
	v_pk_mul_f32 v[18:19], v[160:161], v[8:9] op_sel_hi:[1,0]
	v_pk_mul_f32 v[20:21], v[158:159], v[8:9] op_sel_hi:[1,0]
	v_exp_f32_e32 v18, v18
	v_exp_f32_e32 v20, v20
	v_exp_f32_e32 v21, v21
	v_exp_f32_e32 v19, v19
	v_lshl_add_u64 v[12:13], v[12:13], 0, v[0:1]
	global_store_dwordx2 v[12:13], v[16:17], off
	v_pk_add_f32 v[20:21], v[20:21], 1.0 op_sel_hi:[1,0]
	v_pk_add_f32 v[18:19], v[18:19], 1.0 op_sel_hi:[1,0]
	v_rcp_f32_e32 v20, v20
	v_rcp_f32_e32 v21, v21
	v_rcp_f32_e32 v18, v18
	v_rcp_f32_e32 v19, v19
	v_mul_f32_e32 v12, 0x41000000, v11
	v_pk_mul_f32 v[16:17], v[158:159], v[154:155]
	v_pk_mul_f32 v[14:15], v[14:15], v[12:13] op_sel_hi:[1,0]
	v_pk_mul_f32 v[16:17], v[16:17], v[12:13] op_sel_hi:[1,0]
	v_pk_mul_f32 v[14:15], v[14:15], v[18:19]
	v_pk_mul_f32 v[16:17], v[16:17], v[20:21]
	v_pk_mul_f32 v[18:19], v[152:153], v[148:149]
	v_pk_mul_f32 v[20:21], v[150:151], v[146:147]
	v_pk_mul_f32 v[22:23], v[150:151], v[8:9] op_sel_hi:[1,0]
	v_pk_mul_f32 v[20:21], v[20:21], v[12:13] op_sel_hi:[1,0]
	v_pk_mul_f32 v[12:13], v[18:19], v[12:13] op_sel_hi:[1,0]
	v_pk_mul_f32 v[18:19], v[152:153], v[8:9] op_sel_hi:[1,0]
	v_exp_f32_e32 v22, v22
	v_exp_f32_e32 v23, v23
	v_exp_f32_e32 v18, v18
	v_exp_f32_e32 v19, v19
	v_med3_f32 v11, v16, s71, v228
	v_pk_add_f32 v[22:23], v[22:23], 1.0 op_sel_hi:[1,0]
	v_med3_f32 v16, v17, s71, v228
	v_pk_add_f32 v[18:19], v[18:19], 1.0 op_sel_hi:[1,0]
	v_rcp_f32_e32 v22, v22
	v_rcp_f32_e32 v23, v23
	v_rcp_f32_e32 v18, v18
	v_rcp_f32_e32 v19, v19
	v_med3_f32 v17, v14, s71, v228
	v_mov_b32_e32 v14, v65
	v_cvt_pk_fp8_f32 v14, v11, v16
	v_pk_mul_f32 v[12:13], v[12:13], v[18:19]
	v_pk_mul_f32 v[18:19], v[20:21], v[22:23]
	v_med3_f32 v15, v15, s71, v228
	v_cvt_pk_fp8_f32 v14, v17, v15 op_sel:[0,0,1]
	v_med3_f32 v11, v18, s71, v228
	v_med3_f32 v16, v19, s71, v228
	v_mov_b32_e32 v15, v65
	v_cvt_pk_fp8_f32 v15, v11, v16
	v_med3_f32 v12, v12, s71, v228
	v_med3_f32 v13, v13, s71, v228
	v_or_b32_e32 v8, 32, v10
	v_cvt_pk_fp8_f32 v15, v12, v13 op_sel:[0,0,1]
	v_mad_i64_i32 v[12:13], s[26:27], v8, s78, v[4:5]
	v_lshl_add_u64 v[12:13], v[12:13], 0, v[0:1]
	global_store_dwordx2 v[12:13], v[14:15], off
	v_mul_f32_e32 v12, 0xbfb8aa3b, v9
	v_pk_mul_f32 v[18:19], v[144:145], v[12:13] op_sel_hi:[1,0]
	v_pk_mul_f32 v[20:21], v[142:143], v[12:13] op_sel_hi:[1,0]
	v_exp_f32_e32 v18, v18
	v_exp_f32_e32 v20, v20
	v_exp_f32_e32 v21, v21
	v_exp_f32_e32 v19, v19
	v_mul_f32_e32 v8, v9, v9
	v_mul_f32_e32 v8, 0x41000000, v8
	v_pk_add_f32 v[20:21], v[20:21], 1.0 op_sel_hi:[1,0]
	v_pk_add_f32 v[18:19], v[18:19], 1.0 op_sel_hi:[1,0]
	v_rcp_f32_e32 v20, v20
	v_rcp_f32_e32 v21, v21
	v_rcp_f32_e32 v18, v18
	v_rcp_f32_e32 v19, v19
	v_pk_mul_f32 v[14:15], v[144:145], v[140:141]
	v_pk_mul_f32 v[16:17], v[142:143], v[138:139]
	v_pk_mul_f32 v[14:15], v[14:15], v[8:9] op_sel_hi:[1,0]
	v_pk_mul_f32 v[16:17], v[16:17], v[8:9] op_sel_hi:[1,0]
	v_pk_mul_f32 v[14:15], v[14:15], v[18:19]
	v_pk_mul_f32 v[16:17], v[16:17], v[20:21]
	v_pk_mul_f32 v[18:19], v[136:137], v[132:133]
	v_pk_mul_f32 v[20:21], v[134:135], v[130:131]
	v_med3_f32 v16, v16, s71, v228
	v_pk_mul_f32 v[20:21], v[20:21], v[8:9] op_sel_hi:[1,0]
	v_pk_mul_f32 v[8:9], v[18:19], v[8:9] op_sel_hi:[1,0]
	v_pk_mul_f32 v[18:19], v[136:137], v[12:13] op_sel_hi:[1,0]
	v_pk_mul_f32 v[12:13], v[134:135], v[12:13] op_sel_hi:[1,0]
	v_exp_f32_e32 v18, v18
	v_exp_f32_e32 v19, v19
	v_exp_f32_e32 v12, v12
	v_exp_f32_e32 v13, v13
	v_med3_f32 v17, v17, s71, v228
	v_pk_add_f32 v[18:19], v[18:19], 1.0 op_sel_hi:[1,0]
	v_med3_f32 v15, v15, s71, v228
	v_rcp_f32_e32 v18, v18
	v_rcp_f32_e32 v19, v19
	v_pk_add_f32 v[12:13], v[12:13], 1.0 op_sel_hi:[1,0]
	v_or_b32_e32 v11, 48, v10
	v_rcp_f32_e32 v12, v12
	v_rcp_f32_e32 v13, v13
	v_pk_mul_f32 v[8:9], v[8:9], v[18:19]
	v_med3_f32 v18, v14, s71, v228
	v_mov_b32_e32 v14, v65
	v_cvt_pk_fp8_f32 v14, v16, v17
	v_pk_mul_f32 v[12:13], v[20:21], v[12:13]
	v_med3_f32 v8, v8, s71, v228
	v_med3_f32 v12, v12, s71, v228
	v_cvt_pk_fp8_f32 v14, v18, v15 op_sel:[0,0,1]
	v_med3_f32 v13, v13, s71, v228
	v_mov_b32_e32 v15, v65
	v_cvt_pk_fp8_f32 v15, v12, v13
	v_med3_f32 v9, v9, s71, v228
	v_pk_mul_f32 v[12:13], v[120:121], v[128:129]
	v_cvt_pk_fp8_f32 v15, v8, v9 op_sel:[0,0,1]
	v_mad_i64_i32 v[8:9], s[26:27], v11, s78, v[4:5]
	v_lshl_add_u64 v[8:9], v[8:9], 0, v[0:1]
	global_store_dwordx2 v[8:9], v[14:15], off
	v_mul_f32_e32 v8, v6, v6
	v_mul_f32_e32 v6, 0xbfb8aa3b, v6
	v_pk_mul_f32 v[16:17], v[120:121], v[6:7] op_sel_hi:[1,0]
	v_pk_mul_f32 v[18:19], v[118:119], v[6:7] op_sel_hi:[1,0]
	v_exp_f32_e32 v16, v16
	v_exp_f32_e32 v18, v18
	v_exp_f32_e32 v19, v19
	v_exp_f32_e32 v17, v17
	v_mul_f32_e32 v8, 0x41000000, v8
	v_pk_mul_f32 v[14:15], v[118:119], v[126:127]
	v_pk_add_f32 v[18:19], v[18:19], 1.0 op_sel_hi:[1,0]
	v_pk_add_f32 v[16:17], v[16:17], 1.0 op_sel_hi:[1,0]
	v_rcp_f32_e32 v18, v18
	v_rcp_f32_e32 v19, v19
	v_rcp_f32_e32 v16, v16
	v_rcp_f32_e32 v17, v17
	v_pk_mul_f32 v[14:15], v[14:15], v[8:9] op_sel_hi:[1,0]
	v_pk_mul_f32 v[12:13], v[12:13], v[8:9] op_sel_hi:[1,0]
	v_pk_mul_f32 v[14:15], v[14:15], v[18:19]
	v_pk_mul_f32 v[12:13], v[12:13], v[16:17]
	v_pk_mul_f32 v[16:17], v[112:113], v[124:125]
	v_pk_mul_f32 v[18:19], v[110:111], v[122:123]
	v_pk_mul_f32 v[20:21], v[110:111], v[6:7] op_sel_hi:[1,0]
	v_pk_mul_f32 v[18:19], v[18:19], v[8:9] op_sel_hi:[1,0]
	v_pk_mul_f32 v[8:9], v[16:17], v[8:9] op_sel_hi:[1,0]
	v_pk_mul_f32 v[16:17], v[112:113], v[6:7] op_sel_hi:[1,0]
	v_exp_f32_e32 v20, v20
	v_exp_f32_e32 v21, v21
	v_exp_f32_e32 v16, v16
	v_exp_f32_e32 v17, v17
	v_med3_f32 v6, v14, s71, v228
	v_pk_add_f32 v[20:21], v[20:21], 1.0 op_sel_hi:[1,0]
	v_med3_f32 v14, v15, s71, v228
	v_pk_add_f32 v[16:17], v[16:17], 1.0 op_sel_hi:[1,0]
	v_rcp_f32_e32 v20, v20
	v_rcp_f32_e32 v21, v21
	v_rcp_f32_e32 v16, v16
	v_rcp_f32_e32 v17, v17
	v_med3_f32 v15, v12, s71, v228
	v_mov_b32_e32 v12, v65
	v_cvt_pk_fp8_f32 v12, v6, v14
	v_pk_mul_f32 v[8:9], v[8:9], v[16:17]
	v_pk_mul_f32 v[16:17], v[18:19], v[20:21]
	v_med3_f32 v13, v13, s71, v228
	v_cvt_pk_fp8_f32 v12, v15, v13 op_sel:[0,0,1]
	v_med3_f32 v6, v16, s71, v228
	v_med3_f32 v14, v17, s71, v228
	v_mov_b32_e32 v13, v65
	v_cvt_pk_fp8_f32 v13, v6, v14
	v_med3_f32 v8, v8, s71, v228
	v_med3_f32 v9, v9, s71, v228
	v_add_u32_e32 v11, 0x80, v10
	v_cvt_pk_fp8_f32 v13, v8, v9 op_sel:[0,0,1]
	v_mad_i64_i32 v[8:9], s[26:27], v11, s78, v[4:5]
	v_lshl_add_u64 v[8:9], v[8:9], 0, v[0:1]
	global_store_dwordx2 v[8:9], v[12:13], off
	v_mul_f32_e32 v8, 0xbfb8aa3b, v7
	v_pk_mul_f32 v[16:17], v[108:109], v[8:9] op_sel_hi:[1,0]
	v_pk_mul_f32 v[18:19], v[106:107], v[8:9] op_sel_hi:[1,0]
	v_exp_f32_e32 v16, v16
	v_exp_f32_e32 v18, v18
	v_exp_f32_e32 v19, v19
	v_exp_f32_e32 v17, v17
	v_mul_f32_e32 v6, v7, v7
	v_mul_f32_e32 v6, 0x41000000, v6
	v_pk_add_f32 v[18:19], v[18:19], 1.0 op_sel_hi:[1,0]
	v_pk_add_f32 v[16:17], v[16:17], 1.0 op_sel_hi:[1,0]
	v_rcp_f32_e32 v18, v18
	v_rcp_f32_e32 v19, v19
	v_rcp_f32_e32 v16, v16
	v_rcp_f32_e32 v17, v17
	v_pk_mul_f32 v[12:13], v[108:109], v[116:117]
	v_pk_mul_f32 v[14:15], v[106:107], v[114:115]
	v_pk_mul_f32 v[12:13], v[12:13], v[6:7] op_sel_hi:[1,0]
	v_pk_mul_f32 v[14:15], v[14:15], v[6:7] op_sel_hi:[1,0]
	v_pk_mul_f32 v[12:13], v[12:13], v[16:17]
	v_pk_mul_f32 v[14:15], v[14:15], v[18:19]
	v_pk_mul_f32 v[16:17], v[100:101], v[104:105]
	v_pk_mul_f32 v[18:19], v[98:99], v[102:103]
	v_med3_f32 v14, v14, s71, v228
	v_pk_mul_f32 v[18:19], v[18:19], v[6:7] op_sel_hi:[1,0]
	v_pk_mul_f32 v[6:7], v[16:17], v[6:7] op_sel_hi:[1,0]
	v_pk_mul_f32 v[16:17], v[100:101], v[8:9] op_sel_hi:[1,0]
	v_pk_mul_f32 v[8:9], v[98:99], v[8:9] op_sel_hi:[1,0]
	v_exp_f32_e32 v16, v16
	v_exp_f32_e32 v17, v17
	v_exp_f32_e32 v8, v8
	v_exp_f32_e32 v9, v9
	v_med3_f32 v15, v15, s71, v228
	v_pk_add_f32 v[16:17], v[16:17], 1.0 op_sel_hi:[1,0]
	v_med3_f32 v13, v13, s71, v228
	v_rcp_f32_e32 v16, v16
	v_rcp_f32_e32 v17, v17
	v_pk_add_f32 v[8:9], v[8:9], 1.0 op_sel_hi:[1,0]
	v_add_u32_e32 v11, 0x90, v10
	v_rcp_f32_e32 v8, v8
	v_rcp_f32_e32 v9, v9
	v_pk_mul_f32 v[6:7], v[6:7], v[16:17]
	v_med3_f32 v16, v12, s71, v228
	v_mov_b32_e32 v12, v65
	v_cvt_pk_fp8_f32 v12, v14, v15
	v_pk_mul_f32 v[8:9], v[18:19], v[8:9]
	v_med3_f32 v6, v6, s71, v228
	v_med3_f32 v8, v8, s71, v228
	v_cvt_pk_fp8_f32 v12, v16, v13 op_sel:[0,0,1]
	v_med3_f32 v9, v9, s71, v228
	v_mov_b32_e32 v13, v65
	v_cvt_pk_fp8_f32 v13, v8, v9
	v_med3_f32 v7, v7, s71, v228
	v_pk_mul_f32 v[8:9], v[92:93], v[96:97]
	v_cvt_pk_fp8_f32 v13, v6, v7 op_sel:[0,0,1]
	v_mad_i64_i32 v[6:7], s[26:27], v11, s78, v[4:5]
	v_lshl_add_u64 v[6:7], v[6:7], 0, v[0:1]
	global_store_dwordx2 v[6:7], v[12:13], off
	v_mul_f32_e32 v6, v2, v2
	v_mul_f32_e32 v2, 0xbfb8aa3b, v2
	v_pk_mul_f32 v[14:15], v[92:93], v[2:3] op_sel_hi:[1,0]
	v_pk_mul_f32 v[16:17], v[90:91], v[2:3] op_sel_hi:[1,0]
	v_exp_f32_e32 v14, v14
	v_exp_f32_e32 v16, v16
	v_exp_f32_e32 v17, v17
	v_exp_f32_e32 v15, v15
	v_mul_f32_e32 v6, 0x41000000, v6
	v_pk_mul_f32 v[12:13], v[90:91], v[94:95]
	v_pk_add_f32 v[16:17], v[16:17], 1.0 op_sel_hi:[1,0]
	v_pk_add_f32 v[14:15], v[14:15], 1.0 op_sel_hi:[1,0]
	v_rcp_f32_e32 v16, v16
	v_rcp_f32_e32 v17, v17
	v_rcp_f32_e32 v14, v14
	v_rcp_f32_e32 v15, v15
	v_pk_mul_f32 v[12:13], v[12:13], v[6:7] op_sel_hi:[1,0]
	v_pk_mul_f32 v[8:9], v[8:9], v[6:7] op_sel_hi:[1,0]
	v_pk_mul_f32 v[12:13], v[12:13], v[16:17]
	v_pk_mul_f32 v[8:9], v[8:9], v[14:15]
	v_pk_mul_f32 v[14:15], v[84:85], v[88:89]
	v_pk_mul_f32 v[16:17], v[82:83], v[86:87]
	v_pk_mul_f32 v[18:19], v[82:83], v[2:3] op_sel_hi:[1,0]
	v_pk_mul_f32 v[16:17], v[16:17], v[6:7] op_sel_hi:[1,0]
	v_pk_mul_f32 v[6:7], v[14:15], v[6:7] op_sel_hi:[1,0]
	v_pk_mul_f32 v[14:15], v[84:85], v[2:3] op_sel_hi:[1,0]
	v_exp_f32_e32 v18, v18
	v_exp_f32_e32 v19, v19
	v_exp_f32_e32 v14, v14
	v_exp_f32_e32 v15, v15
	v_med3_f32 v11, v12, s71, v228
	v_pk_add_f32 v[18:19], v[18:19], 1.0 op_sel_hi:[1,0]
	v_med3_f32 v12, v13, s71, v228
	v_pk_add_f32 v[14:15], v[14:15], 1.0 op_sel_hi:[1,0]
	v_rcp_f32_e32 v18, v18
	v_rcp_f32_e32 v19, v19
	v_rcp_f32_e32 v14, v14
	v_rcp_f32_e32 v15, v15
	v_med3_f32 v13, v8, s71, v228
	v_mov_b32_e32 v8, v65
	v_cvt_pk_fp8_f32 v8, v11, v12
	v_pk_mul_f32 v[6:7], v[6:7], v[14:15]
	v_pk_mul_f32 v[14:15], v[16:17], v[18:19]
	v_med3_f32 v9, v9, s71, v228
	v_cvt_pk_fp8_f32 v8, v13, v9 op_sel:[0,0,1]
	v_med3_f32 v11, v14, s71, v228
	v_med3_f32 v12, v15, s71, v228
	v_mov_b32_e32 v9, v65
	v_cvt_pk_fp8_f32 v9, v11, v12
	v_med3_f32 v6, v6, s71, v228
	v_med3_f32 v7, v7, s71, v228
	v_add_u32_e32 v2, 0xa0, v10
	v_cvt_pk_fp8_f32 v9, v6, v7 op_sel:[0,0,1]
	v_mad_i64_i32 v[6:7], s[26:27], v2, s78, v[4:5]
	v_lshl_add_u64 v[6:7], v[6:7], 0, v[0:1]
	global_store_dwordx2 v[6:7], v[8:9], off
	v_mul_f32_e32 v6, 0xbfb8aa3b, v3
	v_pk_mul_f32 v[14:15], v[76:77], v[6:7] op_sel_hi:[1,0]
	v_pk_mul_f32 v[16:17], v[74:75], v[6:7] op_sel_hi:[1,0]
	v_exp_f32_e32 v14, v14
	v_exp_f32_e32 v16, v16
	v_exp_f32_e32 v17, v17
	v_exp_f32_e32 v15, v15
	v_mul_f32_e32 v2, v3, v3
	v_mul_f32_e32 v2, 0x41000000, v2
	v_pk_add_f32 v[16:17], v[16:17], 1.0 op_sel_hi:[1,0]
	v_pk_add_f32 v[14:15], v[14:15], 1.0 op_sel_hi:[1,0]
	v_rcp_f32_e32 v16, v16
	v_rcp_f32_e32 v17, v17
	v_rcp_f32_e32 v14, v14
	v_rcp_f32_e32 v15, v15
	v_pk_mul_f32 v[8:9], v[76:77], v[80:81]
	v_pk_mul_f32 v[12:13], v[74:75], v[78:79]
	v_pk_mul_f32 v[8:9], v[8:9], v[2:3] op_sel_hi:[1,0]
	v_pk_mul_f32 v[12:13], v[12:13], v[2:3] op_sel_hi:[1,0]
	v_pk_mul_f32 v[8:9], v[8:9], v[14:15]
	v_pk_mul_f32 v[12:13], v[12:13], v[16:17]
	v_pk_mul_f32 v[14:15], v[68:69], v[72:73]
	v_pk_mul_f32 v[16:17], v[66:67], v[70:71]
	v_med3_f32 v11, v12, s71, v228
	v_pk_mul_f32 v[16:17], v[16:17], v[2:3] op_sel_hi:[1,0]
	v_pk_mul_f32 v[2:3], v[14:15], v[2:3] op_sel_hi:[1,0]
	v_pk_mul_f32 v[14:15], v[68:69], v[6:7] op_sel_hi:[1,0]
	v_pk_mul_f32 v[6:7], v[66:67], v[6:7] op_sel_hi:[1,0]
	v_exp_f32_e32 v14, v14
	v_exp_f32_e32 v6, v6
	v_exp_f32_e32 v7, v7
	v_exp_f32_e32 v15, v15
	v_med3_f32 v12, v13, s71, v228
	v_med3_f32 v13, v8, s71, v228
	v_pk_add_f32 v[6:7], v[6:7], 1.0 op_sel_hi:[1,0]
	v_mov_b32_e32 v8, v65
	v_rcp_f32_e32 v6, v6
	v_rcp_f32_e32 v7, v7
	v_cvt_pk_fp8_f32 v8, v11, v12
	v_pk_add_f32 v[14:15], v[14:15], 1.0 op_sel_hi:[1,0]
	v_med3_f32 v9, v9, s71, v228
	v_rcp_f32_e32 v14, v14
	v_rcp_f32_e32 v15, v15
	v_pk_mul_f32 v[6:7], v[16:17], v[6:7]
	v_cvt_pk_fp8_f32 v8, v13, v9 op_sel:[0,0,1]
	v_med3_f32 v6, v6, s71, v228
	v_med3_f32 v7, v7, s71, v228
	v_mov_b32_e32 v9, v65
	v_cvt_pk_fp8_f32 v9, v6, v7
	v_pk_mul_f32 v[2:3], v[2:3], v[14:15]
	v_add_u32_e32 v10, 0xb0, v10
	v_med3_f32 v2, v2, s71, v228
	v_med3_f32 v3, v3, s71, v228
	v_cvt_pk_fp8_f32 v9, v2, v3 op_sel:[0,0,1]
	v_mad_i64_i32 v[2:3], s[26:27], v10, s78, v[4:5]
	v_lshl_add_u64 v[0:1], v[2:3], 0, v[0:1]
	s_mov_b64 s[26:27], -1
	global_store_dwordx2 v[0:1], v[8:9], off
	s_cbranch_vccnz .LBB0_1172
	s_andn2_b64 vcc, exec, s[16:17]
	s_cbranch_vccnz .LBB0_1171
	s_barrier
	s_branch .LBB0_1171

.LBB0_1278:
	v_mul_i32_i24_e32 v14, 64, v0
	v_sub_u32_e32 v3, v3, v14
	v_mov_b32_e32 v14, 1
	v_lshlrev_b32_e32 v2, 5, v2
	v_ashrrev_i16_sdwa v3, v14, sext(v3) dst_sel:DWORD dst_unused:UNUSED_PAD src0_sel:DWORD src1_sel:BYTE_0
	v_and_b32_e32 v2, 32, v2
	v_bfe_i32 v3, v3, 0, 16
	v_add_lshl_u32 v182, v2, v3, 1
	v_lshlrev_b32_e32 v3, 6, v1
	v_sub_u32_e32 v3, v9, v3
	v_lshlrev_b32_e32 v2, 5, v8
	v_ashrrev_i16_sdwa v3, v14, sext(v3) dst_sel:DWORD dst_unused:UNUSED_PAD src0_sel:DWORD src1_sel:BYTE_0
	s_cmp_ge_i32 s83, s49
	v_and_b32_e32 v2, 32, v2
	v_bfe_i32 v3, v3, 0, 16
	s_cselect_b64 s[6:7], -1, 0
	s_cmp_ge_i32 s83, s50
	v_add_lshl_u32 v183, v2, v3, 1
	v_cndmask_b32_e64 v2, 0, 1, s[6:7]
	s_cselect_b64 s[6:7], -1, 0
	s_cmp_ge_i32 s83, s51
	v_cndmask_b32_e64 v3, 0, 1, s[6:7]
	s_cselect_b64 vcc, -1, 0
	s_cmp_ge_i32 s83, s60
	v_addc_co_u32_e32 v2, vcc, v3, v2, vcc
	s_cselect_b64 s[6:7], -1, 0
	s_cmp_ge_i32 s83, s61
	v_cndmask_b32_e64 v3, 0, 1, s[6:7]
	s_cselect_b64 vcc, -1, 0
	s_cmp_ge_i32 s83, s62
	v_addc_co_u32_e32 v2, vcc, v2, v3, vcc
	s_cselect_b64 s[6:7], -1, 0
	s_cmp_ge_i32 s83, s63
	v_cndmask_b32_e64 v3, 0, 1, s[6:7]
	s_cselect_b64 vcc, -1, 0
	v_addc_co_u32_e32 v184, vcc, v2, v3, vcc
	s_waitcnt vmcnt(0)
	v_max_i32_e32 v2, 0, v10
	v_lshl_add_u32 v174, v2, 10, v182
	v_max_i32_e32 v2, 0, v11
	v_lshl_add_u32 v176, v2, 10, v183
	v_max_i32_e32 v2, 0, v12
	v_lshl_add_u32 v32, v2, 10, v182
	v_max_i32_e32 v2, 0, v13
	s_mov_b32 s6, 0x700000
	v_lshl_add_u32 v178, v2, 10, v183
	v_mul_hi_u32 v3, v184, s6
	v_mul_lo_u32 v2, v184, s6
	s_ashr_i32 s39, s38, 31
	v_lshl_add_u64 v[2:3], s[10:11], 0, v[2:3]
	s_lshl_b64 s[22:23], s[38:39], 18
	v_lshl_add_u64 v[180:181], v[2:3], 0, s[22:23]
	v_lshlrev_b32_e32 v2, 1, v4
	v_lshrrev_b32_e32 v3, 2, v4
	v_and_b32_e32 v0, 3, v0
	s_mov_b32 s7, 0x3fffe0
	v_and_b32_e32 v2, 24, v2
	v_and_b32_e32 v3, 4, v3
	v_and_or_b32 v0, v4, s7, v0
	v_or3_b32 v0, v0, v3, v2
	v_and_b32_e32 v1, 3, v1
	v_lshl_add_u32 v162, v0, 10, v182
	v_lshlrev_b32_e32 v0, 1, v5
	v_lshrrev_b32_e32 v2, 2, v5
	v_and_or_b32 v1, v5, s7, v1
	s_lshl_b32 s7, s28, 10
	v_and_b32_e32 v0, 24, v0
	v_and_b32_e32 v2, 4, v2
	s_add_i32 s39, s7, 0
	v_or3_b32 v0, v1, v2, v0
	s_add_i32 m0, s39, 0x10000
	v_readfirstlane_b32 s22, v180
	v_readfirstlane_b32 s23, v181
	v_lshl_add_u32 v164, v0, 10, v183
	s_add_i32 s56, s39, 0x2000
	s_add_i32 s57, s39, 0x4000
	s_add_i32 s66, s39, 0x6000
	s_ashr_i32 s29, s36, 8
	global_load_lds_dwordx4 v162, s[22:23]
	s_add_i32 m0, s39, 0x12000
	v_mov_b32_e32 v33, 0
	global_load_lds_dwordx4 v164, s[22:23]
	s_mov_b64 s[22:23], 0x20000
	v_lshl_add_u64 v[0:1], v[180:181], 0, s[22:23]
	s_add_i32 m0, s39, 0x14000
	v_readfirstlane_b32 s24, v0
	v_readfirstlane_b32 s25, v1
	v_mov_b32_e32 v163, v33
	v_mov_b32_e32 v165, v33
	v_writelane_b32 v254, s37, 27
	v_lshl_add_u64 v[2:3], v[180:181], 0, v[162:163]
	v_lshl_add_u64 v[0:1], v[180:181], 0, v[164:165]
	global_load_lds_dwordx4 v162, s[24:25]
	s_add_i32 m0, s39, 0x16000
	s_cmp_eq_u32 s29, 1
	global_load_lds_dwordx4 v164, s[24:25]
	s_mov_b32 m0, s39
	v_mov_b32_e32 v175, v33
	global_load_lds_dwordx4 v174, s[8:9]
	s_mov_b32 m0, s56
	s_cselect_b64 s[24:25], -1, 0
	global_load_lds_dwordx4 v176, s[8:9]
	s_mov_b32 m0, s57
	s_cmp_lg_u32 s29, 1
	global_load_lds_dwordx4 v32, s[8:9]
	s_mov_b32 m0, s66
	v_mov_b32_e32 v177, v33
	global_load_lds_dwordx4 v178, s[8:9]
	s_cbranch_scc1 .LBB0_1280
	s_barrier
.LBB0_1280:
	s_add_u32 s26, s54, 0x24900000
	s_mov_b64 s[40:41], 0x80
	s_addc_u32 s27, s55, 0
	s_add_i32 m0, s39, 0x18000
	v_lshl_add_u64 v[2:3], v[2:3], 0, s[40:41]
	s_waitcnt vmcnt(2)
	s_barrier
	global_load_lds_dwordx4 v[2:3], off
	v_lshl_add_u64 v[0:1], v[0:1], 0, s[40:41]
	s_add_i32 m0, s39, 0x1a000
	s_add_i32 s67, s39, 0x8000
	global_load_lds_dwordx4 v[0:1], off
	v_lshl_add_u64 v[0:1], s[12:13], 0, v[174:175]
	s_mov_b32 m0, s67
	s_add_i32 s68, s39, 0xa000
	global_load_lds_dwordx4 v[0:1], off
	v_lshl_add_u64 v[0:1], s[12:13], 0, v[176:177]
	s_mov_b32 m0, s68
	s_mov_b64 s[40:41], 0x20080
	global_load_lds_dwordx4 v[0:1], off
	v_lshl_add_u64 v[0:1], v[180:181], 0, s[40:41]
	s_add_i32 m0, s39, 0x1c000
	v_lshl_add_u64 v[2:3], v[0:1], 0, v[162:163]
	global_load_lds_dwordx4 v[2:3], off
	v_lshl_add_u64 v[0:1], v[0:1], 0, v[164:165]
	s_add_i32 m0, s39, 0x1e000
	v_and_b32_e32 v8, 15, v7
	global_load_lds_dwordx4 v[0:1], off
	v_lshrrev_b32_e32 v7, 1, v7
	v_and_b32_e32 v7, 24, v7
	v_lshlrev_b32_e32 v9, 1, v7
	v_lshl_or_b32 v185, s29, 6, v8
	v_lshl_or_b32 v9, v8, 6, v9
	v_lshlrev_b32_e32 v8, 2, v8
	s_lshl_b32 s29, s29, 13
	v_and_b32_e32 v10, 32, v8
	v_bitop3_b32 v11, v9, s29, v10 bitop3:0xde
	s_lshl_b32 s29, s28, 5
	s_and_b32 s37, s29, 0x60
	s_and_b32 s40, s36, 0xffffffc0
	s_lshl_b32 s29, s37, 7
	s_lshl_b32 s69, s28, 8
	s_add_i32 s42, 0, 0x20400
	s_ashr_i32 s41, s40, 31
	v_bitop3_b32 v186, v9, s29, v10 bitop3:0xde
	s_add_i32 s70, s42, s69
	s_lshl_b64 s[28:29], s[40:41], 2
	s_add_u32 s28, s20, s28
	s_addc_u32 s29, s21, s29
	v_or_b32_e32 v0, s40, v6
	v_lshlrev_b32_e32 v2, 2, v6
	v_mov_b32_e32 v3, v33
	s_cmpk_lt_u32 s36, 0x100
	s_waitcnt vmcnt(6)
	v_lshlrev_b32_e32 v0, 2, v0
	v_lshl_add_u64 v[166:167], s[28:29], 0, v[2:3]
	s_cselect_b64 s[28:29], -1, 0
	s_and_b32 s36, s36, 0xffffff00
	s_mov_b32 s35, 0
	v_ashrrev_i32_e32 v1, 31, v0
	s_add_i32 s42, s42, s36
	v_lshlrev_b32_e32 v175, 2, v4
	v_lshlrev_b32_e32 v177, 2, v5
	v_lshl_add_u64 v[168:169], s[30:31], 0, v[0:1]
	v_or_b32_e32 v187, s37, v7
	v_add_u32_e32 v188, s42, v8
	v_mov_b64_e32 v[170:171], s[34:35]
	s_add_i32 s71, 0, 0x20200
	s_add_i32 s78, 0, 0x10000
	s_add_i32 s79, 0, 0x14000
	v_add_u32_e32 v189, 0, v11
	v_mov_b32_e32 v190, 0x7f7f7f7f
	s_mov_b32 s80, 0xc3dc0000
	s_movk_i32 s81, 0xe00
	v_mov_b32_e32 v191, 0x43dc0000
	s_mov_b32 s84, s83
	s_barrier
	s_branch .LBB0_1283

.LBB0_1282:
	s_andn2_b64 vcc, exec, s[34:35]
	v_mov_b32_e32 v178, v195
	v_mov_b32_e32 v32, v194
	v_mov_b32_e32 v176, v193
	v_mov_b32_e32 v174, v192
	s_mov_b32 s38, s30
	s_mov_b32 s83, s84
	v_mov_b64_e32 v[180:181], v[172:173]
	s_mov_b32 s35, s82
	s_cbranch_vccz .LBB0_1300

.LBB0_1291:
	v_mul_hi_u32 v1, v184, s6
	v_mul_lo_u32 v0, v184, s6
	s_ashr_i32 s31, s30, 31
	v_lshl_add_u64 v[0:1], s[10:11], 0, v[0:1]
	s_lshl_b64 s[40:41], s[30:31], 18
	v_mov_b32_e32 v78, 0
	v_lshl_add_u64 v[172:173], v[0:1], 0, s[40:41]
	v_mov_b32_e32 v179, v33
	s_mov_b32 s31, 0
	s_xor_b64 s[40:41], s[36:37], -1
	s_mov_b64 s[42:43], s[12:13]
	v_mov_b32_e32 v195, v178
	v_mov_b32_e32 v194, v32
	v_mov_b32_e32 v193, v176
	v_mov_b32_e32 v192, v174
	v_mov_b32_e32 v79, v78
	v_mov_b32_e32 v80, v78
	v_mov_b32_e32 v81, v78
	v_mov_b32_e32 v86, v78
	v_mov_b32_e32 v87, v78
	v_mov_b32_e32 v88, v78
	v_mov_b32_e32 v89, v78
	v_mov_b32_e32 v98, v78
	v_mov_b32_e32 v99, v78
	v_mov_b32_e32 v100, v78
	v_mov_b32_e32 v101, v78
	v_mov_b32_e32 v106, v78
	v_mov_b32_e32 v107, v78
	v_mov_b32_e32 v108, v78
	v_mov_b32_e32 v109, v78
	v_mov_b32_e32 v114, v78
	v_mov_b32_e32 v115, v78
	v_mov_b32_e32 v116, v78
	v_mov_b32_e32 v117, v78
	v_mov_b32_e32 v122, v78
	v_mov_b32_e32 v123, v78
	v_mov_b32_e32 v124, v78
	v_mov_b32_e32 v125, v78
	v_mov_b32_e32 v130, v78
	v_mov_b32_e32 v131, v78
	v_mov_b32_e32 v132, v78
	v_mov_b32_e32 v133, v78
	v_mov_b32_e32 v138, v78
	v_mov_b32_e32 v139, v78
	v_mov_b32_e32 v140, v78
	v_mov_b32_e32 v141, v78
	v_mov_b32_e32 v146, v78
	v_mov_b32_e32 v147, v78
	v_mov_b32_e32 v148, v78
	v_mov_b32_e32 v149, v78
	v_mov_b32_e32 v154, v78
	v_mov_b32_e32 v155, v78
	v_mov_b32_e32 v156, v78
	v_mov_b32_e32 v157, v78
	v_mov_b32_e32 v102, v78
	v_mov_b32_e32 v103, v78
	v_mov_b32_e32 v104, v78
	v_mov_b32_e32 v105, v78
	v_mov_b32_e32 v110, v78
	v_mov_b32_e32 v111, v78
	v_mov_b32_e32 v112, v78
	v_mov_b32_e32 v113, v78
	v_mov_b32_e32 v118, v78
	v_mov_b32_e32 v119, v78
	v_mov_b32_e32 v120, v78
	v_mov_b32_e32 v121, v78
	v_mov_b32_e32 v126, v78
	v_mov_b32_e32 v127, v78
	v_mov_b32_e32 v128, v78
	v_mov_b32_e32 v129, v78
	v_mov_b32_e32 v134, v78
	v_mov_b32_e32 v135, v78
	v_mov_b32_e32 v136, v78
	v_mov_b32_e32 v137, v78
	v_mov_b32_e32 v142, v78
	v_mov_b32_e32 v143, v78
	v_mov_b32_e32 v144, v78
	v_mov_b32_e32 v145, v78
	v_mov_b32_e32 v150, v78
	v_mov_b32_e32 v151, v78
	v_mov_b32_e32 v152, v78
	v_mov_b32_e32 v153, v78
	v_mov_b32_e32 v158, v78
	v_mov_b32_e32 v159, v78
	v_mov_b32_e32 v160, v78
	v_mov_b32_e32 v161, v78
	v_mov_b32_e32 v74, v78
	v_mov_b32_e32 v75, v78
	v_mov_b32_e32 v76, v78
	v_mov_b32_e32 v77, v78
	v_mov_b32_e32 v66, v78
	v_mov_b32_e32 v67, v78
	v_mov_b32_e32 v68, v78
	v_mov_b32_e32 v69, v78
	v_mov_b32_e32 v58, v78
	v_mov_b32_e32 v59, v78
	v_mov_b32_e32 v60, v78
	v_mov_b32_e32 v61, v78
	v_mov_b32_e32 v50, v78
	v_mov_b32_e32 v51, v78
	v_mov_b32_e32 v52, v78
	v_mov_b32_e32 v53, v78
	v_mov_b32_e32 v42, v78
	v_mov_b32_e32 v43, v78
	v_mov_b32_e32 v44, v78
	v_mov_b32_e32 v45, v78
	v_mov_b32_e32 v34, v78
	v_mov_b32_e32 v35, v78
	v_mov_b32_e32 v36, v78
	v_mov_b32_e32 v37, v78
	v_mov_b32_e32 v94, v78
	v_mov_b32_e32 v95, v78
	v_mov_b32_e32 v96, v78
	v_mov_b32_e32 v97, v78
	v_mov_b32_e32 v90, v78
	v_mov_b32_e32 v91, v78
	v_mov_b32_e32 v92, v78
	v_mov_b32_e32 v93, v78
	v_mov_b32_e32 v82, v78
	v_mov_b32_e32 v83, v78
	v_mov_b32_e32 v84, v78
	v_mov_b32_e32 v85, v78
	v_mov_b32_e32 v70, v78
	v_mov_b32_e32 v71, v78
	v_mov_b32_e32 v72, v78
	v_mov_b32_e32 v73, v78
	v_mov_b32_e32 v62, v78
	v_mov_b32_e32 v63, v78
	v_mov_b32_e32 v64, v78
	v_mov_b32_e32 v65, v78
	v_mov_b32_e32 v54, v78
	v_mov_b32_e32 v55, v78
	v_mov_b32_e32 v56, v78
	v_mov_b32_e32 v57, v78
	v_mov_b32_e32 v46, v78
	v_mov_b32_e32 v47, v78
	v_mov_b32_e32 v48, v78
	v_mov_b32_e32 v49, v78
	v_mov_b32_e32 v38, v78
	v_mov_b32_e32 v39, v78
	v_mov_b32_e32 v40, v78
	v_mov_b32_e32 v41, v78
	s_branch .LBB0_1293
.LBB0_1292:
	v_add_u32_e32 v0, s78, v186
	v_add_u32_e32 v4, s79, v186
	ds_read_b128 v[24:27], v0
	ds_read_b128 v[28:31], v0 offset:1024
	ds_read_b128 v[16:19], v0 offset:2048
	ds_read_b128 v[20:23], v0 offset:3072
	ds_read_b128 v[8:11], v4
	ds_read_b128 v[12:15], v4 offset:1024
	ds_read_b128 v[0:3], v4 offset:2048
	ds_read_b128 v[4:7], v4 offset:3072
	v_lshl_add_u64 v[228:229], s[42:43], 0, v[32:33]
	s_add_i32 m0, s39, 0xc000
	ds_read_b128 v[196:199], v189
	ds_read_b128 v[200:203], v189 offset:1024
	ds_read_b128 v[204:207], v189 offset:2048
	ds_read_b128 v[208:211], v189 offset:3072
	ds_read_b128 v[212:215], v189 offset:4096
	ds_read_b128 v[216:219], v189 offset:5120
	ds_read_b128 v[220:223], v189 offset:6144
	ds_read_b128 v[224:227], v189 offset:7168
	global_load_lds_dwordx4 v[228:229], off
	v_lshl_add_u64 v[228:229], s[42:43], 0, v[178:179]
	s_add_i32 m0, s39, 0xe000
	s_nop 0
	global_load_lds_dwordx4 v[228:229], off
	s_waitcnt vmcnt(8)
	s_waitcnt lgkmcnt(0)
	s_barrier
	s_setprio 1
	s_waitcnt lgkmcnt(0)
	v_mfma_scale_f32_16x16x128_f8f6f4 v[158:161], v[24:31], v[196:203], v[158:161], v190, v190 op_sel_hi:[0,0,0]
	v_mfma_scale_f32_16x16x128_f8f6f4 v[150:153], v[16:23], v[196:203], v[150:153], v190, v190 op_sel_hi:[0,0,0]
	v_mfma_scale_f32_16x16x128_f8f6f4 v[142:145], v[24:31], v[204:211], v[142:145], v190, v190 op_sel_hi:[0,0,0]
	v_mfma_scale_f32_16x16x128_f8f6f4 v[134:137], v[16:23], v[204:211], v[134:137], v190, v190 op_sel_hi:[0,0,0]
	v_mfma_scale_f32_16x16x128_f8f6f4 v[126:129], v[24:31], v[212:219], v[126:129], v190, v190 op_sel_hi:[0,0,0]
	v_mfma_scale_f32_16x16x128_f8f6f4 v[118:121], v[16:23], v[212:219], v[118:121], v190, v190 op_sel_hi:[0,0,0]
	v_mfma_scale_f32_16x16x128_f8f6f4 v[110:113], v[24:31], v[220:227], v[110:113], v190, v190 op_sel_hi:[0,0,0]
	v_mfma_scale_f32_16x16x128_f8f6f4 v[102:105], v[16:23], v[220:227], v[102:105], v190, v190 op_sel_hi:[0,0,0]
	s_setprio 0
	s_setprio 1
	v_mfma_scale_f32_16x16x128_f8f6f4 v[154:157], v[8:15], v[196:203], v[154:157], v190, v190 op_sel_hi:[0,0,0]
	v_mfma_scale_f32_16x16x128_f8f6f4 v[146:149], v[0:7], v[196:203], v[146:149], v190, v190 op_sel_hi:[0,0,0]
	v_mfma_scale_f32_16x16x128_f8f6f4 v[138:141], v[8:15], v[204:211], v[138:141], v190, v190 op_sel_hi:[0,0,0]
	v_mfma_scale_f32_16x16x128_f8f6f4 v[130:133], v[0:7], v[204:211], v[130:133], v190, v190 op_sel_hi:[0,0,0]
	v_mfma_scale_f32_16x16x128_f8f6f4 v[122:125], v[8:15], v[212:219], v[122:125], v190, v190 op_sel_hi:[0,0,0]
	v_mfma_scale_f32_16x16x128_f8f6f4 v[114:117], v[0:7], v[212:219], v[114:117], v190, v190 op_sel_hi:[0,0,0]
	v_mfma_scale_f32_16x16x128_f8f6f4 v[106:109], v[8:15], v[220:227], v[106:109], v190, v190 op_sel_hi:[0,0,0]
	v_mfma_scale_f32_16x16x128_f8f6f4 v[98:101], v[0:7], v[220:227], v[98:101], v190, v190 op_sel_hi:[0,0,0]
	s_setprio 0
	s_barrier
	s_cmp_gt_u32 s31, 5
	v_sub_co_u32_e64 v230, s[44:45], s31, 6
	s_cselect_b64 vcc, -1, 0
	v_add_u32_e32 v231, 8, v230
	v_cndmask_b32_e32 v230, v231, v230, vcc
	v_ashrrev_i32_e32 v231, 31, v230
	v_cndmask_b32_e32 v229, v181, v173, vcc
	v_cndmask_b32_e32 v228, v180, v172, vcc
	v_lshlrev_b64 v[230:231], 7, v[230:231]
	v_lshl_add_u64 v[228:229], v[228:229], 0, v[230:231]
	s_add_i32 s34, s78, s7
	v_lshl_add_u64 v[232:233], v[228:229], 0, v[162:163]
	s_mov_b32 m0, s34
	ds_read_b128 v[196:199], v189 offset:16384
	ds_read_b128 v[200:203], v189 offset:17408
	ds_read_b128 v[204:207], v189 offset:18432
	ds_read_b128 v[208:211], v189 offset:19456
	ds_read_b128 v[212:215], v189 offset:20480
	ds_read_b128 v[216:219], v189 offset:21504
	ds_read_b128 v[220:223], v189 offset:22528
	ds_read_b128 v[224:227], v189 offset:23552
	global_load_lds_dwordx4 v[232:233], off
	v_lshl_add_u64 v[232:233], v[228:229], 0, v[164:165]
	s_add_i32 m0, s34, 0x2000
	v_lshl_add_u64 v[228:229], v[228:229], 0, s[22:23]
	s_add_i32 s34, s79, s7
	global_load_lds_dwordx4 v[232:233], off
	v_lshl_add_u64 v[232:233], v[228:229], 0, v[162:163]
	s_mov_b32 m0, s34
	v_lshl_add_u64 v[228:229], v[228:229], 0, v[164:165]
	global_load_lds_dwordx4 v[232:233], off
	s_add_i32 m0, s34, 0x2000
	s_nop 0
	global_load_lds_dwordx4 v[228:229], off
	v_lshl_add_u64 v[228:229], s[8:9], 0, v[230:231]
	v_cndmask_b32_e32 v230, v174, v192, vcc
	v_readfirstlane_b32 s46, v228
	v_readfirstlane_b32 s47, v229
	s_mov_b32 m0, s39
	v_cndmask_b32_e32 v231, v176, v193, vcc
	s_nop 2
	global_load_lds_dwordx4 v230, s[46:47]
	s_mov_b32 m0, s56
	s_nop 0
	global_load_lds_dwordx4 v231, s[46:47]
	s_waitcnt vmcnt(8)
	s_waitcnt lgkmcnt(0)
	s_barrier
	s_setprio 1
	s_waitcnt lgkmcnt(0)
	v_mfma_scale_f32_16x16x128_f8f6f4 v[86:89], v[24:31], v[196:203], v[86:89], v190, v190 op_sel_hi:[0,0,0]
	v_mfma_scale_f32_16x16x128_f8f6f4 v[78:81], v[16:23], v[196:203], v[78:81], v190, v190 op_sel_hi:[0,0,0]
	v_mfma_scale_f32_16x16x128_f8f6f4 v[74:77], v[24:31], v[204:211], v[74:77], v190, v190 op_sel_hi:[0,0,0]
	v_mfma_scale_f32_16x16x128_f8f6f4 v[66:69], v[16:23], v[204:211], v[66:69], v190, v190 op_sel_hi:[0,0,0]
	v_mfma_scale_f32_16x16x128_f8f6f4 v[58:61], v[24:31], v[212:219], v[58:61], v190, v190 op_sel_hi:[0,0,0]
	v_mfma_scale_f32_16x16x128_f8f6f4 v[50:53], v[16:23], v[212:219], v[50:53], v190, v190 op_sel_hi:[0,0,0]
	v_mfma_scale_f32_16x16x128_f8f6f4 v[42:45], v[24:31], v[220:227], v[42:45], v190, v190 op_sel_hi:[0,0,0]
	v_mfma_scale_f32_16x16x128_f8f6f4 v[34:37], v[16:23], v[220:227], v[34:37], v190, v190 op_sel_hi:[0,0,0]
	s_setprio 0
	s_setprio 1
	v_mfma_scale_f32_16x16x128_f8f6f4 v[94:97], v[8:15], v[196:203], v[94:97], v190, v190 op_sel_hi:[0,0,0]
	v_mfma_scale_f32_16x16x128_f8f6f4 v[90:93], v[0:7], v[196:203], v[90:93], v190, v190 op_sel_hi:[0,0,0]
	v_mfma_scale_f32_16x16x128_f8f6f4 v[82:85], v[8:15], v[204:211], v[82:85], v190, v190 op_sel_hi:[0,0,0]
	v_mfma_scale_f32_16x16x128_f8f6f4 v[70:73], v[0:7], v[204:211], v[70:73], v190, v190 op_sel_hi:[0,0,0]
	v_mfma_scale_f32_16x16x128_f8f6f4 v[62:65], v[8:15], v[212:219], v[62:65], v190, v190 op_sel_hi:[0,0,0]
	v_mfma_scale_f32_16x16x128_f8f6f4 v[54:57], v[0:7], v[212:219], v[54:57], v190, v190 op_sel_hi:[0,0,0]
	v_mfma_scale_f32_16x16x128_f8f6f4 v[46:49], v[8:15], v[220:227], v[46:49], v190, v190 op_sel_hi:[0,0,0]
	v_mfma_scale_f32_16x16x128_f8f6f4 v[38:41], v[0:7], v[220:227], v[38:41], v190, v190 op_sel_hi:[0,0,0]
	s_setprio 0
	s_barrier
	s_add_i32 s34, 0, 0x18000
	s_add_i32 s85, 0, 0x1c000
	v_add_u32_e32 v0, s34, v186
	v_add_u32_e32 v4, s85, v186
	ds_read_b128 v[16:19], v0
	ds_read_b128 v[20:23], v0 offset:1024
	ds_read_b128 v[24:27], v0 offset:2048
	ds_read_b128 v[28:31], v0 offset:3072
	ds_read_b128 v[8:11], v4
	ds_read_b128 v[12:15], v4 offset:1024
	ds_read_b128 v[0:3], v4 offset:2048
	ds_read_b128 v[4:7], v4 offset:3072
	s_mov_b32 m0, s57
	v_cndmask_b32_e32 v228, v32, v194, vcc
	ds_read_b128 v[196:199], v189 offset:32768
	ds_read_b128 v[200:203], v189 offset:33792
	ds_read_b128 v[204:207], v189 offset:34816
	ds_read_b128 v[208:211], v189 offset:35840
	ds_read_b128 v[212:215], v189 offset:36864
	ds_read_b128 v[216:219], v189 offset:37888
	ds_read_b128 v[220:223], v189 offset:38912
	ds_read_b128 v[224:227], v189 offset:39936
	v_cndmask_b32_e32 v229, v178, v195, vcc
	global_load_lds_dwordx4 v228, s[46:47]
	s_mov_b32 m0, s66
	s_nop 0
	global_load_lds_dwordx4 v229, s[46:47]
	s_waitcnt vmcnt(8)
	s_waitcnt lgkmcnt(0)
	s_barrier
	s_setprio 1
	s_waitcnt lgkmcnt(0)
	v_mfma_scale_f32_16x16x128_f8f6f4 v[158:161], v[16:23], v[196:203], v[158:161], v190, v190 op_sel_hi:[0,0,0]
	v_mfma_scale_f32_16x16x128_f8f6f4 v[150:153], v[24:31], v[196:203], v[150:153], v190, v190 op_sel_hi:[0,0,0]
	v_mfma_scale_f32_16x16x128_f8f6f4 v[142:145], v[16:23], v[204:211], v[142:145], v190, v190 op_sel_hi:[0,0,0]
	v_mfma_scale_f32_16x16x128_f8f6f4 v[134:137], v[24:31], v[204:211], v[134:137], v190, v190 op_sel_hi:[0,0,0]
	v_mfma_scale_f32_16x16x128_f8f6f4 v[126:129], v[16:23], v[212:219], v[126:129], v190, v190 op_sel_hi:[0,0,0]
	v_mfma_scale_f32_16x16x128_f8f6f4 v[118:121], v[24:31], v[212:219], v[118:121], v190, v190 op_sel_hi:[0,0,0]
	v_mfma_scale_f32_16x16x128_f8f6f4 v[110:113], v[16:23], v[220:227], v[110:113], v190, v190 op_sel_hi:[0,0,0]
	v_mfma_scale_f32_16x16x128_f8f6f4 v[102:105], v[24:31], v[220:227], v[102:105], v190, v190 op_sel_hi:[0,0,0]
	s_setprio 0
	s_setprio 1
	v_mfma_scale_f32_16x16x128_f8f6f4 v[154:157], v[8:15], v[196:203], v[154:157], v190, v190 op_sel_hi:[0,0,0]
	v_mfma_scale_f32_16x16x128_f8f6f4 v[146:149], v[0:7], v[196:203], v[146:149], v190, v190 op_sel_hi:[0,0,0]
	v_mfma_scale_f32_16x16x128_f8f6f4 v[138:141], v[8:15], v[204:211], v[138:141], v190, v190 op_sel_hi:[0,0,0]
	v_mfma_scale_f32_16x16x128_f8f6f4 v[130:133], v[0:7], v[204:211], v[130:133], v190, v190 op_sel_hi:[0,0,0]
	v_mfma_scale_f32_16x16x128_f8f6f4 v[122:125], v[8:15], v[212:219], v[122:125], v190, v190 op_sel_hi:[0,0,0]
	v_mfma_scale_f32_16x16x128_f8f6f4 v[114:117], v[0:7], v[212:219], v[114:117], v190, v190 op_sel_hi:[0,0,0]
	v_mfma_scale_f32_16x16x128_f8f6f4 v[106:109], v[8:15], v[220:227], v[106:109], v190, v190 op_sel_hi:[0,0,0]
	v_mfma_scale_f32_16x16x128_f8f6f4 v[98:101], v[0:7], v[220:227], v[98:101], v190, v190 op_sel_hi:[0,0,0]
	s_setprio 0
	s_barrier
	s_cmp_gt_u32 s31, 4
	s_cselect_b64 vcc, -1, 0
	s_and_b64 s[46:47], vcc, exec
	s_cselect_b32 s46, -5, 3
	s_add_i32 s46, s46, s31
	s_ashr_i32 s47, s46, 31
	v_cndmask_b32_e32 v229, v181, v173, vcc
	v_cndmask_b32_e32 v228, v180, v172, vcc
	s_lshl_b64 s[46:47], s[46:47], 7
	v_lshl_add_u64 v[228:229], v[228:229], 0, s[46:47]
	s_add_i32 s34, s34, s7
	v_lshl_add_u64 v[230:231], v[228:229], 0, v[162:163]
	s_mov_b32 m0, s34
	ds_read_b128 v[196:199], v189 offset:49152
	ds_read_b128 v[200:203], v189 offset:50176
	ds_read_b128 v[204:207], v189 offset:51200
	ds_read_b128 v[208:211], v189 offset:52224
	ds_read_b128 v[212:215], v189 offset:53248
	ds_read_b128 v[216:219], v189 offset:54272
	ds_read_b128 v[220:223], v189 offset:55296
	ds_read_b128 v[224:227], v189 offset:56320
	global_load_lds_dwordx4 v[230:231], off
	v_lshl_add_u64 v[230:231], v[228:229], 0, v[164:165]
	s_add_i32 m0, s34, 0x2000
	v_lshl_add_u64 v[228:229], v[228:229], 0, s[22:23]
	s_add_i32 s34, s85, s7
	global_load_lds_dwordx4 v[230:231], off
	v_lshl_add_u64 v[230:231], v[228:229], 0, v[162:163]
	s_mov_b32 m0, s34
	v_lshl_add_u64 v[228:229], v[228:229], 0, v[164:165]
	global_load_lds_dwordx4 v[230:231], off
	s_add_i32 m0, s34, 0x2000
	s_add_u32 s46, s8, s46
	global_load_lds_dwordx4 v[228:229], off
	s_addc_u32 s47, s9, s47
	v_cndmask_b32_e32 v228, v174, v192, vcc
	s_mov_b32 m0, s67
	v_cndmask_b32_e32 v229, v176, v193, vcc
	global_load_lds_dwordx4 v228, s[46:47]
	s_mov_b32 m0, s68
	s_nop 0
	global_load_lds_dwordx4 v229, s[46:47]
	s_waitcnt vmcnt(8)
	s_waitcnt lgkmcnt(0)
	s_barrier
	s_setprio 1
	s_waitcnt lgkmcnt(0)
	v_mfma_scale_f32_16x16x128_f8f6f4 v[86:89], v[16:23], v[196:203], v[86:89], v190, v190 op_sel_hi:[0,0,0]
	v_mfma_scale_f32_16x16x128_f8f6f4 v[78:81], v[24:31], v[196:203], v[78:81], v190, v190 op_sel_hi:[0,0,0]
	v_mfma_scale_f32_16x16x128_f8f6f4 v[74:77], v[16:23], v[204:211], v[74:77], v190, v190 op_sel_hi:[0,0,0]
	v_mfma_scale_f32_16x16x128_f8f6f4 v[66:69], v[24:31], v[204:211], v[66:69], v190, v190 op_sel_hi:[0,0,0]
	v_mfma_scale_f32_16x16x128_f8f6f4 v[58:61], v[16:23], v[212:219], v[58:61], v190, v190 op_sel_hi:[0,0,0]
	v_mfma_scale_f32_16x16x128_f8f6f4 v[50:53], v[24:31], v[212:219], v[50:53], v190, v190 op_sel_hi:[0,0,0]
	v_mfma_scale_f32_16x16x128_f8f6f4 v[42:45], v[16:23], v[220:227], v[42:45], v190, v190 op_sel_hi:[0,0,0]
	v_mfma_scale_f32_16x16x128_f8f6f4 v[34:37], v[24:31], v[220:227], v[34:37], v190, v190 op_sel_hi:[0,0,0]
	s_setprio 0
	s_setprio 1
	v_mfma_scale_f32_16x16x128_f8f6f4 v[94:97], v[8:15], v[196:203], v[94:97], v190, v190 op_sel_hi:[0,0,0]
	v_mfma_scale_f32_16x16x128_f8f6f4 v[90:93], v[0:7], v[196:203], v[90:93], v190, v190 op_sel_hi:[0,0,0]
	v_mfma_scale_f32_16x16x128_f8f6f4 v[82:85], v[8:15], v[204:211], v[82:85], v190, v190 op_sel_hi:[0,0,0]
	v_mfma_scale_f32_16x16x128_f8f6f4 v[70:73], v[0:7], v[204:211], v[70:73], v190, v190 op_sel_hi:[0,0,0]
	v_mfma_scale_f32_16x16x128_f8f6f4 v[62:65], v[8:15], v[212:219], v[62:65], v190, v190 op_sel_hi:[0,0,0]
	v_mfma_scale_f32_16x16x128_f8f6f4 v[54:57], v[0:7], v[212:219], v[54:57], v190, v190 op_sel_hi:[0,0,0]
	v_mfma_scale_f32_16x16x128_f8f6f4 v[46:49], v[8:15], v[220:227], v[46:49], v190, v190 op_sel_hi:[0,0,0]
	v_mfma_scale_f32_16x16x128_f8f6f4 v[38:41], v[0:7], v[220:227], v[38:41], v190, v190 op_sel_hi:[0,0,0]
	s_setprio 0
	s_barrier
	s_add_u32 s42, s42, 0x100
	s_addc_u32 s43, s43, 0
	s_add_i32 s31, s31, 2
	s_and_b64 vcc, exec, s[44:45]
	s_cbranch_vccz .LBB0_1295

.LBB0_1297:
	s_mul_hi_u32 s31, s35, 0xaaaaaaab
	s_lshr_b32 s31, s31, 1
	s_mul_i32 s31, s31, 3
	s_sub_i32 s31, s35, s31
	s_nop 15
	s_nop 7
	v_lshl_add_u32 v0, s31, 11, v188
	ds_read2_b32 v[12:13], v0 offset1:16
	ds_read2_b32 v[8:9], v0 offset0:32 offset1:48
	ds_read2_b32 v[6:7], v0 offset0:128 offset1:144
	ds_read2_b32 v[2:3], v0 offset0:160 offset1:176
	v_pk_mul_f32 v[14:15], v[160:161], v[156:157]
	s_waitcnt lgkmcnt(0)
	v_mul_f32_e32 v4, v12, v12
	v_mul_f32_e32 v12, 0xbfb8aa3b, v12
	v_pk_mul_f32 v[18:19], v[160:161], v[12:13] op_sel_hi:[1,0]
	v_pk_mul_f32 v[20:21], v[158:159], v[12:13] op_sel_hi:[1,0]
	v_exp_f32_e32 v18, v18
	v_exp_f32_e32 v20, v20
	v_exp_f32_e32 v21, v21
	v_exp_f32_e32 v19, v19
	v_mul_f32_e32 v4, 0x41000000, v4
	v_pk_mul_f32 v[16:17], v[158:159], v[154:155]
	v_pk_add_f32 v[20:21], v[20:21], 1.0 op_sel_hi:[1,0]
	v_pk_add_f32 v[18:19], v[18:19], 1.0 op_sel_hi:[1,0]
	v_rcp_f32_e32 v20, v20
	v_rcp_f32_e32 v21, v21
	v_rcp_f32_e32 v18, v18
	v_rcp_f32_e32 v19, v19
	v_pk_mul_f32 v[16:17], v[16:17], v[4:5] op_sel_hi:[1,0]
	v_pk_mul_f32 v[14:15], v[14:15], v[4:5] op_sel_hi:[1,0]
	v_pk_mul_f32 v[16:17], v[16:17], v[20:21]
	v_pk_mul_f32 v[14:15], v[14:15], v[18:19]
	v_pk_mul_f32 v[18:19], v[152:153], v[148:149]
	v_pk_mul_f32 v[20:21], v[150:151], v[146:147]
	v_pk_mul_f32 v[22:23], v[150:151], v[12:13] op_sel_hi:[1,0]
	v_pk_mul_f32 v[20:21], v[20:21], v[4:5] op_sel_hi:[1,0]
	v_pk_mul_f32 v[4:5], v[18:19], v[4:5] op_sel_hi:[1,0]
	v_pk_mul_f32 v[18:19], v[152:153], v[12:13] op_sel_hi:[1,0]
	v_exp_f32_e32 v22, v22
	v_exp_f32_e32 v23, v23
	v_exp_f32_e32 v18, v18
	v_exp_f32_e32 v19, v19
	v_med3_f32 v11, v16, s80, v191
	v_pk_add_f32 v[22:23], v[22:23], 1.0 op_sel_hi:[1,0]
	v_med3_f32 v12, v17, s80, v191
	v_pk_add_f32 v[18:19], v[18:19], 1.0 op_sel_hi:[1,0]
	v_rcp_f32_e32 v22, v22
	v_rcp_f32_e32 v23, v23
	v_rcp_f32_e32 v18, v18
	v_rcp_f32_e32 v19, v19
	v_med3_f32 v16, v14, s80, v191
	v_mov_b32_e32 v14, v33
	v_cvt_pk_fp8_f32 v14, v11, v12
	v_pk_mul_f32 v[4:5], v[4:5], v[18:19]
	v_pk_mul_f32 v[18:19], v[20:21], v[22:23]
	v_med3_f32 v15, v15, s80, v191
	v_cvt_pk_fp8_f32 v14, v16, v15 op_sel:[0,0,1]
	v_med3_f32 v11, v18, s80, v191
	v_med3_f32 v12, v19, s80, v191
	v_mov_b32_e32 v15, v33
	v_cvt_pk_fp8_f32 v15, v11, v12
	v_med3_f32 v4, v4, s80, v191
	v_med3_f32 v5, v5, s80, v191
	v_lshl_or_b32 v0, s38, 7, v187
	v_cvt_pk_fp8_f32 v15, v4, v5 op_sel:[0,0,1]
	v_lshl_add_u32 v10, s83, 8, v185
	v_mov_b64_e32 v[4:5], s[26:27]
	v_ashrrev_i32_e32 v1, 31, v0
	v_mad_i64_i32 v[16:17], s[34:35], v10, s81, v[4:5]
	v_lshl_add_u64 v[16:17], v[16:17], 0, v[0:1]
	global_store_dwordx2 v[16:17], v[14:15], off
	v_mul_f32_e32 v14, 0xbfb8aa3b, v13
	v_pk_mul_f32 v[20:21], v[144:145], v[14:15] op_sel_hi:[1,0]
	v_pk_mul_f32 v[22:23], v[142:143], v[14:15] op_sel_hi:[1,0]
	v_exp_f32_e32 v20, v20
	v_exp_f32_e32 v22, v22
	v_exp_f32_e32 v23, v23
	v_exp_f32_e32 v21, v21
	v_mul_f32_e32 v11, v13, v13
	v_mul_f32_e32 v12, 0x41000000, v11
	v_pk_add_f32 v[22:23], v[22:23], 1.0 op_sel_hi:[1,0]
	v_pk_add_f32 v[20:21], v[20:21], 1.0 op_sel_hi:[1,0]
	v_rcp_f32_e32 v22, v22
	v_rcp_f32_e32 v23, v23
	v_rcp_f32_e32 v20, v20
	v_rcp_f32_e32 v21, v21
	v_pk_mul_f32 v[16:17], v[144:145], v[140:141]
	v_pk_mul_f32 v[18:19], v[142:143], v[138:139]
	v_pk_mul_f32 v[16:17], v[16:17], v[12:13] op_sel_hi:[1,0]
	v_pk_mul_f32 v[18:19], v[18:19], v[12:13] op_sel_hi:[1,0]
	v_pk_mul_f32 v[16:17], v[16:17], v[20:21]
	v_pk_mul_f32 v[18:19], v[18:19], v[22:23]
	v_pk_mul_f32 v[20:21], v[136:137], v[132:133]
	v_pk_mul_f32 v[22:23], v[134:135], v[130:131]
	v_med3_f32 v18, v18, s80, v191
	v_pk_mul_f32 v[22:23], v[22:23], v[12:13] op_sel_hi:[1,0]
	v_pk_mul_f32 v[12:13], v[20:21], v[12:13] op_sel_hi:[1,0]
	v_pk_mul_f32 v[20:21], v[136:137], v[14:15] op_sel_hi:[1,0]
	v_pk_mul_f32 v[14:15], v[134:135], v[14:15] op_sel_hi:[1,0]
	v_exp_f32_e32 v20, v20
	v_exp_f32_e32 v21, v21
	v_exp_f32_e32 v14, v14
	v_exp_f32_e32 v15, v15
	v_med3_f32 v19, v19, s80, v191
	v_pk_add_f32 v[20:21], v[20:21], 1.0 op_sel_hi:[1,0]
	v_med3_f32 v17, v17, s80, v191
	v_rcp_f32_e32 v20, v20
	v_rcp_f32_e32 v21, v21
	v_pk_add_f32 v[14:15], v[14:15], 1.0 op_sel_hi:[1,0]
	v_or_b32_e32 v11, 16, v10
	v_rcp_f32_e32 v14, v14
	v_rcp_f32_e32 v15, v15
	v_pk_mul_f32 v[12:13], v[12:13], v[20:21]
	v_med3_f32 v20, v16, s80, v191
	v_mov_b32_e32 v16, v33
	v_cvt_pk_fp8_f32 v16, v18, v19
	v_pk_mul_f32 v[14:15], v[22:23], v[14:15]
	v_med3_f32 v12, v12, s80, v191
	v_med3_f32 v14, v14, s80, v191
	v_cvt_pk_fp8_f32 v16, v20, v17 op_sel:[0,0,1]
	v_med3_f32 v15, v15, s80, v191
	v_mov_b32_e32 v17, v33
	v_cvt_pk_fp8_f32 v17, v14, v15
	v_med3_f32 v13, v13, s80, v191
	v_pk_mul_f32 v[14:15], v[128:129], v[124:125]
	s_and_b64 vcc, exec, s[36:37]
	v_cvt_pk_fp8_f32 v17, v12, v13 op_sel:[0,0,1]
	v_mad_i64_i32 v[12:13], s[34:35], v11, s81, v[4:5]
	v_mul_f32_e32 v11, v8, v8
	v_mul_f32_e32 v8, 0xbfb8aa3b, v8
	v_pk_mul_f32 v[18:19], v[128:129], v[8:9] op_sel_hi:[1,0]
	v_pk_mul_f32 v[20:21], v[126:127], v[8:9] op_sel_hi:[1,0]
	v_exp_f32_e32 v18, v18
	v_exp_f32_e32 v20, v20
	v_exp_f32_e32 v21, v21
	v_exp_f32_e32 v19, v19
	v_lshl_add_u64 v[12:13], v[12:13], 0, v[0:1]
	global_store_dwordx2 v[12:13], v[16:17], off
	v_pk_add_f32 v[20:21], v[20:21], 1.0 op_sel_hi:[1,0]
	v_pk_add_f32 v[18:19], v[18:19], 1.0 op_sel_hi:[1,0]
	v_rcp_f32_e32 v20, v20
	v_rcp_f32_e32 v21, v21
	v_rcp_f32_e32 v18, v18
	v_rcp_f32_e32 v19, v19
	v_mul_f32_e32 v12, 0x41000000, v11
	v_pk_mul_f32 v[16:17], v[126:127], v[122:123]
	v_pk_mul_f32 v[14:15], v[14:15], v[12:13] op_sel_hi:[1,0]
	v_pk_mul_f32 v[16:17], v[16:17], v[12:13] op_sel_hi:[1,0]
	v_pk_mul_f32 v[14:15], v[14:15], v[18:19]
	v_pk_mul_f32 v[16:17], v[16:17], v[20:21]
	v_pk_mul_f32 v[18:19], v[120:121], v[116:117]
	v_pk_mul_f32 v[20:21], v[118:119], v[114:115]
	v_pk_mul_f32 v[22:23], v[118:119], v[8:9] op_sel_hi:[1,0]
	v_pk_mul_f32 v[20:21], v[20:21], v[12:13] op_sel_hi:[1,0]
	v_pk_mul_f32 v[12:13], v[18:19], v[12:13] op_sel_hi:[1,0]
	v_pk_mul_f32 v[18:19], v[120:121], v[8:9] op_sel_hi:[1,0]
	v_exp_f32_e32 v22, v22
	v_exp_f32_e32 v23, v23
	v_exp_f32_e32 v18, v18
	v_exp_f32_e32 v19, v19
	v_med3_f32 v11, v16, s80, v191
	v_pk_add_f32 v[22:23], v[22:23], 1.0 op_sel_hi:[1,0]
	v_med3_f32 v16, v17, s80, v191
	v_pk_add_f32 v[18:19], v[18:19], 1.0 op_sel_hi:[1,0]
	v_rcp_f32_e32 v22, v22
	v_rcp_f32_e32 v23, v23
	v_rcp_f32_e32 v18, v18
	v_rcp_f32_e32 v19, v19
	v_med3_f32 v17, v14, s80, v191
	v_mov_b32_e32 v14, v33
	v_cvt_pk_fp8_f32 v14, v11, v16
	v_pk_mul_f32 v[12:13], v[12:13], v[18:19]
	v_pk_mul_f32 v[18:19], v[20:21], v[22:23]
	v_med3_f32 v15, v15, s80, v191
	v_cvt_pk_fp8_f32 v14, v17, v15 op_sel:[0,0,1]
	v_med3_f32 v11, v18, s80, v191
	v_med3_f32 v16, v19, s80, v191
	v_mov_b32_e32 v15, v33
	v_cvt_pk_fp8_f32 v15, v11, v16
	v_med3_f32 v12, v12, s80, v191
	v_med3_f32 v13, v13, s80, v191
	v_or_b32_e32 v8, 32, v10
	v_cvt_pk_fp8_f32 v15, v12, v13 op_sel:[0,0,1]
	v_mad_i64_i32 v[12:13], s[34:35], v8, s81, v[4:5]
	v_lshl_add_u64 v[12:13], v[12:13], 0, v[0:1]
	global_store_dwordx2 v[12:13], v[14:15], off
	v_mul_f32_e32 v12, 0xbfb8aa3b, v9
	v_pk_mul_f32 v[18:19], v[112:113], v[12:13] op_sel_hi:[1,0]
	v_pk_mul_f32 v[20:21], v[110:111], v[12:13] op_sel_hi:[1,0]
	v_exp_f32_e32 v18, v18
	v_exp_f32_e32 v20, v20
	v_exp_f32_e32 v21, v21
	v_exp_f32_e32 v19, v19
	v_mul_f32_e32 v8, v9, v9
	v_mul_f32_e32 v8, 0x41000000, v8
	v_pk_add_f32 v[20:21], v[20:21], 1.0 op_sel_hi:[1,0]
	v_pk_add_f32 v[18:19], v[18:19], 1.0 op_sel_hi:[1,0]
	v_rcp_f32_e32 v20, v20
	v_rcp_f32_e32 v21, v21
	v_rcp_f32_e32 v18, v18
	v_rcp_f32_e32 v19, v19
	v_pk_mul_f32 v[14:15], v[112:113], v[108:109]
	v_pk_mul_f32 v[16:17], v[110:111], v[106:107]
	v_pk_mul_f32 v[14:15], v[14:15], v[8:9] op_sel_hi:[1,0]
	v_pk_mul_f32 v[16:17], v[16:17], v[8:9] op_sel_hi:[1,0]
	v_pk_mul_f32 v[14:15], v[14:15], v[18:19]
	v_pk_mul_f32 v[16:17], v[16:17], v[20:21]
	v_pk_mul_f32 v[18:19], v[104:105], v[100:101]
	v_pk_mul_f32 v[20:21], v[102:103], v[98:99]
	v_med3_f32 v16, v16, s80, v191
	v_pk_mul_f32 v[20:21], v[20:21], v[8:9] op_sel_hi:[1,0]
	v_pk_mul_f32 v[8:9], v[18:19], v[8:9] op_sel_hi:[1,0]
	v_pk_mul_f32 v[18:19], v[104:105], v[12:13] op_sel_hi:[1,0]
	v_pk_mul_f32 v[12:13], v[102:103], v[12:13] op_sel_hi:[1,0]
	v_exp_f32_e32 v18, v18
	v_exp_f32_e32 v19, v19
	v_exp_f32_e32 v12, v12
	v_exp_f32_e32 v13, v13
	v_med3_f32 v17, v17, s80, v191
	v_pk_add_f32 v[18:19], v[18:19], 1.0 op_sel_hi:[1,0]
	v_med3_f32 v15, v15, s80, v191
	v_rcp_f32_e32 v18, v18
	v_rcp_f32_e32 v19, v19
	v_pk_add_f32 v[12:13], v[12:13], 1.0 op_sel_hi:[1,0]
	v_or_b32_e32 v11, 48, v10
	v_rcp_f32_e32 v12, v12
	v_rcp_f32_e32 v13, v13
	v_pk_mul_f32 v[8:9], v[8:9], v[18:19]
	v_med3_f32 v18, v14, s80, v191
	v_mov_b32_e32 v14, v33
	v_cvt_pk_fp8_f32 v14, v16, v17
	v_pk_mul_f32 v[12:13], v[20:21], v[12:13]
	v_med3_f32 v8, v8, s80, v191
	v_med3_f32 v12, v12, s80, v191
	v_cvt_pk_fp8_f32 v14, v18, v15 op_sel:[0,0,1]
	v_med3_f32 v13, v13, s80, v191
	v_mov_b32_e32 v15, v33
	v_cvt_pk_fp8_f32 v15, v12, v13
	v_med3_f32 v9, v9, s80, v191
	v_pk_mul_f32 v[12:13], v[88:89], v[96:97]
	v_cvt_pk_fp8_f32 v15, v8, v9 op_sel:[0,0,1]
	v_mad_i64_i32 v[8:9], s[34:35], v11, s81, v[4:5]
	v_lshl_add_u64 v[8:9], v[8:9], 0, v[0:1]
	global_store_dwordx2 v[8:9], v[14:15], off
	v_mul_f32_e32 v8, v6, v6
	v_mul_f32_e32 v6, 0xbfb8aa3b, v6
	v_pk_mul_f32 v[16:17], v[88:89], v[6:7] op_sel_hi:[1,0]
	v_pk_mul_f32 v[18:19], v[86:87], v[6:7] op_sel_hi:[1,0]
	v_exp_f32_e32 v16, v16
	v_exp_f32_e32 v18, v18
	v_exp_f32_e32 v19, v19
	v_exp_f32_e32 v17, v17
	v_mul_f32_e32 v8, 0x41000000, v8
	v_pk_mul_f32 v[14:15], v[86:87], v[94:95]
	v_pk_add_f32 v[18:19], v[18:19], 1.0 op_sel_hi:[1,0]
	v_pk_add_f32 v[16:17], v[16:17], 1.0 op_sel_hi:[1,0]
	v_rcp_f32_e32 v18, v18
	v_rcp_f32_e32 v19, v19
	v_rcp_f32_e32 v16, v16
	v_rcp_f32_e32 v17, v17
	v_pk_mul_f32 v[14:15], v[14:15], v[8:9] op_sel_hi:[1,0]
	v_pk_mul_f32 v[12:13], v[12:13], v[8:9] op_sel_hi:[1,0]
	v_pk_mul_f32 v[14:15], v[14:15], v[18:19]
	v_pk_mul_f32 v[12:13], v[12:13], v[16:17]
	v_pk_mul_f32 v[16:17], v[80:81], v[92:93]
	v_pk_mul_f32 v[18:19], v[78:79], v[90:91]
	v_pk_mul_f32 v[20:21], v[78:79], v[6:7] op_sel_hi:[1,0]
	v_pk_mul_f32 v[18:19], v[18:19], v[8:9] op_sel_hi:[1,0]
	v_pk_mul_f32 v[8:9], v[16:17], v[8:9] op_sel_hi:[1,0]
	v_pk_mul_f32 v[16:17], v[80:81], v[6:7] op_sel_hi:[1,0]
	v_exp_f32_e32 v20, v20
	v_exp_f32_e32 v21, v21
	v_exp_f32_e32 v16, v16
	v_exp_f32_e32 v17, v17
	v_med3_f32 v6, v14, s80, v191
	v_pk_add_f32 v[20:21], v[20:21], 1.0 op_sel_hi:[1,0]
	v_med3_f32 v14, v15, s80, v191
	v_pk_add_f32 v[16:17], v[16:17], 1.0 op_sel_hi:[1,0]
	v_rcp_f32_e32 v20, v20
	v_rcp_f32_e32 v21, v21
	v_rcp_f32_e32 v16, v16
	v_rcp_f32_e32 v17, v17
	v_med3_f32 v15, v12, s80, v191
	v_mov_b32_e32 v12, v33
	v_cvt_pk_fp8_f32 v12, v6, v14
	v_pk_mul_f32 v[8:9], v[8:9], v[16:17]
	v_pk_mul_f32 v[16:17], v[18:19], v[20:21]
	v_med3_f32 v13, v13, s80, v191
	v_cvt_pk_fp8_f32 v12, v15, v13 op_sel:[0,0,1]
	v_med3_f32 v6, v16, s80, v191
	v_med3_f32 v14, v17, s80, v191
	v_mov_b32_e32 v13, v33
	v_cvt_pk_fp8_f32 v13, v6, v14
	v_med3_f32 v8, v8, s80, v191
	v_med3_f32 v9, v9, s80, v191
	v_add_u32_e32 v11, 0x80, v10
	v_cvt_pk_fp8_f32 v13, v8, v9 op_sel:[0,0,1]
	v_mad_i64_i32 v[8:9], s[34:35], v11, s81, v[4:5]
	v_lshl_add_u64 v[8:9], v[8:9], 0, v[0:1]
	global_store_dwordx2 v[8:9], v[12:13], off
	v_mul_f32_e32 v8, 0xbfb8aa3b, v7
	v_pk_mul_f32 v[16:17], v[76:77], v[8:9] op_sel_hi:[1,0]
	v_pk_mul_f32 v[18:19], v[74:75], v[8:9] op_sel_hi:[1,0]
	v_exp_f32_e32 v16, v16
	v_exp_f32_e32 v18, v18
	v_exp_f32_e32 v19, v19
	v_exp_f32_e32 v17, v17
	v_mul_f32_e32 v6, v7, v7
	v_mul_f32_e32 v6, 0x41000000, v6
	v_pk_add_f32 v[18:19], v[18:19], 1.0 op_sel_hi:[1,0]
	v_pk_add_f32 v[16:17], v[16:17], 1.0 op_sel_hi:[1,0]
	v_rcp_f32_e32 v18, v18
	v_rcp_f32_e32 v19, v19
	v_rcp_f32_e32 v16, v16
	v_rcp_f32_e32 v17, v17
	v_pk_mul_f32 v[12:13], v[76:77], v[84:85]
	v_pk_mul_f32 v[14:15], v[74:75], v[82:83]
	v_pk_mul_f32 v[12:13], v[12:13], v[6:7] op_sel_hi:[1,0]
	v_pk_mul_f32 v[14:15], v[14:15], v[6:7] op_sel_hi:[1,0]
	v_pk_mul_f32 v[12:13], v[12:13], v[16:17]
	v_pk_mul_f32 v[14:15], v[14:15], v[18:19]
	v_pk_mul_f32 v[16:17], v[68:69], v[72:73]
	v_pk_mul_f32 v[18:19], v[66:67], v[70:71]
	v_med3_f32 v14, v14, s80, v191
	v_pk_mul_f32 v[18:19], v[18:19], v[6:7] op_sel_hi:[1,0]
	v_pk_mul_f32 v[6:7], v[16:17], v[6:7] op_sel_hi:[1,0]
	v_pk_mul_f32 v[16:17], v[68:69], v[8:9] op_sel_hi:[1,0]
	v_pk_mul_f32 v[8:9], v[66:67], v[8:9] op_sel_hi:[1,0]
	v_exp_f32_e32 v16, v16
	v_exp_f32_e32 v17, v17
	v_exp_f32_e32 v8, v8
	v_exp_f32_e32 v9, v9
	v_med3_f32 v15, v15, s80, v191
	v_pk_add_f32 v[16:17], v[16:17], 1.0 op_sel_hi:[1,0]
	v_med3_f32 v13, v13, s80, v191
	v_rcp_f32_e32 v16, v16
	v_rcp_f32_e32 v17, v17
	v_pk_add_f32 v[8:9], v[8:9], 1.0 op_sel_hi:[1,0]
	v_add_u32_e32 v11, 0x90, v10
	v_rcp_f32_e32 v8, v8
	v_rcp_f32_e32 v9, v9
	v_pk_mul_f32 v[6:7], v[6:7], v[16:17]
	v_med3_f32 v16, v12, s80, v191
	v_mov_b32_e32 v12, v33
	v_cvt_pk_fp8_f32 v12, v14, v15
	v_pk_mul_f32 v[8:9], v[18:19], v[8:9]
	v_med3_f32 v6, v6, s80, v191
	v_med3_f32 v8, v8, s80, v191
	v_cvt_pk_fp8_f32 v12, v16, v13 op_sel:[0,0,1]
	v_med3_f32 v9, v9, s80, v191
	v_mov_b32_e32 v13, v33
	v_cvt_pk_fp8_f32 v13, v8, v9
	v_med3_f32 v7, v7, s80, v191
	v_pk_mul_f32 v[8:9], v[60:61], v[64:65]
	v_cvt_pk_fp8_f32 v13, v6, v7 op_sel:[0,0,1]
	v_mad_i64_i32 v[6:7], s[34:35], v11, s81, v[4:5]
	v_lshl_add_u64 v[6:7], v[6:7], 0, v[0:1]
	global_store_dwordx2 v[6:7], v[12:13], off
	v_mul_f32_e32 v6, v2, v2
	v_mul_f32_e32 v2, 0xbfb8aa3b, v2
	v_pk_mul_f32 v[14:15], v[60:61], v[2:3] op_sel_hi:[1,0]
	v_pk_mul_f32 v[16:17], v[58:59], v[2:3] op_sel_hi:[1,0]
	v_exp_f32_e32 v14, v14
	v_exp_f32_e32 v16, v16
	v_exp_f32_e32 v17, v17
	v_exp_f32_e32 v15, v15
	v_mul_f32_e32 v6, 0x41000000, v6
	v_pk_mul_f32 v[12:13], v[58:59], v[62:63]
	v_pk_add_f32 v[16:17], v[16:17], 1.0 op_sel_hi:[1,0]
	v_pk_add_f32 v[14:15], v[14:15], 1.0 op_sel_hi:[1,0]
	v_rcp_f32_e32 v16, v16
	v_rcp_f32_e32 v17, v17
	v_rcp_f32_e32 v14, v14
	v_rcp_f32_e32 v15, v15
	v_pk_mul_f32 v[12:13], v[12:13], v[6:7] op_sel_hi:[1,0]
	v_pk_mul_f32 v[8:9], v[8:9], v[6:7] op_sel_hi:[1,0]
	v_pk_mul_f32 v[12:13], v[12:13], v[16:17]
	v_pk_mul_f32 v[8:9], v[8:9], v[14:15]
	v_pk_mul_f32 v[14:15], v[52:53], v[56:57]
	v_pk_mul_f32 v[16:17], v[50:51], v[54:55]
	v_pk_mul_f32 v[18:19], v[50:51], v[2:3] op_sel_hi:[1,0]
	v_pk_mul_f32 v[16:17], v[16:17], v[6:7] op_sel_hi:[1,0]
	v_pk_mul_f32 v[6:7], v[14:15], v[6:7] op_sel_hi:[1,0]
	v_pk_mul_f32 v[14:15], v[52:53], v[2:3] op_sel_hi:[1,0]
	v_exp_f32_e32 v18, v18
	v_exp_f32_e32 v19, v19
	v_exp_f32_e32 v14, v14
	v_exp_f32_e32 v15, v15
	v_med3_f32 v11, v12, s80, v191
	v_pk_add_f32 v[18:19], v[18:19], 1.0 op_sel_hi:[1,0]
	v_med3_f32 v12, v13, s80, v191
	v_pk_add_f32 v[14:15], v[14:15], 1.0 op_sel_hi:[1,0]
	v_rcp_f32_e32 v18, v18
	v_rcp_f32_e32 v19, v19
	v_rcp_f32_e32 v14, v14
	v_rcp_f32_e32 v15, v15
	v_med3_f32 v13, v8, s80, v191
	v_mov_b32_e32 v8, v33
	v_cvt_pk_fp8_f32 v8, v11, v12
	v_pk_mul_f32 v[6:7], v[6:7], v[14:15]
	v_pk_mul_f32 v[14:15], v[16:17], v[18:19]
	v_med3_f32 v9, v9, s80, v191
	v_cvt_pk_fp8_f32 v8, v13, v9 op_sel:[0,0,1]
	v_med3_f32 v11, v14, s80, v191
	v_med3_f32 v12, v15, s80, v191
	v_mov_b32_e32 v9, v33
	v_cvt_pk_fp8_f32 v9, v11, v12
	v_med3_f32 v6, v6, s80, v191
	v_med3_f32 v7, v7, s80, v191
	v_add_u32_e32 v2, 0xa0, v10
	v_cvt_pk_fp8_f32 v9, v6, v7 op_sel:[0,0,1]
	v_mad_i64_i32 v[6:7], s[34:35], v2, s81, v[4:5]
	v_lshl_add_u64 v[6:7], v[6:7], 0, v[0:1]
	global_store_dwordx2 v[6:7], v[8:9], off
	v_mul_f32_e32 v6, 0xbfb8aa3b, v3
	v_pk_mul_f32 v[14:15], v[44:45], v[6:7] op_sel_hi:[1,0]
	v_pk_mul_f32 v[16:17], v[42:43], v[6:7] op_sel_hi:[1,0]
	v_exp_f32_e32 v14, v14
	v_exp_f32_e32 v16, v16
	v_exp_f32_e32 v17, v17
	v_exp_f32_e32 v15, v15
	v_mul_f32_e32 v2, v3, v3
	v_mul_f32_e32 v2, 0x41000000, v2
	v_pk_add_f32 v[16:17], v[16:17], 1.0 op_sel_hi:[1,0]
	v_pk_add_f32 v[14:15], v[14:15], 1.0 op_sel_hi:[1,0]
	v_rcp_f32_e32 v16, v16
	v_rcp_f32_e32 v17, v17
	v_rcp_f32_e32 v14, v14
	v_rcp_f32_e32 v15, v15
	v_pk_mul_f32 v[8:9], v[44:45], v[48:49]
	v_pk_mul_f32 v[12:13], v[42:43], v[46:47]
	v_pk_mul_f32 v[8:9], v[8:9], v[2:3] op_sel_hi:[1,0]
	v_pk_mul_f32 v[12:13], v[12:13], v[2:3] op_sel_hi:[1,0]
	v_pk_mul_f32 v[8:9], v[8:9], v[14:15]
	v_pk_mul_f32 v[12:13], v[12:13], v[16:17]
	v_pk_mul_f32 v[14:15], v[36:37], v[40:41]
	v_pk_mul_f32 v[16:17], v[34:35], v[38:39]
	v_med3_f32 v11, v12, s80, v191
	v_pk_mul_f32 v[16:17], v[16:17], v[2:3] op_sel_hi:[1,0]
	v_pk_mul_f32 v[2:3], v[14:15], v[2:3] op_sel_hi:[1,0]
	v_pk_mul_f32 v[14:15], v[36:37], v[6:7] op_sel_hi:[1,0]
	v_pk_mul_f32 v[6:7], v[34:35], v[6:7] op_sel_hi:[1,0]
	v_exp_f32_e32 v14, v14
	v_exp_f32_e32 v6, v6
	v_exp_f32_e32 v7, v7
	v_exp_f32_e32 v15, v15
	v_med3_f32 v12, v13, s80, v191
	v_med3_f32 v13, v8, s80, v191
	v_pk_add_f32 v[6:7], v[6:7], 1.0 op_sel_hi:[1,0]
	v_mov_b32_e32 v8, v33
	v_rcp_f32_e32 v6, v6
	v_rcp_f32_e32 v7, v7
	v_cvt_pk_fp8_f32 v8, v11, v12
	v_pk_add_f32 v[14:15], v[14:15], 1.0 op_sel_hi:[1,0]
	v_med3_f32 v9, v9, s80, v191
	v_rcp_f32_e32 v14, v14
	v_rcp_f32_e32 v15, v15
	v_pk_mul_f32 v[6:7], v[16:17], v[6:7]
	v_cvt_pk_fp8_f32 v8, v13, v9 op_sel:[0,0,1]
	v_med3_f32 v6, v6, s80, v191
	v_med3_f32 v7, v7, s80, v191
	v_mov_b32_e32 v9, v33
	v_cvt_pk_fp8_f32 v9, v6, v7
	v_pk_mul_f32 v[2:3], v[2:3], v[14:15]
	v_add_u32_e32 v10, 0xb0, v10
	v_med3_f32 v2, v2, s80, v191
	v_med3_f32 v3, v3, s80, v191
	v_cvt_pk_fp8_f32 v9, v2, v3 op_sel:[0,0,1]
	v_mad_i64_i32 v[2:3], s[34:35], v10, s81, v[4:5]
	v_lshl_add_u64 v[0:1], v[2:3], 0, v[0:1]
	s_mov_b64 s[34:35], -1
	global_store_dwordx2 v[0:1], v[8:9], off
	s_cbranch_vccz .LBB0_1282
	s_andn2_b64 vcc, exec, s[24:25]
	s_cbranch_vccnz .LBB0_1281
	s_barrier
	s_branch .LBB0_1281
